# all three GEMMs hand-written B-stationary (AGPR) design; weights stored MFMA-fragment-major by prep_k and agg side role so each B load is one contiguous 1KB; f16 MFMA f32 accumulate unchanged
# speedup vs baseline: 1.0750x; 1.0750x over previous
.LBB0_3:
	s_andn2_b64 vcc, exec, s[4:5]
	s_cbranch_vccnz .LBB0_5
	s_load_dwordx4 s[4:7], s[0:1], 0x10
	s_load_dwordx2 s[2:3], s[0:1], 0x30
	s_add_i32 s12, s14, 0xffffff60
	s_lshr_b32 s13, s12, 6
	s_lshl_b32 s8, s13, 18
	s_mov_b32 s9, 0
	s_lshl_b64 s[10:11], s[8:9], 2
	s_waitcnt lgkmcnt(0)
	s_add_u32 s6, s6, s10
	s_addc_u32 s7, s7, s11
	s_cmpk_lt_u32 s12, 0x100
	s_cselect_b32 s5, s7, s5
	s_cselect_b32 s4, s6, s4
	s_bfe_u32 s6, s12, 0x30003
	s_lshl_b32 s8, s14, 6
	s_lshl_b32 s7, s6, 15
	s_and_b32 s8, s8, 0x1c0
	v_and_b32_e32 v1, 63, v0
	s_or_b32 s7, s7, s8
	v_or_b32_e32 v3, s7, v1
	v_lshrrev_b32_e32 v2, 6, v0
	v_lshlrev_b32_e32 v3, 2, v3
	v_lshl_or_b32 v4, v2, 11, v3
	v_or_b32_e32 v5, 16, v2
	v_or_b32_e32 v7, 32, v2
	v_or_b32_e32 v9, 48, v2
	v_lshl_or_b32 v6, v5, 11, v3
	v_lshl_or_b32 v8, v7, 11, v3
	v_lshl_or_b32 v3, v9, 11, v3
	global_load_dword v10, v4, s[4:5] nt
	global_load_dword v11, v6, s[4:5] nt
	global_load_dword v12, v8, s[4:5] nt
	global_load_dword v13, v3, s[4:5] nt
	v_lshlrev_b32_e32 v3, 2, v1
	s_movk_i32 s4, 0x104
	v_lshlrev_b32_e32 v4, 1, v1
	v_lshl_or_b32 v1, v1, 8, v3
	v_mad_u32_u24 v8, v2, s4, v3
	v_lshl_add_u32 v1, v2, 2, v1
	s_lshl_b32 s4, s13, 3
	s_and_b32 s5, s14, 7
	s_add_i32 s4, s4, s5
	s_lshl_b32 s4, s4, 16
	s_lshl_b32 s5, s6, 13
	s_add_i32 s4, s4, s5
	s_add_u32 s2, s2, s4
	s_addc_u32 s3, s3, 0
	v_and_b32_e32 v6, 63, v0
	v_lshrrev_b32_e32 v7, 5, v6
	v_lshlrev_b32_e32 v7, 12, v7
	v_bfe_u32 v9, v6, 3, 2
	v_lshl_or_b32 v7, v9, 8, v7
	v_and_b32_e32 v9, 7, v6
	v_lshl_or_b32 v7, v9, 1, v7
	v_lshrrev_b32_e32 v9, 6, v0
	v_bfe_u32 v14, v9, 2, 2
	v_lshl_or_b32 v7, v14, 10, v7
	v_and_b32_e32 v9, 3, v9
	v_lshl_or_b32 v6, v9, 4, v7
	s_waitcnt vmcnt(3)
	ds_write_b32 v8, v10
	s_waitcnt vmcnt(2)
	ds_write_b32 v8, v11 offset:4160
	s_waitcnt vmcnt(1)
	ds_write_b32 v8, v12 offset:8320
	s_waitcnt vmcnt(0)
	ds_write_b32 v8, v13 offset:12480
	s_waitcnt lgkmcnt(0)
	s_barrier
	ds_read2_b32 v[2:3], v1 offset1:16
	ds_read2_b32 v[4:5], v1 offset0:32 offset1:48
	s_waitcnt lgkmcnt(1)
	v_cvt_f16_f32_e32 v1, v2
	v_cvt_f16_f32_e32 v2, v3
	s_waitcnt lgkmcnt(0)
	v_cvt_f16_f32_e32 v3, v4
	v_cvt_f16_f32_e32 v4, v5
	global_store_short v6, v1, s[2:3]
	global_store_short v6, v2, s[2:3] offset:64
	global_store_short v6, v3, s[2:3] offset:128
	global_store_short v6, v4, s[2:3] offset:192

_Z7agg_ln1PKDF16_S0_S0_PKiS2_S2_PKfS4_S4_PDF16_S4_S4_S5_S5_:
	s_cmpk_gt_u32 s2, 0xff
	s_mov_b64 s[4:5], -1
	s_cbranch_scc0 .LBB1_28
	v_lshl_or_b32 v1, s2, 8, v0
	v_add_u32_e32 v1, 0xffff0000, v1
	s_mov_b32 s3, 0x9c400
	v_cmp_gt_u32_e32 vcc, s3, v1
	s_and_saveexec_b64 s[18:19], vcc
	s_cbranch_execz .LBB1_27
	s_load_dwordx2 s[4:5], s[0:1], 0x20
	s_load_dwordx2 s[6:7], s[0:1], 0x18
	v_lshrrev_b32_e32 v1, 6, v1
	v_lshlrev_b32_e32 v2, 4, v1
	v_and_b32_e32 v24, 63, v0
	v_lshlrev_b32_e32 v8, 3, v24
	s_waitcnt lgkmcnt(0)
	global_load_dwordx4 v[28:31], v2, s[6:7]
	global_load_dwordx4 v[2:5], v2, s[4:5]
	s_waitcnt vmcnt(0)
	v_add_u32_e32 v26, v3, v2
	v_add_u32_e32 v3, v26, v4
	v_add_u32_e32 v25, v3, v5
	v_cmp_gt_i32_e32 vcc, 1, v25
	s_and_saveexec_b64 s[4:5], vcc
	s_xor_b64 s[4:5], exec, s[4:5]
	v_mov_b32_e32 v9, 0
	s_or_saveexec_b64 s[22:23], s[4:5]
	s_load_dwordx2 s[20:21], s[0:1], 0x48
	v_mov_b32_e32 v11, 0
	v_mov_b64_e32 v[18:19], 0
	v_mov_b32_e32 v10, v11
	v_mov_b32_e32 v13, v11
	v_mov_b32_e32 v12, v11
	v_mov_b32_e32 v15, v11
	v_mov_b32_e32 v14, v11
	v_mov_b32_e32 v17, v11
	v_mov_b32_e32 v16, v11
	s_xor_b64 exec, exec, s[22:23]
	s_cbranch_execz .LBB1_26
	s_load_dwordx2 s[24:25], s[0:1], 0x28
	s_load_dwordx2 s[26:27], s[0:1], 0x0
	v_mov_b32_e32 v4, v28
	v_sub_u32_e32 v28, v29, v2
	v_sub_u32_e32 v27, v30, v26
	v_sub_u32_e32 v5, v31, v3
	s_waitcnt lgkmcnt(0)
	v_mov_b32_e32 v9, 0
	v_lshrrev_b32_e32 v10, 1, v0
	s_mov_b32 s3, 0
	s_mov_b64 s[28:29], 0
	v_mov_b64_e32 v[18:19], 0
	v_and_b32_e32 v20, 28, v10
	v_mov_b32_e32 v21, v9
	v_mov_b32_e32 v16, v9
	v_mov_b32_e32 v17, v9
	v_mov_b32_e32 v14, v9
	v_mov_b32_e32 v15, v9
	v_mov_b32_e32 v12, v9
	v_mov_b32_e32 v13, v9
	v_mov_b32_e32 v10, v9
	v_mov_b32_e32 v11, v9
	s_branch .LBB1_7

.LBB1_33:
	global_load_dword v6, v[0:1], off nt
	v_add_u32_e32 v4, 4, v4
	v_cmp_lt_u32_e32 vcc, 59, v4
	v_lshl_add_u64 v[0:1], v[0:1], 0, s[0:1]
	s_or_b64 s[2:3], vcc, s[2:3]
	s_waitcnt vmcnt(0)
	ds_write_b32 v5, v6
	v_add_u32_e32 v5, 0x410, v5
	s_andn2_b64 exec, exec, s[2:3]
	s_cbranch_execnz .LBB1_33
	s_or_b64 exec, exec, s[2:3]
	v_lshlrev_b32_e32 v0, 8, v2
	v_lshl_or_b32 v0, v2, 2, v0
	v_lshl_add_u32 v4, v3, 2, v0
	s_waitcnt lgkmcnt(0)
	s_barrier
	ds_read2_b32 v[6:7], v4 offset1:4
	ds_read2_b32 v[8:9], v4 offset0:8 offset1:12
	ds_read2_b32 v[10:11], v4 offset0:16 offset1:20
	ds_read2_b32 v[12:13], v4 offset0:24 offset1:28
	ds_read2_b32 v[14:15], v4 offset0:32 offset1:36
	ds_read2_b32 v[16:17], v4 offset0:40 offset1:44
	ds_read2_b32 v[18:19], v4 offset0:48 offset1:52
	ds_read2_b32 v[20:21], v4 offset0:56 offset1:60
	v_bfe_u32 v0, v2, 3, 2
	v_lshlrev_b32_e32 v0, 8, v0
	v_and_b32_e32 v1, 7, v2
	v_lshl_or_b32 v0, v1, 1, v0
	v_lshl_or_b32 v0, v3, 4, v0
	v_lshrrev_b32_e32 v1, 5, v2
	s_waitcnt lgkmcnt(0)
	v_cvt_f16_f32_e32 v6, v6
	v_cvt_f16_f32_e32 v7, v7
	v_cvt_f16_f32_e32 v8, v8
	v_cvt_f16_f32_e32 v9, v9
	v_cvt_f16_f32_e32 v10, v10
	v_cvt_f16_f32_e32 v11, v11
	v_cvt_f16_f32_e32 v12, v12
	v_cvt_f16_f32_e32 v13, v13
	v_cvt_f16_f32_e32 v14, v14
	v_cvt_f16_f32_e32 v15, v15
	v_cvt_f16_f32_e32 v16, v16
	v_cvt_f16_f32_e32 v17, v17
	v_cvt_f16_f32_e32 v18, v18
	v_cvt_f16_f32_e32 v19, v19
	v_cvt_f16_f32_e32 v20, v20
	v_cvt_f16_f32_e32 v21, v21
	s_cmpk_eq_u32 s8, 0x200
	s_cbranch_scc1 .Lagg_w2t
	v_lshl_or_b32 v0, v1, 12, v0
	s_lshl_b32 s0, s10, 16
	s_lshl_b32 s1, s9, 13
	s_add_i32 s0, s0, s1
	s_add_u32 s4, s4, s0
	s_addc_u32 s5, s5, 0
	global_store_short v0, v6, s[4:5]
	global_store_short v0, v7, s[4:5] offset:1024
	global_store_short v0, v8, s[4:5] offset:2048
	global_store_short v0, v9, s[4:5] offset:3072
	global_store_short v0, v10, s[4:5] offset:64
	global_store_short v0, v11, s[4:5] offset:1088
	global_store_short v0, v12, s[4:5] offset:2112
	global_store_short v0, v13, s[4:5] offset:3136
	global_store_short v0, v14, s[4:5] offset:128
	global_store_short v0, v15, s[4:5] offset:1152
	global_store_short v0, v16, s[4:5] offset:2176
	global_store_short v0, v17, s[4:5] offset:3200
	global_store_short v0, v18, s[4:5] offset:192
	global_store_short v0, v19, s[4:5] offset:1216
	global_store_short v0, v20, s[4:5] offset:2240
	global_store_short v0, v21, s[4:5] offset:3264
	s_endpgm
.Lagg_w2t:
	v_lshl_or_b32 v0, v1, 11, v0
	v_add_u32_e32 v1, 0x10000, v0
	s_lshl_b32 s0, s10, 17
	s_lshl_b32 s1, s9, 12
	s_add_i32 s0, s0, s1
	s_add_u32 s4, s4, s0
	s_addc_u32 s5, s5, 0
	global_store_short v0, v6, s[4:5]
	global_store_short v0, v7, s[4:5] offset:1024
	global_store_short v0, v8, s[4:5] offset:64
	global_store_short v0, v9, s[4:5] offset:1088
	global_store_short v0, v10, s[4:5] offset:128
	global_store_short v0, v11, s[4:5] offset:1152
	global_store_short v0, v12, s[4:5] offset:192
	global_store_short v0, v13, s[4:5] offset:1216
	global_store_short v1, v14, s[4:5]
	global_store_short v1, v15, s[4:5] offset:1024
	global_store_short v1, v16, s[4:5] offset:64
	global_store_short v1, v17, s[4:5] offset:1088
	global_store_short v1, v18, s[4:5] offset:128
	global_store_short v1, v19, s[4:5] offset:1152
	global_store_short v1, v20, s[4:5] offset:192
	global_store_short v1, v21, s[4:5] offset:1216
	s_endpgm

_Z6gemm_kILi0ELi1ELi2EEvPKDF16_S1_iiiPKfS1_PDF16_PfS4_:
	s_lshr_b32 s37, s2, 3
	s_cmp_lt_u32 s37, 128
	s_cbranch_scc1 LgA_exit
	s_sub_u32 s37, s37, 128
	s_and_b32 s36, s2, 7
	s_cmp_ge_u32 s37, 30
	s_cbranch_scc1 LgA_map_tail
	s_cmp_ge_u32 s37, 10
	s_cselect_b32 s38, 1, 0
	s_cmp_ge_u32 s37, 20
	s_cselect_b32 s39, 1, 0
	s_add_u32 s38, s38, s39
	s_mul_i32 s39, s38, 10
	s_sub_u32 s21, s37, s39
	s_mul_i32 s36, s36, 3
	s_add_u32 s22, s36, s38
	s_branch LgA_map_done

LgA_map_done:
	s_load_dwordx4 s[4:7], s[0:1], 0x0
	s_load_dwordx4 s[8:11], s[0:1], 0x20
	s_load_dwordx4 s[12:15], s[0:1], 0x30
	s_load_dwordx2 s[16:17], s[0:1], 0x40
	v_lshrrev_b32_e32 v20, 6, v0
	v_and_b32_e32 v1, 63, v0
	v_readfirstlane_b32 s20, v20
	v_and_b32_e32 v2, 15, v0
	v_bfe_u32 v3, v0, 4, 2
	v_and_b32_e32 v16, 7, v2
	v_xor_b32_e32 v16, v16, v3
	v_lshlrev_b32_e32 v16, 4, v16
	v_lshl_or_b32 v4, v2, 7, v16
	v_lshrrev_b32_e32 v16, 3, v1
	v_and_b32_e32 v17, 7, v1
	v_xor_b32_e32 v17, v17, v16
	v_lshlrev_b32_e32 v17, 4, v17
	v_lshl_or_b32 v9, v16, 7, v17
	v_add_u32_e32 v10, 0x140000, v9
	s_mul_i32 s23, s22, 25
	s_sub_u32 s24, 625, s23
	s_min_u32 s24, s24, 25
	s_waitcnt lgkmcnt(0)
	s_mul_i32 s36, s20, 0x280000
	s_lshl_b32 s37, s23, 11
	s_add_u32 s36, s36, s37
	s_add_u32 s26, s4, s36
	s_addc_u32 s27, s5, 0
	s_mul_i32 s28, s20, 0x1000
	s_add_u32 s46, s28, 0x14000
	s_mov_b32 s47, s28
	s_mov_b32 s29, 0
	s_cmp_ge_u32 s21, 8
	s_cbranch_scc1 LgA_setup_self
	v_mul_u32_u24_e32 v16, 2176, v2
	v_lshl_add_u32 v14, v3, 4, v16
	s_lshr_b32 s36, s21, 1
	s_lshl_b32 s37, s23, 6
	s_add_u32 s36, s36, s37
	s_mul_i32 s36, s36, 544
	s_and_b32 s37, s21, 1
	s_lshl_b32 s38, s37, 8
	s_lshl_b32 s39, s20, 6
	s_add_u32 s38, s38, s39
	s_add_u32 s36, s36, s38
	s_add_u32 s30, s12, s36
	s_addc_u32 s31, s13, 0
	s_mul_i32 s37, s37, 240
	s_mul_i32 s39, s20, 60
	s_add_u32 s37, s37, s39
	s_sub_u32 s37, 512, s37
	v_add_u32_e32 v112, s37, v16
	s_mov_b32 s44, 0x0c0c0400
	s_mov_b32 s45, 0x05040100
	s_branch LgA_setup_done

LgA_setup_done:
	s_mov_b32 m0, s28
	s_add_u32 s28, s28, 0x4000
	s_cmp_ge_u32 s28, s46
	s_cselect_b32 s28, s47, s28
	global_load_lds_dwordx4 v9, s[26:27]
	global_load_lds_dwordx4 v9, s[26:27] offset:1024
	s_add_u32 m0, m0, 0x800
	s_nop 0
	global_load_lds_dwordx4 v10, s[26:27]
	global_load_lds_dwordx4 v10, s[26:27] offset:1024
	s_add_u32 s26, s26, 0x800
	s_addc_u32 s27, s27, 0
	s_mov_b32 m0, s28
	s_add_u32 s28, s28, 0x4000
	s_cmp_ge_u32 s28, s46
	s_cselect_b32 s28, s47, s28
	global_load_lds_dwordx4 v9, s[26:27]
	global_load_lds_dwordx4 v9, s[26:27] offset:1024
	s_add_u32 m0, m0, 0x800
	s_nop 0
	global_load_lds_dwordx4 v10, s[26:27]
	global_load_lds_dwordx4 v10, s[26:27] offset:1024
	s_add_u32 s26, s26, 0x800
	s_addc_u32 s27, s27, 0
	s_lshl_b32 s36, s21, 2
	s_add_u32 s36, s36, s20
	s_mul_i32 s36, s36, 0x10000
	v_lshlrev_b32_e32 v16, 4, v1
	v_add_u32_e32 v13, s36, v16
	global_load_dwordx4 a[0:3], v13, s[6:7] offset:0
	global_load_dwordx4 a[4:7], v13, s[6:7] offset:1024
	global_load_dwordx4 a[8:11], v13, s[6:7] offset:2048
	global_load_dwordx4 a[12:15], v13, s[6:7] offset:3072
	v_add_u32_e32 v13, 0x1000, v13
	global_load_dwordx4 a[16:19], v13, s[6:7] offset:0
	global_load_dwordx4 a[20:23], v13, s[6:7] offset:1024
	global_load_dwordx4 a[24:27], v13, s[6:7] offset:2048
	global_load_dwordx4 a[28:31], v13, s[6:7] offset:3072
	v_add_u32_e32 v13, 0x1000, v13
	global_load_dwordx4 a[32:35], v13, s[6:7] offset:0
	global_load_dwordx4 a[36:39], v13, s[6:7] offset:1024
	global_load_dwordx4 a[40:43], v13, s[6:7] offset:2048
	global_load_dwordx4 a[44:47], v13, s[6:7] offset:3072
	v_add_u32_e32 v13, 0x1000, v13
	global_load_dwordx4 a[48:51], v13, s[6:7] offset:0
	global_load_dwordx4 a[52:55], v13, s[6:7] offset:1024
	global_load_dwordx4 a[56:59], v13, s[6:7] offset:2048
	global_load_dwordx4 a[60:63], v13, s[6:7] offset:3072
	v_add_u32_e32 v13, 0x1000, v13
	global_load_dwordx4 a[64:67], v13, s[6:7] offset:0
	global_load_dwordx4 a[68:71], v13, s[6:7] offset:1024
	global_load_dwordx4 a[72:75], v13, s[6:7] offset:2048
	global_load_dwordx4 a[76:79], v13, s[6:7] offset:3072
	v_add_u32_e32 v13, 0x1000, v13
	global_load_dwordx4 a[80:83], v13, s[6:7] offset:0
	global_load_dwordx4 a[84:87], v13, s[6:7] offset:1024
	global_load_dwordx4 a[88:91], v13, s[6:7] offset:2048
	global_load_dwordx4 a[92:95], v13, s[6:7] offset:3072
	v_add_u32_e32 v13, 0x1000, v13
	global_load_dwordx4 a[96:99], v13, s[6:7] offset:0
	global_load_dwordx4 a[100:103], v13, s[6:7] offset:1024
	global_load_dwordx4 a[104:107], v13, s[6:7] offset:2048
	global_load_dwordx4 a[108:111], v13, s[6:7] offset:3072
	v_add_u32_e32 v13, 0x1000, v13
	global_load_dwordx4 a[112:115], v13, s[6:7] offset:0
	global_load_dwordx4 a[116:119], v13, s[6:7] offset:1024
	global_load_dwordx4 a[120:123], v13, s[6:7] offset:2048
	global_load_dwordx4 a[124:127], v13, s[6:7] offset:3072
	v_add_u32_e32 v13, 0x1000, v13
	global_load_dwordx4 a[128:131], v13, s[6:7] offset:0
	global_load_dwordx4 a[132:135], v13, s[6:7] offset:1024
	global_load_dwordx4 a[136:139], v13, s[6:7] offset:2048
	global_load_dwordx4 a[140:143], v13, s[6:7] offset:3072
	v_add_u32_e32 v13, 0x1000, v13
	global_load_dwordx4 a[144:147], v13, s[6:7] offset:0
	global_load_dwordx4 a[148:151], v13, s[6:7] offset:1024
	global_load_dwordx4 a[152:155], v13, s[6:7] offset:2048
	global_load_dwordx4 a[156:159], v13, s[6:7] offset:3072
	v_add_u32_e32 v13, 0x1000, v13
	global_load_dwordx4 a[160:163], v13, s[6:7] offset:0
	global_load_dwordx4 a[164:167], v13, s[6:7] offset:1024
	global_load_dwordx4 a[168:171], v13, s[6:7] offset:2048
	global_load_dwordx4 a[172:175], v13, s[6:7] offset:3072
	v_add_u32_e32 v13, 0x1000, v13
	global_load_dwordx4 a[176:179], v13, s[6:7] offset:0
	global_load_dwordx4 a[180:183], v13, s[6:7] offset:1024
	global_load_dwordx4 a[184:187], v13, s[6:7] offset:2048
	global_load_dwordx4 a[188:191], v13, s[6:7] offset:3072
	v_add_u32_e32 v13, 0x1000, v13
	global_load_dwordx4 a[192:195], v13, s[6:7] offset:0
	global_load_dwordx4 a[196:199], v13, s[6:7] offset:1024
	global_load_dwordx4 a[200:203], v13, s[6:7] offset:2048
	global_load_dwordx4 a[204:207], v13, s[6:7] offset:3072
	v_add_u32_e32 v13, 0x1000, v13
	global_load_dwordx4 a[208:211], v13, s[6:7] offset:0
	global_load_dwordx4 a[212:215], v13, s[6:7] offset:1024
	global_load_dwordx4 a[216:219], v13, s[6:7] offset:2048
	global_load_dwordx4 a[220:223], v13, s[6:7] offset:3072
	v_add_u32_e32 v13, 0x1000, v13
	global_load_dwordx4 a[224:227], v13, s[6:7] offset:0
	global_load_dwordx4 a[228:231], v13, s[6:7] offset:1024
	global_load_dwordx4 a[232:235], v13, s[6:7] offset:2048
	global_load_dwordx4 a[236:239], v13, s[6:7] offset:3072
	v_add_u32_e32 v13, 0x1000, v13
	global_load_dwordx4 a[240:243], v13, s[6:7] offset:0
	global_load_dwordx4 a[244:247], v13, s[6:7] offset:1024
	global_load_dwordx4 a[248:251], v13, s[6:7] offset:2048
	global_load_dwordx4 a[252:255], v13, s[6:7] offset:3072
	s_mov_b32 m0, s28
	s_add_u32 s28, s28, 0x4000
	s_cmp_ge_u32 s28, s46
	s_cselect_b32 s28, s47, s28
	global_load_lds_dwordx4 v9, s[26:27]
	global_load_lds_dwordx4 v9, s[26:27] offset:1024
	s_add_u32 m0, m0, 0x800
	s_nop 0
	global_load_lds_dwordx4 v10, s[26:27]
	global_load_lds_dwordx4 v10, s[26:27] offset:1024
	s_add_u32 s26, s26, 0x800
	s_addc_u32 s27, s27, 0
	s_mov_b32 m0, s28
	s_add_u32 s28, s28, 0x4000
	s_cmp_ge_u32 s28, s46
	s_cselect_b32 s28, s47, s28
	global_load_lds_dwordx4 v9, s[26:27]
	global_load_lds_dwordx4 v9, s[26:27] offset:1024
	s_add_u32 m0, m0, 0x800
	s_nop 0
	global_load_lds_dwordx4 v10, s[26:27]
	global_load_lds_dwordx4 v10, s[26:27] offset:1024
	s_add_u32 s26, s26, 0x800
	s_addc_u32 s27, s27, 0
	s_waitcnt vmcnt(63)
	s_barrier
	v_add_u32_e32 v5, s29, v4
	v_xor_b32_e32 v6, 64, v5
	s_add_u32 s29, s29, 0x4000
	s_cmp_ge_u32 s29, 0x14000
	s_cselect_b32 s29, 0, s29
	ds_read_b128 v[128:131], v5 offset:0
	ds_read_b128 v[132:135], v6 offset:0
	ds_read_b128 v[136:139], v5 offset:2048
	ds_read_b128 v[140:143], v6 offset:2048
	ds_read_b128 v[144:147], v5 offset:4096
	ds_read_b128 v[148:151], v6 offset:4096
	ds_read_b128 v[152:155], v5 offset:6144
	ds_read_b128 v[156:159], v6 offset:6144
	ds_read_b128 v[160:163], v5 offset:8192
	ds_read_b128 v[164:167], v6 offset:8192
	ds_read_b128 v[168:171], v5 offset:10240
	ds_read_b128 v[172:175], v6 offset:10240
	ds_read_b128 v[176:179], v5 offset:12288
	ds_read_b128 v[180:183], v6 offset:12288
	ds_read_b128 v[184:187], v5 offset:14336
	ds_read_b128 v[188:191], v6 offset:14336
	s_waitcnt lgkmcnt(0)
	s_cmp_ge_u32 s21, 8
	s_cbranch_scc1 LgA_self_body
	s_mov_b32 m0, s28
	s_add_u32 s28, s28, 0x4000
	s_cmp_ge_u32 s28, s46
	s_cselect_b32 s28, s47, s28
	global_load_lds_dwordx4 v9, s[26:27]
	global_load_lds_dwordx4 v9, s[26:27] offset:1024
	s_add_u32 m0, m0, 0x800
	s_nop 0
	global_load_lds_dwordx4 v10, s[26:27]
	global_load_lds_dwordx4 v10, s[26:27] offset:1024
	s_add_u32 s26, s26, 0x800
	s_addc_u32 s27, s27, 0
	v_add_u32_e32 v7, s29, v4
	v_xor_b32_e32 v8, 64, v7
	s_add_u32 s29, s29, 0x4000
	s_cmp_ge_u32 s29, 0x14000
	s_cselect_b32 s29, 0, s29
	s_waitcnt vmcnt(63)
	v_mfma_f32_16x16x32_f16 v[48:51], a[0:3], v[128:131], 0
	v_mfma_f32_16x16x32_f16 v[52:55], a[4:7], v[128:131], 0
	v_mfma_f32_16x16x32_f16 v[56:59], a[8:11], v[128:131], 0
	ds_read_b128 v[192:195], v7 offset:0
	v_mfma_f32_16x16x32_f16 v[60:63], a[12:15], v[128:131], 0
	ds_read_b128 v[196:199], v8 offset:0
	s_waitcnt vmcnt(63)
	v_mfma_f32_16x16x32_f16 v[48:51], a[16:19], v[132:135], v[48:51]
	ds_read_b128 v[200:203], v7 offset:2048
	v_mfma_f32_16x16x32_f16 v[52:55], a[20:23], v[132:135], v[52:55]
	ds_read_b128 v[204:207], v8 offset:2048
	v_mfma_f32_16x16x32_f16 v[56:59], a[24:27], v[132:135], v[56:59]
	ds_read_b128 v[208:211], v7 offset:4096
	v_mfma_f32_16x16x32_f16 v[60:63], a[28:31], v[132:135], v[60:63]
	ds_read_b128 v[212:215], v8 offset:4096
	s_waitcnt vmcnt(63)
	v_mfma_f32_16x16x32_f16 v[48:51], a[32:35], v[136:139], v[48:51]
	ds_read_b128 v[216:219], v7 offset:6144
	v_mfma_f32_16x16x32_f16 v[52:55], a[36:39], v[136:139], v[52:55]
	ds_read_b128 v[220:223], v8 offset:6144
	v_mfma_f32_16x16x32_f16 v[56:59], a[40:43], v[136:139], v[56:59]
	ds_read_b128 v[224:227], v7 offset:8192
	v_mfma_f32_16x16x32_f16 v[60:63], a[44:47], v[136:139], v[60:63]
	ds_read_b128 v[228:231], v8 offset:8192
	s_waitcnt vmcnt(60)
	v_mfma_f32_16x16x32_f16 v[48:51], a[48:51], v[140:143], v[48:51]
	ds_read_b128 v[232:235], v7 offset:10240
	v_mfma_f32_16x16x32_f16 v[52:55], a[52:55], v[140:143], v[52:55]
	ds_read_b128 v[236:239], v8 offset:10240
	v_mfma_f32_16x16x32_f16 v[56:59], a[56:59], v[140:143], v[56:59]
	ds_read_b128 v[240:243], v7 offset:12288
	v_mfma_f32_16x16x32_f16 v[60:63], a[60:63], v[140:143], v[60:63]
	ds_read_b128 v[244:247], v8 offset:12288
	s_waitcnt vmcnt(56)
	v_mfma_f32_16x16x32_f16 v[48:51], a[64:67], v[144:147], v[48:51]
	ds_read_b128 v[248:251], v7 offset:14336
	v_mfma_f32_16x16x32_f16 v[52:55], a[68:71], v[144:147], v[52:55]
	ds_read_b128 v[252:255], v8 offset:14336
	v_mfma_f32_16x16x32_f16 v[56:59], a[72:75], v[144:147], v[56:59]
	v_mfma_f32_16x16x32_f16 v[60:63], a[76:79], v[144:147], v[60:63]
	s_waitcnt vmcnt(52)
	v_mfma_f32_16x16x32_f16 v[48:51], a[80:83], v[148:151], v[48:51]
	v_mfma_f32_16x16x32_f16 v[52:55], a[84:87], v[148:151], v[52:55]
	v_mfma_f32_16x16x32_f16 v[56:59], a[88:91], v[148:151], v[56:59]
	v_mfma_f32_16x16x32_f16 v[60:63], a[92:95], v[148:151], v[60:63]
	s_waitcnt vmcnt(48)
	v_mfma_f32_16x16x32_f16 v[48:51], a[96:99], v[152:155], v[48:51]
	v_mfma_f32_16x16x32_f16 v[52:55], a[100:103], v[152:155], v[52:55]
	v_mfma_f32_16x16x32_f16 v[56:59], a[104:107], v[152:155], v[56:59]
	v_mfma_f32_16x16x32_f16 v[60:63], a[108:111], v[152:155], v[60:63]
	s_waitcnt vmcnt(44)
	v_mfma_f32_16x16x32_f16 v[48:51], a[112:115], v[156:159], v[48:51]
	v_mfma_f32_16x16x32_f16 v[52:55], a[116:119], v[156:159], v[52:55]
	v_mfma_f32_16x16x32_f16 v[56:59], a[120:123], v[156:159], v[56:59]
	v_mfma_f32_16x16x32_f16 v[60:63], a[124:127], v[156:159], v[60:63]
	s_waitcnt vmcnt(40)
	v_mfma_f32_16x16x32_f16 v[48:51], a[128:131], v[160:163], v[48:51]
	v_mfma_f32_16x16x32_f16 v[52:55], a[132:135], v[160:163], v[52:55]
	v_mfma_f32_16x16x32_f16 v[56:59], a[136:139], v[160:163], v[56:59]
	v_mfma_f32_16x16x32_f16 v[60:63], a[140:143], v[160:163], v[60:63]
	s_waitcnt vmcnt(36)
	v_mfma_f32_16x16x32_f16 v[48:51], a[144:147], v[164:167], v[48:51]
	v_mfma_f32_16x16x32_f16 v[52:55], a[148:151], v[164:167], v[52:55]
	v_mfma_f32_16x16x32_f16 v[56:59], a[152:155], v[164:167], v[56:59]
	v_mfma_f32_16x16x32_f16 v[60:63], a[156:159], v[164:167], v[60:63]
	s_waitcnt vmcnt(32)
	v_mfma_f32_16x16x32_f16 v[48:51], a[160:163], v[168:171], v[48:51]
	v_mfma_f32_16x16x32_f16 v[52:55], a[164:167], v[168:171], v[52:55]
	v_mfma_f32_16x16x32_f16 v[56:59], a[168:171], v[168:171], v[56:59]
	v_mfma_f32_16x16x32_f16 v[60:63], a[172:175], v[168:171], v[60:63]
	s_waitcnt vmcnt(28)
	v_mfma_f32_16x16x32_f16 v[48:51], a[176:179], v[172:175], v[48:51]
	v_mfma_f32_16x16x32_f16 v[52:55], a[180:183], v[172:175], v[52:55]
	v_mfma_f32_16x16x32_f16 v[56:59], a[184:187], v[172:175], v[56:59]
	v_mfma_f32_16x16x32_f16 v[60:63], a[188:191], v[172:175], v[60:63]
	s_waitcnt vmcnt(24)
	v_mfma_f32_16x16x32_f16 v[48:51], a[192:195], v[176:179], v[48:51]
	v_mfma_f32_16x16x32_f16 v[52:55], a[196:199], v[176:179], v[52:55]
	v_mfma_f32_16x16x32_f16 v[56:59], a[200:203], v[176:179], v[56:59]
	v_mfma_f32_16x16x32_f16 v[60:63], a[204:207], v[176:179], v[60:63]
	s_waitcnt vmcnt(20)
	v_mfma_f32_16x16x32_f16 v[48:51], a[208:211], v[180:183], v[48:51]
	v_mfma_f32_16x16x32_f16 v[52:55], a[212:215], v[180:183], v[52:55]
	v_mfma_f32_16x16x32_f16 v[56:59], a[216:219], v[180:183], v[56:59]
	v_mfma_f32_16x16x32_f16 v[60:63], a[220:223], v[180:183], v[60:63]
	s_waitcnt vmcnt(16)
	v_mfma_f32_16x16x32_f16 v[48:51], a[224:227], v[184:187], v[48:51]
	v_mfma_f32_16x16x32_f16 v[52:55], a[228:231], v[184:187], v[52:55]
	v_mfma_f32_16x16x32_f16 v[56:59], a[232:235], v[184:187], v[56:59]
	v_mfma_f32_16x16x32_f16 v[60:63], a[236:239], v[184:187], v[60:63]
	s_waitcnt vmcnt(12)
	v_mfma_f32_16x16x32_f16 v[48:51], a[240:243], v[188:191], v[48:51]
	v_mfma_f32_16x16x32_f16 v[52:55], a[244:247], v[188:191], v[52:55]
	v_mfma_f32_16x16x32_f16 v[56:59], a[248:251], v[188:191], v[56:59]
	v_mfma_f32_16x16x32_f16 v[60:63], a[252:255], v[188:191], v[60:63]
LgAq_loop:
	s_waitcnt vmcnt(8) lgkmcnt(0)
	s_barrier
	v_mfma_f32_16x16x32_f16 v[64:67], a[0:3], v[192:195], 0
	v_mfma_f32_16x16x32_f16 v[68:71], a[4:7], v[192:195], 0
	v_add_u32_e32 v5, s29, v4
	v_xor_b32_e32 v6, 64, v5
	s_add_u32 s29, s29, 0x4000
	s_cmp_ge_u32 s29, 0x14000
	s_cselect_b32 s29, 0, s29
	v_mfma_f32_16x16x32_f16 v[72:75], a[8:11], v[192:195], 0
	ds_read_b128 v[128:131], v5 offset:0
	v_mfma_f32_16x16x32_f16 v[76:79], a[12:15], v[192:195], 0
	ds_read_b128 v[132:135], v6 offset:0
	v_max3_f32 v16, |v48|, 0, |v49|
	v_mfma_f32_16x16x32_f16 v[64:67], a[16:19], v[196:199], v[64:67]
	ds_read_b128 v[136:139], v5 offset:2048
	v_max3_f32 v16, v16, |v50|, |v51|
	v_mfma_f32_16x16x32_f16 v[68:71], a[20:23], v[196:199], v[68:71]
	ds_read_b128 v[140:143], v6 offset:2048
	v_max3_f32 v16, v16, |v52|, |v53|
	v_mfma_f32_16x16x32_f16 v[72:75], a[24:27], v[196:199], v[72:75]
	ds_read_b128 v[144:147], v5 offset:4096
	v_max3_f32 v16, v16, |v54|, |v55|
	v_mfma_f32_16x16x32_f16 v[76:79], a[28:31], v[196:199], v[76:79]
	ds_read_b128 v[148:151], v6 offset:4096
	v_max3_f32 v16, v16, |v56|, |v57|
	v_mfma_f32_16x16x32_f16 v[64:67], a[32:35], v[200:203], v[64:67]
	ds_read_b128 v[152:155], v5 offset:6144
	v_max3_f32 v16, v16, |v58|, |v59|
	v_mfma_f32_16x16x32_f16 v[68:71], a[36:39], v[200:203], v[68:71]
	ds_read_b128 v[156:159], v6 offset:6144
	v_max3_f32 v16, v16, |v60|, |v61|
	v_mfma_f32_16x16x32_f16 v[72:75], a[40:43], v[200:203], v[72:75]
	ds_read_b128 v[160:163], v5 offset:8192
	v_max3_f32 v16, v16, |v62|, |v63|
	v_mfma_f32_16x16x32_f16 v[76:79], a[44:47], v[200:203], v[76:79]
	ds_read_b128 v[164:167], v6 offset:8192
	v_mov_b32_e32 v17, v16
	v_mfma_f32_16x16x32_f16 v[64:67], a[48:51], v[204:207], v[64:67]
	ds_read_b128 v[168:171], v5 offset:10240
	v_mov_b32_e32 v18, v16
	v_mfma_f32_16x16x32_f16 v[68:71], a[52:55], v[204:207], v[68:71]
	ds_read_b128 v[172:175], v6 offset:10240
	v_permlane32_swap_b32_e32 v17, v18
	v_mfma_f32_16x16x32_f16 v[72:75], a[56:59], v[204:207], v[72:75]
	ds_read_b128 v[176:179], v5 offset:12288
	v_max_f32_e32 v16, v17, v18
	v_mfma_f32_16x16x32_f16 v[76:79], a[60:63], v[204:207], v[76:79]
	ds_read_b128 v[180:183], v6 offset:12288
	v_mov_b32_e32 v17, v16
	v_mfma_f32_16x16x32_f16 v[64:67], a[64:67], v[208:211], v[64:67]
	ds_read_b128 v[184:187], v5 offset:14336
	v_mfma_f32_16x16x32_f16 v[68:71], a[68:71], v[208:211], v[68:71]
	ds_read_b128 v[188:191], v6 offset:14336
	v_mov_b32_e32 v18, v16
	v_mfma_f32_16x16x32_f16 v[72:75], a[72:75], v[208:211], v[72:75]
	s_nop 0
	v_permlane16_swap_b32_e32 v17, v18
	v_mfma_f32_16x16x32_f16 v[76:79], a[76:79], v[208:211], v[76:79]
	v_max_f32_e32 v16, v17, v18
	v_mfma_f32_16x16x32_f16 v[64:67], a[80:83], v[212:215], v[64:67]
	v_rcp_f32_e32 v19, v16
	v_mfma_f32_16x16x32_f16 v[68:71], a[84:87], v[212:215], v[68:71]
	v_cmp_lt_f32_e32 vcc, 0, v16
	v_mfma_f32_16x16x32_f16 v[72:75], a[88:91], v[212:215], v[72:75]
	s_mov_b32 m0, s28
	s_add_u32 s28, s28, 0x4000
	s_cmp_ge_u32 s28, s46
	s_cselect_b32 s28, s47, s28
	global_load_lds_dwordx4 v9, s[26:27]
	v_mul_f32_e32 v19, 0x42fe0000, v19
	v_mfma_f32_16x16x32_f16 v[76:79], a[92:95], v[212:215], v[76:79]
	v_mul_f32_e32 v20, 0x3c010204, v16
	v_mfma_f32_16x16x32_f16 v[64:67], a[96:99], v[216:219], v[64:67]
	v_cndmask_b32_e32 v19, 0, v19, vcc
	v_mfma_f32_16x16x32_f16 v[68:71], a[100:103], v[216:219], v[68:71]
	v_cndmask_b32_e32 v20, 1.0, v20, vcc
	v_mfma_f32_16x16x32_f16 v[72:75], a[104:107], v[216:219], v[72:75]
	v_fmaak_f32 v96, v19, v48, 0x4b400000
	v_mfma_f32_16x16x32_f16 v[76:79], a[108:111], v[216:219], v[76:79]
	v_fmaak_f32 v97, v19, v49, 0x4b400000
	v_mfma_f32_16x16x32_f16 v[64:67], a[112:115], v[220:223], v[64:67]
	v_fmaak_f32 v98, v19, v50, 0x4b400000
	v_mfma_f32_16x16x32_f16 v[68:71], a[116:119], v[220:223], v[68:71]
	v_fmaak_f32 v99, v19, v51, 0x4b400000
	v_mfma_f32_16x16x32_f16 v[72:75], a[120:123], v[220:223], v[72:75]
	v_mfma_f32_16x16x32_f16 v[76:79], a[124:127], v[220:223], v[76:79]
	v_fmaak_f32 v100, v19, v52, 0x4b400000
	v_mfma_f32_16x16x32_f16 v[64:67], a[128:131], v[224:227], v[64:67]
	v_fmaak_f32 v101, v19, v53, 0x4b400000
	v_mfma_f32_16x16x32_f16 v[68:71], a[132:135], v[224:227], v[68:71]
	global_load_lds_dwordx4 v9, s[26:27] offset:1024
	v_fmaak_f32 v102, v19, v54, 0x4b400000
	v_mfma_f32_16x16x32_f16 v[72:75], a[136:139], v[224:227], v[72:75]
	v_fmaak_f32 v103, v19, v55, 0x4b400000
	v_mfma_f32_16x16x32_f16 v[76:79], a[140:143], v[224:227], v[76:79]
	v_fmaak_f32 v104, v19, v56, 0x4b400000
	v_mfma_f32_16x16x32_f16 v[64:67], a[144:147], v[228:231], v[64:67]
	v_fmaak_f32 v105, v19, v57, 0x4b400000
	v_mfma_f32_16x16x32_f16 v[68:71], a[148:151], v[228:231], v[68:71]
	v_fmaak_f32 v106, v19, v58, 0x4b400000
	v_mfma_f32_16x16x32_f16 v[72:75], a[152:155], v[228:231], v[72:75]
	v_fmaak_f32 v107, v19, v59, 0x4b400000
	v_mfma_f32_16x16x32_f16 v[76:79], a[156:159], v[228:231], v[76:79]
	v_fmaak_f32 v108, v19, v60, 0x4b400000
	v_mfma_f32_16x16x32_f16 v[64:67], a[160:163], v[232:235], v[64:67]
	v_fmaak_f32 v109, v19, v61, 0x4b400000
	v_mfma_f32_16x16x32_f16 v[68:71], a[164:167], v[232:235], v[68:71]
	v_fmaak_f32 v110, v19, v62, 0x4b400000
	v_mfma_f32_16x16x32_f16 v[72:75], a[168:171], v[232:235], v[72:75]
	v_fmaak_f32 v111, v19, v63, 0x4b400000
	v_mfma_f32_16x16x32_f16 v[76:79], a[172:175], v[232:235], v[76:79]
	v_perm_b32 v21, v97, v96, s44
	v_mfma_f32_16x16x32_f16 v[64:67], a[176:179], v[236:239], v[64:67]
	s_add_u32 m0, m0, 0x800
	s_nop 0
	global_load_lds_dwordx4 v10, s[26:27]
	v_mfma_f32_16x16x32_f16 v[68:71], a[180:183], v[236:239], v[68:71]
	v_perm_b32 v22, v99, v98, s44
	v_mfma_f32_16x16x32_f16 v[72:75], a[184:187], v[236:239], v[72:75]
	v_perm_b32 v23, v101, v100, s44
	v_mfma_f32_16x16x32_f16 v[76:79], a[188:191], v[236:239], v[76:79]
	v_perm_b32 v24, v103, v102, s44
	v_mfma_f32_16x16x32_f16 v[64:67], a[192:195], v[240:243], v[64:67]
	v_perm_b32 v25, v105, v104, s44
	v_mfma_f32_16x16x32_f16 v[68:71], a[196:199], v[240:243], v[68:71]
	v_perm_b32 v26, v107, v106, s44
	v_mfma_f32_16x16x32_f16 v[72:75], a[200:203], v[240:243], v[72:75]
	v_perm_b32 v27, v109, v108, s44
	v_mfma_f32_16x16x32_f16 v[76:79], a[204:207], v[240:243], v[76:79]
	v_perm_b32 v28, v111, v110, s44
	v_mfma_f32_16x16x32_f16 v[64:67], a[208:211], v[244:247], v[64:67]
	v_perm_b32 v96, v22, v21, s45
	v_mfma_f32_16x16x32_f16 v[68:71], a[212:215], v[244:247], v[68:71]
	v_perm_b32 v97, v24, v23, s45
	v_mfma_f32_16x16x32_f16 v[72:75], a[216:219], v[244:247], v[72:75]
	v_perm_b32 v98, v26, v25, s45
	v_mfma_f32_16x16x32_f16 v[76:79], a[220:223], v[244:247], v[76:79]
	v_perm_b32 v99, v28, v27, s45
	v_mfma_f32_16x16x32_f16 v[64:67], a[224:227], v[248:251], v[64:67]
	global_load_lds_dwordx4 v10, s[26:27] offset:1024
	global_store_dwordx4 v14, v[96:99], s[30:31]
	v_mfma_f32_16x16x32_f16 v[68:71], a[228:231], v[248:251], v[68:71]
	s_add_u32 s26, s26, 0x800
	s_addc_u32 s27, s27, 0
	global_store_dword v112, v20, s[30:31]
	v_mfma_f32_16x16x32_f16 v[72:75], a[232:235], v[248:251], v[72:75]
	v_mfma_f32_16x16x32_f16 v[76:79], a[236:239], v[248:251], v[76:79]
	s_add_u32 s30, s30, 0x8800
	s_addc_u32 s31, s31, 0
	v_mfma_f32_16x16x32_f16 v[64:67], a[240:243], v[252:255], v[64:67]
	v_mfma_f32_16x16x32_f16 v[68:71], a[244:247], v[252:255], v[68:71]
	v_mfma_f32_16x16x32_f16 v[72:75], a[248:251], v[252:255], v[72:75]
	v_mfma_f32_16x16x32_f16 v[76:79], a[252:255], v[252:255], v[76:79]
	s_sub_u32 s24, s24, 1
	s_cmp_le_u32 s24, 1
	s_cbranch_scc1 LgAq_exitA
	s_waitcnt vmcnt(8) lgkmcnt(0)
	s_barrier
	v_mfma_f32_16x16x32_f16 v[48:51], a[0:3], v[128:131], 0
	v_mfma_f32_16x16x32_f16 v[52:55], a[4:7], v[128:131], 0
	v_add_u32_e32 v7, s29, v4
	v_xor_b32_e32 v8, 64, v7
	s_add_u32 s29, s29, 0x4000
	s_cmp_ge_u32 s29, 0x14000
	s_cselect_b32 s29, 0, s29
	v_mfma_f32_16x16x32_f16 v[56:59], a[8:11], v[128:131], 0
	ds_read_b128 v[192:195], v7 offset:0
	v_mfma_f32_16x16x32_f16 v[60:63], a[12:15], v[128:131], 0
	ds_read_b128 v[196:199], v8 offset:0
	v_max3_f32 v16, |v64|, 0, |v65|
	v_mfma_f32_16x16x32_f16 v[48:51], a[16:19], v[132:135], v[48:51]
	ds_read_b128 v[200:203], v7 offset:2048
	v_max3_f32 v16, v16, |v66|, |v67|
	v_mfma_f32_16x16x32_f16 v[52:55], a[20:23], v[132:135], v[52:55]
	ds_read_b128 v[204:207], v8 offset:2048
	v_max3_f32 v16, v16, |v68|, |v69|
	v_mfma_f32_16x16x32_f16 v[56:59], a[24:27], v[132:135], v[56:59]
	ds_read_b128 v[208:211], v7 offset:4096
	v_max3_f32 v16, v16, |v70|, |v71|
	v_mfma_f32_16x16x32_f16 v[60:63], a[28:31], v[132:135], v[60:63]
	ds_read_b128 v[212:215], v8 offset:4096
	v_max3_f32 v16, v16, |v72|, |v73|
	v_mfma_f32_16x16x32_f16 v[48:51], a[32:35], v[136:139], v[48:51]
	ds_read_b128 v[216:219], v7 offset:6144
	v_max3_f32 v16, v16, |v74|, |v75|
	v_mfma_f32_16x16x32_f16 v[52:55], a[36:39], v[136:139], v[52:55]
	ds_read_b128 v[220:223], v8 offset:6144
	v_max3_f32 v16, v16, |v76|, |v77|
	v_mfma_f32_16x16x32_f16 v[56:59], a[40:43], v[136:139], v[56:59]
	ds_read_b128 v[224:227], v7 offset:8192
	v_max3_f32 v16, v16, |v78|, |v79|
	v_mfma_f32_16x16x32_f16 v[60:63], a[44:47], v[136:139], v[60:63]
	ds_read_b128 v[228:231], v8 offset:8192
	v_mov_b32_e32 v17, v16
	v_mfma_f32_16x16x32_f16 v[48:51], a[48:51], v[140:143], v[48:51]
	ds_read_b128 v[232:235], v7 offset:10240
	v_mov_b32_e32 v18, v16
	v_mfma_f32_16x16x32_f16 v[52:55], a[52:55], v[140:143], v[52:55]
	ds_read_b128 v[236:239], v8 offset:10240
	v_permlane32_swap_b32_e32 v17, v18
	v_mfma_f32_16x16x32_f16 v[56:59], a[56:59], v[140:143], v[56:59]
	ds_read_b128 v[240:243], v7 offset:12288
	v_max_f32_e32 v16, v17, v18
	v_mfma_f32_16x16x32_f16 v[60:63], a[60:63], v[140:143], v[60:63]
	ds_read_b128 v[244:247], v8 offset:12288
	v_mov_b32_e32 v17, v16
	v_mfma_f32_16x16x32_f16 v[48:51], a[64:67], v[144:147], v[48:51]
	ds_read_b128 v[248:251], v7 offset:14336
	v_mfma_f32_16x16x32_f16 v[52:55], a[68:71], v[144:147], v[52:55]
	ds_read_b128 v[252:255], v8 offset:14336
	v_mov_b32_e32 v18, v16
	v_mfma_f32_16x16x32_f16 v[56:59], a[72:75], v[144:147], v[56:59]
	s_nop 0
	v_permlane16_swap_b32_e32 v17, v18
	v_mfma_f32_16x16x32_f16 v[60:63], a[76:79], v[144:147], v[60:63]
	v_max_f32_e32 v16, v17, v18
	v_mfma_f32_16x16x32_f16 v[48:51], a[80:83], v[148:151], v[48:51]
	v_rcp_f32_e32 v19, v16
	v_mfma_f32_16x16x32_f16 v[52:55], a[84:87], v[148:151], v[52:55]
	v_cmp_lt_f32_e32 vcc, 0, v16
	v_mfma_f32_16x16x32_f16 v[56:59], a[88:91], v[148:151], v[56:59]
	s_mov_b32 m0, s28
	s_add_u32 s28, s28, 0x4000
	s_cmp_ge_u32 s28, s46
	s_cselect_b32 s28, s47, s28
	global_load_lds_dwordx4 v9, s[26:27]
	v_mul_f32_e32 v19, 0x42fe0000, v19
	v_mfma_f32_16x16x32_f16 v[60:63], a[92:95], v[148:151], v[60:63]
	v_mul_f32_e32 v20, 0x3c010204, v16
	v_mfma_f32_16x16x32_f16 v[48:51], a[96:99], v[152:155], v[48:51]
	v_cndmask_b32_e32 v19, 0, v19, vcc
	v_mfma_f32_16x16x32_f16 v[52:55], a[100:103], v[152:155], v[52:55]
	v_cndmask_b32_e32 v20, 1.0, v20, vcc
	v_mfma_f32_16x16x32_f16 v[56:59], a[104:107], v[152:155], v[56:59]
	v_fmaak_f32 v96, v19, v64, 0x4b400000
	v_mfma_f32_16x16x32_f16 v[60:63], a[108:111], v[152:155], v[60:63]
	v_fmaak_f32 v97, v19, v65, 0x4b400000
	v_mfma_f32_16x16x32_f16 v[48:51], a[112:115], v[156:159], v[48:51]
	v_fmaak_f32 v98, v19, v66, 0x4b400000
	v_mfma_f32_16x16x32_f16 v[52:55], a[116:119], v[156:159], v[52:55]
	v_fmaak_f32 v99, v19, v67, 0x4b400000
	v_mfma_f32_16x16x32_f16 v[56:59], a[120:123], v[156:159], v[56:59]
	v_mfma_f32_16x16x32_f16 v[60:63], a[124:127], v[156:159], v[60:63]
	v_fmaak_f32 v100, v19, v68, 0x4b400000
	v_mfma_f32_16x16x32_f16 v[48:51], a[128:131], v[160:163], v[48:51]
	v_fmaak_f32 v101, v19, v69, 0x4b400000
	v_mfma_f32_16x16x32_f16 v[52:55], a[132:135], v[160:163], v[52:55]
	global_load_lds_dwordx4 v9, s[26:27] offset:1024
	v_fmaak_f32 v102, v19, v70, 0x4b400000
	v_mfma_f32_16x16x32_f16 v[56:59], a[136:139], v[160:163], v[56:59]
	v_fmaak_f32 v103, v19, v71, 0x4b400000
	v_mfma_f32_16x16x32_f16 v[60:63], a[140:143], v[160:163], v[60:63]
	v_fmaak_f32 v104, v19, v72, 0x4b400000
	v_mfma_f32_16x16x32_f16 v[48:51], a[144:147], v[164:167], v[48:51]
	v_fmaak_f32 v105, v19, v73, 0x4b400000
	v_mfma_f32_16x16x32_f16 v[52:55], a[148:151], v[164:167], v[52:55]
	v_fmaak_f32 v106, v19, v74, 0x4b400000
	v_mfma_f32_16x16x32_f16 v[56:59], a[152:155], v[164:167], v[56:59]
	v_fmaak_f32 v107, v19, v75, 0x4b400000
	v_mfma_f32_16x16x32_f16 v[60:63], a[156:159], v[164:167], v[60:63]
	v_fmaak_f32 v108, v19, v76, 0x4b400000
	v_mfma_f32_16x16x32_f16 v[48:51], a[160:163], v[168:171], v[48:51]
	v_fmaak_f32 v109, v19, v77, 0x4b400000
	v_mfma_f32_16x16x32_f16 v[52:55], a[164:167], v[168:171], v[52:55]
	v_fmaak_f32 v110, v19, v78, 0x4b400000
	v_mfma_f32_16x16x32_f16 v[56:59], a[168:171], v[168:171], v[56:59]
	v_fmaak_f32 v111, v19, v79, 0x4b400000
	v_mfma_f32_16x16x32_f16 v[60:63], a[172:175], v[168:171], v[60:63]
	v_perm_b32 v21, v97, v96, s44
	v_mfma_f32_16x16x32_f16 v[48:51], a[176:179], v[172:175], v[48:51]
	s_add_u32 m0, m0, 0x800
	s_nop 0
	global_load_lds_dwordx4 v10, s[26:27]
	v_mfma_f32_16x16x32_f16 v[52:55], a[180:183], v[172:175], v[52:55]
	v_perm_b32 v22, v99, v98, s44
	v_mfma_f32_16x16x32_f16 v[56:59], a[184:187], v[172:175], v[56:59]
	v_perm_b32 v23, v101, v100, s44
	v_mfma_f32_16x16x32_f16 v[60:63], a[188:191], v[172:175], v[60:63]
	v_perm_b32 v24, v103, v102, s44
	v_mfma_f32_16x16x32_f16 v[48:51], a[192:195], v[176:179], v[48:51]
	v_perm_b32 v25, v105, v104, s44
	v_mfma_f32_16x16x32_f16 v[52:55], a[196:199], v[176:179], v[52:55]
	v_perm_b32 v26, v107, v106, s44
	v_mfma_f32_16x16x32_f16 v[56:59], a[200:203], v[176:179], v[56:59]
	v_perm_b32 v27, v109, v108, s44
	v_mfma_f32_16x16x32_f16 v[60:63], a[204:207], v[176:179], v[60:63]
	v_perm_b32 v28, v111, v110, s44
	v_mfma_f32_16x16x32_f16 v[48:51], a[208:211], v[180:183], v[48:51]
	v_perm_b32 v96, v22, v21, s45
	v_mfma_f32_16x16x32_f16 v[52:55], a[212:215], v[180:183], v[52:55]
	v_perm_b32 v97, v24, v23, s45
	v_mfma_f32_16x16x32_f16 v[56:59], a[216:219], v[180:183], v[56:59]
	v_perm_b32 v98, v26, v25, s45
	v_mfma_f32_16x16x32_f16 v[60:63], a[220:223], v[180:183], v[60:63]
	v_perm_b32 v99, v28, v27, s45
	v_mfma_f32_16x16x32_f16 v[48:51], a[224:227], v[184:187], v[48:51]
	global_load_lds_dwordx4 v10, s[26:27] offset:1024
	global_store_dwordx4 v14, v[96:99], s[30:31]
	v_mfma_f32_16x16x32_f16 v[52:55], a[228:231], v[184:187], v[52:55]
	s_add_u32 s26, s26, 0x800
	s_addc_u32 s27, s27, 0
	global_store_dword v112, v20, s[30:31]
	v_mfma_f32_16x16x32_f16 v[56:59], a[232:235], v[184:187], v[56:59]
	v_mfma_f32_16x16x32_f16 v[60:63], a[236:239], v[184:187], v[60:63]
	s_add_u32 s30, s30, 0x8800
	s_addc_u32 s31, s31, 0
	v_mfma_f32_16x16x32_f16 v[48:51], a[240:243], v[188:191], v[48:51]
	v_mfma_f32_16x16x32_f16 v[52:55], a[244:247], v[188:191], v[52:55]
	v_mfma_f32_16x16x32_f16 v[56:59], a[248:251], v[188:191], v[56:59]
	v_mfma_f32_16x16x32_f16 v[60:63], a[252:255], v[188:191], v[60:63]
	s_sub_u32 s24, s24, 1
	s_cmp_le_u32 s24, 1
	s_cbranch_scc0 LgAq_loop
	s_nop 7
	s_nop 7
	v_max3_f32 v16, |v48|, 0, |v49|
	v_max3_f32 v16, v16, |v50|, |v51|
	v_max3_f32 v16, v16, |v52|, |v53|
	v_max3_f32 v16, v16, |v54|, |v55|
	v_max3_f32 v16, v16, |v56|, |v57|
	v_max3_f32 v16, v16, |v58|, |v59|
	v_max3_f32 v16, v16, |v60|, |v61|
	v_max3_f32 v16, v16, |v62|, |v63|
	v_mov_b32_e32 v17, v16
	v_mov_b32_e32 v18, v16
	s_nop 1
	v_permlane32_swap_b32_e32 v17, v18
	v_max_f32_e32 v16, v17, v18
	v_mov_b32_e32 v17, v16
	v_mov_b32_e32 v18, v16
	s_nop 1
	v_permlane16_swap_b32_e32 v17, v18
	v_max_f32_e32 v16, v17, v18
	v_rcp_f32_e32 v19, v16
	v_cmp_lt_f32_e32 vcc, 0, v16
	v_mul_f32_e32 v19, 0x42fe0000, v19
	v_mul_f32_e32 v20, 0x3c010204, v16
	v_cndmask_b32_e32 v19, 0, v19, vcc
	v_cndmask_b32_e32 v20, 1.0, v20, vcc
	v_fmaak_f32 v96, v19, v48, 0x4b400000
	v_fmaak_f32 v97, v19, v49, 0x4b400000
	v_fmaak_f32 v98, v19, v50, 0x4b400000
	v_fmaak_f32 v99, v19, v51, 0x4b400000
	v_fmaak_f32 v100, v19, v52, 0x4b400000
	v_fmaak_f32 v101, v19, v53, 0x4b400000
	v_fmaak_f32 v102, v19, v54, 0x4b400000
	v_fmaak_f32 v103, v19, v55, 0x4b400000
	v_fmaak_f32 v104, v19, v56, 0x4b400000
	v_fmaak_f32 v105, v19, v57, 0x4b400000
	v_fmaak_f32 v106, v19, v58, 0x4b400000
	v_fmaak_f32 v107, v19, v59, 0x4b400000
	v_fmaak_f32 v108, v19, v60, 0x4b400000
	v_fmaak_f32 v109, v19, v61, 0x4b400000
	v_fmaak_f32 v110, v19, v62, 0x4b400000
	v_fmaak_f32 v111, v19, v63, 0x4b400000
	v_perm_b32 v21, v97, v96, s44
	v_perm_b32 v22, v99, v98, s44
	v_perm_b32 v23, v101, v100, s44
	v_perm_b32 v24, v103, v102, s44
	v_perm_b32 v25, v105, v104, s44
	v_perm_b32 v26, v107, v106, s44
	v_perm_b32 v27, v109, v108, s44
	v_perm_b32 v28, v111, v110, s44
	v_perm_b32 v96, v22, v21, s45
	v_perm_b32 v97, v24, v23, s45
	v_perm_b32 v98, v26, v25, s45
	v_perm_b32 v99, v28, v27, s45
	global_store_dwordx4 v14, v[96:99], s[30:31]
	global_store_dword v112, v20, s[30:31]
	s_add_u32 s30, s30, 0x8800
	s_addc_u32 s31, s31, 0
	s_endpgm

LgAs_loop:
	s_waitcnt vmcnt(8) lgkmcnt(0)
	s_barrier
	v_mfma_f32_16x16x32_f16 v[64:67], a[0:3], v[192:195], v[32:35]
	global_load_dwordx4 v[88:91], v15, s[32:33]
	global_load_dwordx4 v[92:95], v15, s[32:33] offset:16
	s_add_u32 s32, s32, 0x800
	s_addc_u32 s33, s33, 0
	v_mfma_f32_16x16x32_f16 v[68:71], a[4:7], v[192:195], v[36:39]
	v_add_u32_e32 v5, s29, v4
	v_xor_b32_e32 v6, 64, v5
	s_add_u32 s29, s29, 0x4000
	s_cmp_ge_u32 s29, 0x14000
	s_cselect_b32 s29, 0, s29
	v_mfma_f32_16x16x32_f16 v[72:75], a[8:11], v[192:195], v[40:43]
	ds_read_b128 v[128:131], v5 offset:0
	v_mfma_f32_16x16x32_f16 v[76:79], a[12:15], v[192:195], v[44:47]
	ds_read_b128 v[132:135], v6 offset:0
	s_waitcnt vmcnt(6)
	v_mfma_f32_16x16x32_f16 v[64:67], a[16:19], v[196:199], v[64:67]
	ds_read_b128 v[136:139], v5 offset:2048
	v_cvt_f32_f16_e32 v96, v80
	v_mfma_f32_16x16x32_f16 v[68:71], a[20:23], v[196:199], v[68:71]
	ds_read_b128 v[140:143], v6 offset:2048
	v_cvt_f32_f16_sdwa v97, v80 dst_sel:DWORD dst_unused:UNUSED_PAD src0_sel:WORD_1
	v_mfma_f32_16x16x32_f16 v[72:75], a[24:27], v[196:199], v[72:75]
	ds_read_b128 v[144:147], v5 offset:4096
	v_cvt_f32_f16_e32 v98, v81
	v_mfma_f32_16x16x32_f16 v[76:79], a[28:31], v[196:199], v[76:79]
	ds_read_b128 v[148:151], v6 offset:4096
	v_mfma_f32_16x16x32_f16 v[64:67], a[32:35], v[200:203], v[64:67]
	ds_read_b128 v[152:155], v5 offset:6144
	v_cvt_f32_f16_sdwa v99, v81 dst_sel:DWORD dst_unused:UNUSED_PAD src0_sel:WORD_1
	v_mfma_f32_16x16x32_f16 v[68:71], a[36:39], v[200:203], v[68:71]
	ds_read_b128 v[156:159], v6 offset:6144
	v_cvt_f32_f16_e32 v100, v82
	v_mfma_f32_16x16x32_f16 v[72:75], a[40:43], v[200:203], v[72:75]
	ds_read_b128 v[160:163], v5 offset:8192
	v_cvt_f32_f16_sdwa v101, v82 dst_sel:DWORD dst_unused:UNUSED_PAD src0_sel:WORD_1
	v_mfma_f32_16x16x32_f16 v[76:79], a[44:47], v[200:203], v[76:79]
	ds_read_b128 v[164:167], v6 offset:8192
	v_mfma_f32_16x16x32_f16 v[64:67], a[48:51], v[204:207], v[64:67]
	ds_read_b128 v[168:171], v5 offset:10240
	v_cvt_f32_f16_e32 v102, v83
	v_mfma_f32_16x16x32_f16 v[68:71], a[52:55], v[204:207], v[68:71]
	ds_read_b128 v[172:175], v6 offset:10240
	v_cvt_f32_f16_sdwa v103, v83 dst_sel:DWORD dst_unused:UNUSED_PAD src0_sel:WORD_1
	v_mfma_f32_16x16x32_f16 v[72:75], a[56:59], v[204:207], v[72:75]
	ds_read_b128 v[176:179], v5 offset:12288
	v_cvt_f32_f16_e32 v104, v84
	v_mfma_f32_16x16x32_f16 v[76:79], a[60:63], v[204:207], v[76:79]
	ds_read_b128 v[180:183], v6 offset:12288
	v_mfma_f32_16x16x32_f16 v[64:67], a[64:67], v[208:211], v[64:67]
	ds_read_b128 v[184:187], v5 offset:14336
	v_cvt_f32_f16_sdwa v105, v84 dst_sel:DWORD dst_unused:UNUSED_PAD src0_sel:WORD_1
	v_mfma_f32_16x16x32_f16 v[68:71], a[68:71], v[208:211], v[68:71]
	ds_read_b128 v[188:191], v6 offset:14336
	v_cvt_f32_f16_e32 v106, v85
	v_mfma_f32_16x16x32_f16 v[72:75], a[72:75], v[208:211], v[72:75]
	v_cvt_f32_f16_sdwa v107, v85 dst_sel:DWORD dst_unused:UNUSED_PAD src0_sel:WORD_1
	v_mfma_f32_16x16x32_f16 v[76:79], a[76:79], v[208:211], v[76:79]
	v_cvt_f32_f16_e32 v108, v86
	v_mfma_f32_16x16x32_f16 v[64:67], a[80:83], v[212:215], v[64:67]
	v_mfma_f32_16x16x32_f16 v[68:71], a[84:87], v[212:215], v[68:71]
	v_cvt_f32_f16_sdwa v109, v86 dst_sel:DWORD dst_unused:UNUSED_PAD src0_sel:WORD_1
	v_mfma_f32_16x16x32_f16 v[72:75], a[88:91], v[212:215], v[72:75]
	s_mov_b32 m0, s28
	s_add_u32 s28, s28, 0x4000
	s_cmp_ge_u32 s28, s46
	s_cselect_b32 s28, s47, s28
	global_load_lds_dwordx4 v9, s[26:27]
	v_cvt_f32_f16_e32 v110, v87
	v_mfma_f32_16x16x32_f16 v[76:79], a[92:95], v[212:215], v[76:79]
	v_cvt_f32_f16_sdwa v111, v87 dst_sel:DWORD dst_unused:UNUSED_PAD src0_sel:WORD_1
	v_mfma_f32_16x16x32_f16 v[64:67], a[96:99], v[216:219], v[64:67]
	v_mfma_f32_16x16x32_f16 v[68:71], a[100:103], v[216:219], v[68:71]
	v_add_f32_e32 v96, v96, v48
	v_mfma_f32_16x16x32_f16 v[72:75], a[104:107], v[216:219], v[72:75]
	v_add_f32_e32 v97, v97, v49
	v_mfma_f32_16x16x32_f16 v[76:79], a[108:111], v[216:219], v[76:79]
	v_add_f32_e32 v98, v98, v50
	v_mfma_f32_16x16x32_f16 v[64:67], a[112:115], v[220:223], v[64:67]
	v_mfma_f32_16x16x32_f16 v[68:71], a[116:119], v[220:223], v[68:71]
	v_add_f32_e32 v99, v99, v51
	v_mfma_f32_16x16x32_f16 v[72:75], a[120:123], v[220:223], v[72:75]
	v_add_f32_e32 v100, v100, v52
	v_mfma_f32_16x16x32_f16 v[76:79], a[124:127], v[220:223], v[76:79]
	v_add_f32_e32 v101, v101, v53
	v_mfma_f32_16x16x32_f16 v[64:67], a[128:131], v[224:227], v[64:67]
	v_add_f32_e32 v102, v102, v54
	v_mfma_f32_16x16x32_f16 v[68:71], a[132:135], v[224:227], v[68:71]
	global_load_lds_dwordx4 v9, s[26:27] offset:1024
	v_mfma_f32_16x16x32_f16 v[72:75], a[136:139], v[224:227], v[72:75]
	v_add_f32_e32 v103, v103, v55
	v_mfma_f32_16x16x32_f16 v[76:79], a[140:143], v[224:227], v[76:79]
	v_add_f32_e32 v104, v104, v56
	v_mfma_f32_16x16x32_f16 v[64:67], a[144:147], v[228:231], v[64:67]
	v_add_f32_e32 v105, v105, v57
	v_mfma_f32_16x16x32_f16 v[68:71], a[148:151], v[228:231], v[68:71]
	v_mfma_f32_16x16x32_f16 v[72:75], a[152:155], v[228:231], v[72:75]
	v_add_f32_e32 v106, v106, v58
	v_mfma_f32_16x16x32_f16 v[76:79], a[156:159], v[228:231], v[76:79]
	v_add_f32_e32 v107, v107, v59
	v_mfma_f32_16x16x32_f16 v[64:67], a[160:163], v[232:235], v[64:67]
	v_add_f32_e32 v108, v108, v60
	v_mfma_f32_16x16x32_f16 v[68:71], a[164:167], v[232:235], v[68:71]
	v_mfma_f32_16x16x32_f16 v[72:75], a[168:171], v[232:235], v[72:75]
	v_add_f32_e32 v109, v109, v61
	v_mfma_f32_16x16x32_f16 v[76:79], a[172:175], v[232:235], v[76:79]
	v_add_f32_e32 v110, v110, v62
	v_mfma_f32_16x16x32_f16 v[64:67], a[176:179], v[236:239], v[64:67]
	s_add_u32 m0, m0, 0x800
	s_nop 0
	global_load_lds_dwordx4 v10, s[26:27]
	v_add_f32_e32 v111, v111, v63
	v_mfma_f32_16x16x32_f16 v[68:71], a[180:183], v[236:239], v[68:71]
	v_cvt_pk_f16_f32 v16, v96, v97
	v_mfma_f32_16x16x32_f16 v[72:75], a[184:187], v[236:239], v[72:75]
	v_mfma_f32_16x16x32_f16 v[76:79], a[188:191], v[236:239], v[76:79]
	v_cvt_pk_f16_f32 v17, v98, v99
	v_mfma_f32_16x16x32_f16 v[64:67], a[192:195], v[240:243], v[64:67]
	v_cvt_pk_f16_f32 v18, v100, v101
	v_mfma_f32_16x16x32_f16 v[68:71], a[196:199], v[240:243], v[68:71]
	v_cvt_pk_f16_f32 v19, v102, v103
	v_mfma_f32_16x16x32_f16 v[72:75], a[200:203], v[240:243], v[72:75]
	v_mfma_f32_16x16x32_f16 v[76:79], a[204:207], v[240:243], v[76:79]
	v_cvt_pk_f16_f32 v20, v104, v105
	v_mfma_f32_16x16x32_f16 v[64:67], a[208:211], v[244:247], v[64:67]
	v_cvt_pk_f16_f32 v21, v106, v107
	v_mfma_f32_16x16x32_f16 v[68:71], a[212:215], v[244:247], v[68:71]
	v_cvt_pk_f16_f32 v22, v108, v109
	v_mfma_f32_16x16x32_f16 v[72:75], a[216:219], v[244:247], v[72:75]
	v_mfma_f32_16x16x32_f16 v[76:79], a[220:223], v[244:247], v[76:79]
	v_cvt_pk_f16_f32 v23, v110, v111
	v_mfma_f32_16x16x32_f16 v[64:67], a[224:227], v[248:251], v[64:67]
	global_load_lds_dwordx4 v10, s[26:27] offset:1024
	global_store_dwordx4 v14, v[16:19], s[30:31]
	v_mfma_f32_16x16x32_f16 v[68:71], a[228:231], v[248:251], v[68:71]
	s_add_u32 s26, s26, 0x800
	s_addc_u32 s27, s27, 0
	global_store_dwordx4 v14, v[20:23], s[30:31] offset:16
	v_mfma_f32_16x16x32_f16 v[72:75], a[232:235], v[248:251], v[72:75]
	v_mfma_f32_16x16x32_f16 v[76:79], a[236:239], v[248:251], v[76:79]
	s_add_u32 s30, s30, 0x4000
	s_addc_u32 s31, s31, 0
	v_mfma_f32_16x16x32_f16 v[64:67], a[240:243], v[252:255], v[64:67]
	v_mfma_f32_16x16x32_f16 v[68:71], a[244:247], v[252:255], v[68:71]
	v_mfma_f32_16x16x32_f16 v[72:75], a[248:251], v[252:255], v[72:75]
	v_mfma_f32_16x16x32_f16 v[76:79], a[252:255], v[252:255], v[76:79]
	s_sub_u32 s24, s24, 1
	s_cmp_le_u32 s24, 1
	s_cbranch_scc1 LgAs_exitA
	s_waitcnt vmcnt(8) lgkmcnt(0)
	s_barrier
	v_mfma_f32_16x16x32_f16 v[48:51], a[0:3], v[128:131], v[32:35]
	global_load_dwordx4 v[80:83], v15, s[32:33]
	global_load_dwordx4 v[84:87], v15, s[32:33] offset:16
	s_add_u32 s32, s32, 0x800
	s_addc_u32 s33, s33, 0
	v_mfma_f32_16x16x32_f16 v[52:55], a[4:7], v[128:131], v[36:39]
	v_add_u32_e32 v7, s29, v4
	v_xor_b32_e32 v8, 64, v7
	s_add_u32 s29, s29, 0x4000
	s_cmp_ge_u32 s29, 0x14000
	s_cselect_b32 s29, 0, s29
	v_mfma_f32_16x16x32_f16 v[56:59], a[8:11], v[128:131], v[40:43]
	ds_read_b128 v[192:195], v7 offset:0
	v_mfma_f32_16x16x32_f16 v[60:63], a[12:15], v[128:131], v[44:47]
	ds_read_b128 v[196:199], v8 offset:0
	s_waitcnt vmcnt(6)
	v_mfma_f32_16x16x32_f16 v[48:51], a[16:19], v[132:135], v[48:51]
	ds_read_b128 v[200:203], v7 offset:2048
	v_cvt_f32_f16_e32 v96, v88
	v_mfma_f32_16x16x32_f16 v[52:55], a[20:23], v[132:135], v[52:55]
	ds_read_b128 v[204:207], v8 offset:2048
	v_cvt_f32_f16_sdwa v97, v88 dst_sel:DWORD dst_unused:UNUSED_PAD src0_sel:WORD_1
	v_mfma_f32_16x16x32_f16 v[56:59], a[24:27], v[132:135], v[56:59]
	ds_read_b128 v[208:211], v7 offset:4096
	v_cvt_f32_f16_e32 v98, v89
	v_mfma_f32_16x16x32_f16 v[60:63], a[28:31], v[132:135], v[60:63]
	ds_read_b128 v[212:215], v8 offset:4096
	v_mfma_f32_16x16x32_f16 v[48:51], a[32:35], v[136:139], v[48:51]
	ds_read_b128 v[216:219], v7 offset:6144
	v_cvt_f32_f16_sdwa v99, v89 dst_sel:DWORD dst_unused:UNUSED_PAD src0_sel:WORD_1
	v_mfma_f32_16x16x32_f16 v[52:55], a[36:39], v[136:139], v[52:55]
	ds_read_b128 v[220:223], v8 offset:6144
	v_cvt_f32_f16_e32 v100, v90
	v_mfma_f32_16x16x32_f16 v[56:59], a[40:43], v[136:139], v[56:59]
	ds_read_b128 v[224:227], v7 offset:8192
	v_cvt_f32_f16_sdwa v101, v90 dst_sel:DWORD dst_unused:UNUSED_PAD src0_sel:WORD_1
	v_mfma_f32_16x16x32_f16 v[60:63], a[44:47], v[136:139], v[60:63]
	ds_read_b128 v[228:231], v8 offset:8192
	v_mfma_f32_16x16x32_f16 v[48:51], a[48:51], v[140:143], v[48:51]
	ds_read_b128 v[232:235], v7 offset:10240
	v_cvt_f32_f16_e32 v102, v91
	v_mfma_f32_16x16x32_f16 v[52:55], a[52:55], v[140:143], v[52:55]
	ds_read_b128 v[236:239], v8 offset:10240
	v_cvt_f32_f16_sdwa v103, v91 dst_sel:DWORD dst_unused:UNUSED_PAD src0_sel:WORD_1
	v_mfma_f32_16x16x32_f16 v[56:59], a[56:59], v[140:143], v[56:59]
	ds_read_b128 v[240:243], v7 offset:12288
	v_cvt_f32_f16_e32 v104, v92
	v_mfma_f32_16x16x32_f16 v[60:63], a[60:63], v[140:143], v[60:63]
	ds_read_b128 v[244:247], v8 offset:12288
	v_mfma_f32_16x16x32_f16 v[48:51], a[64:67], v[144:147], v[48:51]
	ds_read_b128 v[248:251], v7 offset:14336
	v_cvt_f32_f16_sdwa v105, v92 dst_sel:DWORD dst_unused:UNUSED_PAD src0_sel:WORD_1
	v_mfma_f32_16x16x32_f16 v[52:55], a[68:71], v[144:147], v[52:55]
	ds_read_b128 v[252:255], v8 offset:14336
	v_cvt_f32_f16_e32 v106, v93
	v_mfma_f32_16x16x32_f16 v[56:59], a[72:75], v[144:147], v[56:59]
	v_cvt_f32_f16_sdwa v107, v93 dst_sel:DWORD dst_unused:UNUSED_PAD src0_sel:WORD_1
	v_mfma_f32_16x16x32_f16 v[60:63], a[76:79], v[144:147], v[60:63]
	v_cvt_f32_f16_e32 v108, v94
	v_mfma_f32_16x16x32_f16 v[48:51], a[80:83], v[148:151], v[48:51]
	v_mfma_f32_16x16x32_f16 v[52:55], a[84:87], v[148:151], v[52:55]
	v_cvt_f32_f16_sdwa v109, v94 dst_sel:DWORD dst_unused:UNUSED_PAD src0_sel:WORD_1
	v_mfma_f32_16x16x32_f16 v[56:59], a[88:91], v[148:151], v[56:59]
	s_mov_b32 m0, s28
	s_add_u32 s28, s28, 0x4000
	s_cmp_ge_u32 s28, s46
	s_cselect_b32 s28, s47, s28
	global_load_lds_dwordx4 v9, s[26:27]
	v_cvt_f32_f16_e32 v110, v95
	v_mfma_f32_16x16x32_f16 v[60:63], a[92:95], v[148:151], v[60:63]
	v_cvt_f32_f16_sdwa v111, v95 dst_sel:DWORD dst_unused:UNUSED_PAD src0_sel:WORD_1
	v_mfma_f32_16x16x32_f16 v[48:51], a[96:99], v[152:155], v[48:51]
	v_mfma_f32_16x16x32_f16 v[52:55], a[100:103], v[152:155], v[52:55]
	v_add_f32_e32 v96, v96, v64
	v_mfma_f32_16x16x32_f16 v[56:59], a[104:107], v[152:155], v[56:59]
	v_add_f32_e32 v97, v97, v65
	v_mfma_f32_16x16x32_f16 v[60:63], a[108:111], v[152:155], v[60:63]
	v_add_f32_e32 v98, v98, v66
	v_mfma_f32_16x16x32_f16 v[48:51], a[112:115], v[156:159], v[48:51]
	v_mfma_f32_16x16x32_f16 v[52:55], a[116:119], v[156:159], v[52:55]
	v_add_f32_e32 v99, v99, v67
	v_mfma_f32_16x16x32_f16 v[56:59], a[120:123], v[156:159], v[56:59]
	v_add_f32_e32 v100, v100, v68
	v_mfma_f32_16x16x32_f16 v[60:63], a[124:127], v[156:159], v[60:63]
	v_add_f32_e32 v101, v101, v69
	v_mfma_f32_16x16x32_f16 v[48:51], a[128:131], v[160:163], v[48:51]
	v_add_f32_e32 v102, v102, v70
	v_mfma_f32_16x16x32_f16 v[52:55], a[132:135], v[160:163], v[52:55]
	global_load_lds_dwordx4 v9, s[26:27] offset:1024
	v_mfma_f32_16x16x32_f16 v[56:59], a[136:139], v[160:163], v[56:59]
	v_add_f32_e32 v103, v103, v71
	v_mfma_f32_16x16x32_f16 v[60:63], a[140:143], v[160:163], v[60:63]
	v_add_f32_e32 v104, v104, v72
	v_mfma_f32_16x16x32_f16 v[48:51], a[144:147], v[164:167], v[48:51]
	v_add_f32_e32 v105, v105, v73
	v_mfma_f32_16x16x32_f16 v[52:55], a[148:151], v[164:167], v[52:55]
	v_mfma_f32_16x16x32_f16 v[56:59], a[152:155], v[164:167], v[56:59]
	v_add_f32_e32 v106, v106, v74
	v_mfma_f32_16x16x32_f16 v[60:63], a[156:159], v[164:167], v[60:63]
	v_add_f32_e32 v107, v107, v75
	v_mfma_f32_16x16x32_f16 v[48:51], a[160:163], v[168:171], v[48:51]
	v_add_f32_e32 v108, v108, v76
	v_mfma_f32_16x16x32_f16 v[52:55], a[164:167], v[168:171], v[52:55]
	v_mfma_f32_16x16x32_f16 v[56:59], a[168:171], v[168:171], v[56:59]
	v_add_f32_e32 v109, v109, v77
	v_mfma_f32_16x16x32_f16 v[60:63], a[172:175], v[168:171], v[60:63]
	v_add_f32_e32 v110, v110, v78
	v_mfma_f32_16x16x32_f16 v[48:51], a[176:179], v[172:175], v[48:51]
	s_add_u32 m0, m0, 0x800
	s_nop 0
	global_load_lds_dwordx4 v10, s[26:27]
	v_add_f32_e32 v111, v111, v79
	v_mfma_f32_16x16x32_f16 v[52:55], a[180:183], v[172:175], v[52:55]
	v_cvt_pk_f16_f32 v16, v96, v97
	v_mfma_f32_16x16x32_f16 v[56:59], a[184:187], v[172:175], v[56:59]
	v_mfma_f32_16x16x32_f16 v[60:63], a[188:191], v[172:175], v[60:63]
	v_cvt_pk_f16_f32 v17, v98, v99
	v_mfma_f32_16x16x32_f16 v[48:51], a[192:195], v[176:179], v[48:51]
	v_cvt_pk_f16_f32 v18, v100, v101
	v_mfma_f32_16x16x32_f16 v[52:55], a[196:199], v[176:179], v[52:55]
	v_cvt_pk_f16_f32 v19, v102, v103
	v_mfma_f32_16x16x32_f16 v[56:59], a[200:203], v[176:179], v[56:59]
	v_mfma_f32_16x16x32_f16 v[60:63], a[204:207], v[176:179], v[60:63]
	v_cvt_pk_f16_f32 v20, v104, v105
	v_mfma_f32_16x16x32_f16 v[48:51], a[208:211], v[180:183], v[48:51]
	v_cvt_pk_f16_f32 v21, v106, v107
	v_mfma_f32_16x16x32_f16 v[52:55], a[212:215], v[180:183], v[52:55]
	v_cvt_pk_f16_f32 v22, v108, v109
	v_mfma_f32_16x16x32_f16 v[56:59], a[216:219], v[180:183], v[56:59]
	v_mfma_f32_16x16x32_f16 v[60:63], a[220:223], v[180:183], v[60:63]
	v_cvt_pk_f16_f32 v23, v110, v111
	v_mfma_f32_16x16x32_f16 v[48:51], a[224:227], v[184:187], v[48:51]
	global_load_lds_dwordx4 v10, s[26:27] offset:1024
	global_store_dwordx4 v14, v[16:19], s[30:31]
	v_mfma_f32_16x16x32_f16 v[52:55], a[228:231], v[184:187], v[52:55]
	s_add_u32 s26, s26, 0x800
	s_addc_u32 s27, s27, 0
	global_store_dwordx4 v14, v[20:23], s[30:31] offset:16
	v_mfma_f32_16x16x32_f16 v[56:59], a[232:235], v[184:187], v[56:59]
	v_mfma_f32_16x16x32_f16 v[60:63], a[236:239], v[184:187], v[60:63]
	s_add_u32 s30, s30, 0x4000
	s_addc_u32 s31, s31, 0
	v_mfma_f32_16x16x32_f16 v[48:51], a[240:243], v[188:191], v[48:51]
	v_mfma_f32_16x16x32_f16 v[52:55], a[244:247], v[188:191], v[52:55]
	v_mfma_f32_16x16x32_f16 v[56:59], a[248:251], v[188:191], v[56:59]
	v_mfma_f32_16x16x32_f16 v[60:63], a[252:255], v[188:191], v[60:63]
	s_sub_u32 s24, s24, 1
	s_cmp_le_u32 s24, 1
	s_cbranch_scc0 LgAs_loop
	s_nop 7
	s_nop 7
	s_waitcnt vmcnt(0)
	v_cvt_f32_f16_e32 v96, v80
	v_cvt_f32_f16_sdwa v97, v80 dst_sel:DWORD dst_unused:UNUSED_PAD src0_sel:WORD_1
	v_cvt_f32_f16_e32 v98, v81
	v_cvt_f32_f16_sdwa v99, v81 dst_sel:DWORD dst_unused:UNUSED_PAD src0_sel:WORD_1
	v_cvt_f32_f16_e32 v100, v82
	v_cvt_f32_f16_sdwa v101, v82 dst_sel:DWORD dst_unused:UNUSED_PAD src0_sel:WORD_1
	v_cvt_f32_f16_e32 v102, v83
	v_cvt_f32_f16_sdwa v103, v83 dst_sel:DWORD dst_unused:UNUSED_PAD src0_sel:WORD_1
	v_cvt_f32_f16_e32 v104, v84
	v_cvt_f32_f16_sdwa v105, v84 dst_sel:DWORD dst_unused:UNUSED_PAD src0_sel:WORD_1
	v_cvt_f32_f16_e32 v106, v85
	v_cvt_f32_f16_sdwa v107, v85 dst_sel:DWORD dst_unused:UNUSED_PAD src0_sel:WORD_1
	v_cvt_f32_f16_e32 v108, v86
	v_cvt_f32_f16_sdwa v109, v86 dst_sel:DWORD dst_unused:UNUSED_PAD src0_sel:WORD_1
	v_cvt_f32_f16_e32 v110, v87
	v_cvt_f32_f16_sdwa v111, v87 dst_sel:DWORD dst_unused:UNUSED_PAD src0_sel:WORD_1
	v_add_f32_e32 v96, v96, v48
	v_add_f32_e32 v97, v97, v49
	v_add_f32_e32 v98, v98, v50
	v_add_f32_e32 v99, v99, v51
	v_add_f32_e32 v100, v100, v52
	v_add_f32_e32 v101, v101, v53
	v_add_f32_e32 v102, v102, v54
	v_add_f32_e32 v103, v103, v55
	v_add_f32_e32 v104, v104, v56
	v_add_f32_e32 v105, v105, v57
	v_add_f32_e32 v106, v106, v58
	v_add_f32_e32 v107, v107, v59
	v_add_f32_e32 v108, v108, v60
	v_add_f32_e32 v109, v109, v61
	v_add_f32_e32 v110, v110, v62
	v_add_f32_e32 v111, v111, v63
	v_cvt_pk_f16_f32 v16, v96, v97
	v_cvt_pk_f16_f32 v17, v98, v99
	v_cvt_pk_f16_f32 v18, v100, v101
	v_cvt_pk_f16_f32 v19, v102, v103
	v_cvt_pk_f16_f32 v20, v104, v105
	v_cvt_pk_f16_f32 v21, v106, v107
	v_cvt_pk_f16_f32 v22, v108, v109
	v_cvt_pk_f16_f32 v23, v110, v111
	global_store_dwordx4 v14, v[16:19], s[30:31]
	global_store_dwordx4 v14, v[20:23], s[30:31] offset:16
	s_add_u32 s30, s30, 0x4000
	s_addc_u32 s31, s31, 0
	s_endpgm

_Z6gemm_kILi1ELi2ELi2EEvPKDF16_S1_iiiPKfS1_PDF16_PfS4_:
	s_lshr_b32 s37, s2, 3
	s_cmp_lt_u32 s37, 32
	s_cbranch_scc1 Lg1_exit
	s_sub_u32 s37, s37, 32
	s_and_b32 s36, s2, 7
	s_lshr_b32 s38, s37, 2
	s_lshl_b32 s36, s36, 3
	s_add_u32 s22, s36, s38
	s_and_b32 s21, s37, 3
	s_cmp_ge_u32 s22, 63
	s_cbranch_scc1 Lg1_exit
	s_load_dwordx4 s[4:7], s[0:1], 0x0
	s_load_dwordx4 s[8:11], s[0:1], 0x20
	s_load_dwordx4 s[12:15], s[0:1], 0x30
	s_load_dwordx2 s[16:17], s[0:1], 0x40
	v_lshrrev_b32_e32 v20, 6, v0
	v_and_b32_e32 v1, 63, v0
	v_readfirstlane_b32 s20, v20
	v_and_b32_e32 v2, 15, v0
	v_bfe_u32 v3, v0, 4, 2
	v_and_b32_e32 v16, 7, v2
	v_xor_b32_e32 v16, v16, v3
	v_lshlrev_b32_e32 v16, 4, v16
	v_lshl_or_b32 v4, v2, 7, v16
	v_lshrrev_b32_e32 v16, 3, v1
	v_and_b32_e32 v17, 7, v1
	v_xor_b32_e32 v17, v17, v16
	v_lshlrev_b32_e32 v17, 4, v17
	v_lshl_or_b32 v9, v16, 7, v17
	v_add_u32_e32 v10, 0x140000, v9
	s_mul_i32 s23, s22, 10
	s_sub_u32 s24, 625, s23
	s_min_u32 s24, s24, 10
	s_waitcnt lgkmcnt(0)
	s_mul_i32 s36, s20, 0x280000
	s_lshl_b32 s37, s23, 11
	s_add_u32 s36, s36, s37
	s_add_u32 s26, s4, s36
	s_addc_u32 s27, s5, 0
	s_mul_i32 s28, s20, 0x1000
	s_add_u32 s46, s28, 0x14000
	s_mov_b32 s47, s28
	s_mov_b32 s29, 0
	s_lshl_b32 s36, s21, 8
	s_lshl_b32 s37, s20, 6
	s_add_u32 s36, s36, s37
	v_lshlrev_b32_e32 v16, 4, v3
	v_add_u32_e32 v16, s36, v16
	v_lshlrev_b32_e32 v17, 2, v16
	global_load_dwordx4 v[32:35], v17, s[8:9] offset:0
	global_load_dwordx4 v[36:39], v17, s[8:9] offset:16
	global_load_dwordx4 v[40:43], v17, s[8:9] offset:32
	global_load_dwordx4 v[44:47], v17, s[8:9] offset:48
	v_mov_b32_e32 v113, 0x36b49f67
	v_lshlrev_b32_e32 v18, 5, v3
	v_lshl_or_b32 v14, v2, 7, v18
	s_lshl_b32 s38, s21, 2
	s_add_u32 s38, s38, s20
	s_mul_i32 s38, s38, 0x140000
	s_lshl_b32 s39, s23, 11
	s_add_u32 s38, s38, s39
	s_add_u32 s30, s12, s38
	s_addc_u32 s31, s13, 0
	s_mov_b32 m0, s28
	s_add_u32 s28, s28, 0x4000
	s_cmp_ge_u32 s28, s46
	s_cselect_b32 s28, s47, s28
	global_load_lds_dwordx4 v9, s[26:27]
	global_load_lds_dwordx4 v9, s[26:27] offset:1024
	s_add_u32 m0, m0, 0x800
	s_nop 0
	global_load_lds_dwordx4 v10, s[26:27]
	global_load_lds_dwordx4 v10, s[26:27] offset:1024
	s_add_u32 s26, s26, 0x800
	s_addc_u32 s27, s27, 0
	s_mov_b32 m0, s28
	s_add_u32 s28, s28, 0x4000
	s_cmp_ge_u32 s28, s46
	s_cselect_b32 s28, s47, s28
	global_load_lds_dwordx4 v9, s[26:27]
	global_load_lds_dwordx4 v9, s[26:27] offset:1024
	s_add_u32 m0, m0, 0x800
	s_nop 0
	global_load_lds_dwordx4 v10, s[26:27]
	global_load_lds_dwordx4 v10, s[26:27] offset:1024
	s_add_u32 s26, s26, 0x800
	s_addc_u32 s27, s27, 0
	s_lshl_b32 s36, s21, 2
	s_add_u32 s36, s36, s20
	s_mul_i32 s36, s36, 0x10000
	v_lshlrev_b32_e32 v16, 4, v1
	v_add_u32_e32 v13, s36, v16
	global_load_dwordx4 a[0:3], v13, s[6:7] offset:0
	global_load_dwordx4 a[4:7], v13, s[6:7] offset:1024
	global_load_dwordx4 a[8:11], v13, s[6:7] offset:2048
	global_load_dwordx4 a[12:15], v13, s[6:7] offset:3072
	v_add_u32_e32 v13, 0x1000, v13
	global_load_dwordx4 a[16:19], v13, s[6:7] offset:0
	global_load_dwordx4 a[20:23], v13, s[6:7] offset:1024
	global_load_dwordx4 a[24:27], v13, s[6:7] offset:2048
	global_load_dwordx4 a[28:31], v13, s[6:7] offset:3072
	v_add_u32_e32 v13, 0x1000, v13
	global_load_dwordx4 a[32:35], v13, s[6:7] offset:0
	global_load_dwordx4 a[36:39], v13, s[6:7] offset:1024
	global_load_dwordx4 a[40:43], v13, s[6:7] offset:2048
	global_load_dwordx4 a[44:47], v13, s[6:7] offset:3072
	v_add_u32_e32 v13, 0x1000, v13
	global_load_dwordx4 a[48:51], v13, s[6:7] offset:0
	global_load_dwordx4 a[52:55], v13, s[6:7] offset:1024
	global_load_dwordx4 a[56:59], v13, s[6:7] offset:2048
	global_load_dwordx4 a[60:63], v13, s[6:7] offset:3072
	v_add_u32_e32 v13, 0x1000, v13
	global_load_dwordx4 a[64:67], v13, s[6:7] offset:0
	global_load_dwordx4 a[68:71], v13, s[6:7] offset:1024
	global_load_dwordx4 a[72:75], v13, s[6:7] offset:2048
	global_load_dwordx4 a[76:79], v13, s[6:7] offset:3072
	v_add_u32_e32 v13, 0x1000, v13
	global_load_dwordx4 a[80:83], v13, s[6:7] offset:0
	global_load_dwordx4 a[84:87], v13, s[6:7] offset:1024
	global_load_dwordx4 a[88:91], v13, s[6:7] offset:2048
	global_load_dwordx4 a[92:95], v13, s[6:7] offset:3072
	v_add_u32_e32 v13, 0x1000, v13
	global_load_dwordx4 a[96:99], v13, s[6:7] offset:0
	global_load_dwordx4 a[100:103], v13, s[6:7] offset:1024
	global_load_dwordx4 a[104:107], v13, s[6:7] offset:2048
	global_load_dwordx4 a[108:111], v13, s[6:7] offset:3072
	v_add_u32_e32 v13, 0x1000, v13
	global_load_dwordx4 a[112:115], v13, s[6:7] offset:0
	global_load_dwordx4 a[116:119], v13, s[6:7] offset:1024
	global_load_dwordx4 a[120:123], v13, s[6:7] offset:2048
	global_load_dwordx4 a[124:127], v13, s[6:7] offset:3072
	v_add_u32_e32 v13, 0x1000, v13
	global_load_dwordx4 a[128:131], v13, s[6:7] offset:0
	global_load_dwordx4 a[132:135], v13, s[6:7] offset:1024
	global_load_dwordx4 a[136:139], v13, s[6:7] offset:2048
	global_load_dwordx4 a[140:143], v13, s[6:7] offset:3072
	v_add_u32_e32 v13, 0x1000, v13
	global_load_dwordx4 a[144:147], v13, s[6:7] offset:0
	global_load_dwordx4 a[148:151], v13, s[6:7] offset:1024
	global_load_dwordx4 a[152:155], v13, s[6:7] offset:2048
	global_load_dwordx4 a[156:159], v13, s[6:7] offset:3072
	v_add_u32_e32 v13, 0x1000, v13
	global_load_dwordx4 a[160:163], v13, s[6:7] offset:0
	global_load_dwordx4 a[164:167], v13, s[6:7] offset:1024
	global_load_dwordx4 a[168:171], v13, s[6:7] offset:2048
	global_load_dwordx4 a[172:175], v13, s[6:7] offset:3072
	v_add_u32_e32 v13, 0x1000, v13
	global_load_dwordx4 a[176:179], v13, s[6:7] offset:0
	global_load_dwordx4 a[180:183], v13, s[6:7] offset:1024
	global_load_dwordx4 a[184:187], v13, s[6:7] offset:2048
	global_load_dwordx4 a[188:191], v13, s[6:7] offset:3072
	v_add_u32_e32 v13, 0x1000, v13
	global_load_dwordx4 a[192:195], v13, s[6:7] offset:0
	global_load_dwordx4 a[196:199], v13, s[6:7] offset:1024
	global_load_dwordx4 a[200:203], v13, s[6:7] offset:2048
	global_load_dwordx4 a[204:207], v13, s[6:7] offset:3072
	v_add_u32_e32 v13, 0x1000, v13
	global_load_dwordx4 a[208:211], v13, s[6:7] offset:0
	global_load_dwordx4 a[212:215], v13, s[6:7] offset:1024
	global_load_dwordx4 a[216:219], v13, s[6:7] offset:2048
	global_load_dwordx4 a[220:223], v13, s[6:7] offset:3072
	v_add_u32_e32 v13, 0x1000, v13
	global_load_dwordx4 a[224:227], v13, s[6:7] offset:0
	global_load_dwordx4 a[228:231], v13, s[6:7] offset:1024
	global_load_dwordx4 a[232:235], v13, s[6:7] offset:2048
	global_load_dwordx4 a[236:239], v13, s[6:7] offset:3072
	v_add_u32_e32 v13, 0x1000, v13
	global_load_dwordx4 a[240:243], v13, s[6:7] offset:0
	global_load_dwordx4 a[244:247], v13, s[6:7] offset:1024
	global_load_dwordx4 a[248:251], v13, s[6:7] offset:2048
	global_load_dwordx4 a[252:255], v13, s[6:7] offset:3072
	s_mov_b32 m0, s28
	s_add_u32 s28, s28, 0x4000
	s_cmp_ge_u32 s28, s46
	s_cselect_b32 s28, s47, s28
	global_load_lds_dwordx4 v9, s[26:27]
	global_load_lds_dwordx4 v9, s[26:27] offset:1024
	s_add_u32 m0, m0, 0x800
	s_nop 0
	global_load_lds_dwordx4 v10, s[26:27]
	global_load_lds_dwordx4 v10, s[26:27] offset:1024
	s_add_u32 s26, s26, 0x800
	s_addc_u32 s27, s27, 0
	s_mov_b32 m0, s28
	s_add_u32 s28, s28, 0x4000
	s_cmp_ge_u32 s28, s46
	s_cselect_b32 s28, s47, s28
	global_load_lds_dwordx4 v9, s[26:27]
	global_load_lds_dwordx4 v9, s[26:27] offset:1024
	s_add_u32 m0, m0, 0x800
	s_nop 0
	global_load_lds_dwordx4 v10, s[26:27]
	global_load_lds_dwordx4 v10, s[26:27] offset:1024
	s_add_u32 s26, s26, 0x800
	s_addc_u32 s27, s27, 0
	s_waitcnt vmcnt(63)
	s_barrier
	v_add_u32_e32 v5, s29, v4
	v_xor_b32_e32 v6, 64, v5
	s_add_u32 s29, s29, 0x4000
	s_cmp_ge_u32 s29, 0x14000
	s_cselect_b32 s29, 0, s29
	ds_read_b128 v[128:131], v5 offset:0
	ds_read_b128 v[132:135], v6 offset:0
	ds_read_b128 v[136:139], v5 offset:2048
	ds_read_b128 v[140:143], v6 offset:2048
	ds_read_b128 v[144:147], v5 offset:4096
	ds_read_b128 v[148:151], v6 offset:4096
	ds_read_b128 v[152:155], v5 offset:6144
	ds_read_b128 v[156:159], v6 offset:6144
	ds_read_b128 v[160:163], v5 offset:8192
	ds_read_b128 v[164:167], v6 offset:8192
	ds_read_b128 v[168:171], v5 offset:10240
	ds_read_b128 v[172:175], v6 offset:10240
	ds_read_b128 v[176:179], v5 offset:12288
	ds_read_b128 v[180:183], v6 offset:12288
	ds_read_b128 v[184:187], v5 offset:14336
	ds_read_b128 v[188:191], v6 offset:14336
	s_waitcnt lgkmcnt(0)
	s_mov_b32 m0, s28
	s_add_u32 s28, s28, 0x4000
	s_cmp_ge_u32 s28, s46
	s_cselect_b32 s28, s47, s28
	global_load_lds_dwordx4 v9, s[26:27]
	global_load_lds_dwordx4 v9, s[26:27] offset:1024
	s_add_u32 m0, m0, 0x800
	s_nop 0
	global_load_lds_dwordx4 v10, s[26:27]
	global_load_lds_dwordx4 v10, s[26:27] offset:1024
	s_add_u32 s26, s26, 0x800
	s_addc_u32 s27, s27, 0
	v_add_u32_e32 v7, s29, v4
	v_xor_b32_e32 v8, 64, v7
	s_add_u32 s29, s29, 0x4000
	s_cmp_ge_u32 s29, 0x14000
	s_cselect_b32 s29, 0, s29
	s_waitcnt vmcnt(63)
	v_mfma_f32_16x16x32_f16 v[48:51], a[0:3], v[128:131], v[32:35]
	v_mfma_f32_16x16x32_f16 v[52:55], a[4:7], v[128:131], v[36:39]
	v_mfma_f32_16x16x32_f16 v[56:59], a[8:11], v[128:131], v[40:43]
	ds_read_b128 v[192:195], v7 offset:0
	v_mfma_f32_16x16x32_f16 v[60:63], a[12:15], v[128:131], v[44:47]
	ds_read_b128 v[196:199], v8 offset:0
	s_waitcnt vmcnt(63)
	v_mfma_f32_16x16x32_f16 v[48:51], a[16:19], v[132:135], v[48:51]
	ds_read_b128 v[200:203], v7 offset:2048
	v_mfma_f32_16x16x32_f16 v[52:55], a[20:23], v[132:135], v[52:55]
	ds_read_b128 v[204:207], v8 offset:2048
	v_mfma_f32_16x16x32_f16 v[56:59], a[24:27], v[132:135], v[56:59]
	ds_read_b128 v[208:211], v7 offset:4096
	v_mfma_f32_16x16x32_f16 v[60:63], a[28:31], v[132:135], v[60:63]
	ds_read_b128 v[212:215], v8 offset:4096
	s_waitcnt vmcnt(63)
	v_mfma_f32_16x16x32_f16 v[48:51], a[32:35], v[136:139], v[48:51]
	ds_read_b128 v[216:219], v7 offset:6144
	v_mfma_f32_16x16x32_f16 v[52:55], a[36:39], v[136:139], v[52:55]
	ds_read_b128 v[220:223], v8 offset:6144
	v_mfma_f32_16x16x32_f16 v[56:59], a[40:43], v[136:139], v[56:59]
	ds_read_b128 v[224:227], v7 offset:8192
	v_mfma_f32_16x16x32_f16 v[60:63], a[44:47], v[136:139], v[60:63]
	ds_read_b128 v[228:231], v8 offset:8192
	s_waitcnt vmcnt(60)
	v_mfma_f32_16x16x32_f16 v[48:51], a[48:51], v[140:143], v[48:51]
	ds_read_b128 v[232:235], v7 offset:10240
	v_mfma_f32_16x16x32_f16 v[52:55], a[52:55], v[140:143], v[52:55]
	ds_read_b128 v[236:239], v8 offset:10240
	v_mfma_f32_16x16x32_f16 v[56:59], a[56:59], v[140:143], v[56:59]
	ds_read_b128 v[240:243], v7 offset:12288
	v_mfma_f32_16x16x32_f16 v[60:63], a[60:63], v[140:143], v[60:63]
	ds_read_b128 v[244:247], v8 offset:12288
	s_waitcnt vmcnt(56)
	v_mfma_f32_16x16x32_f16 v[48:51], a[64:67], v[144:147], v[48:51]
	ds_read_b128 v[248:251], v7 offset:14336
	v_mfma_f32_16x16x32_f16 v[52:55], a[68:71], v[144:147], v[52:55]
	ds_read_b128 v[252:255], v8 offset:14336
	v_mfma_f32_16x16x32_f16 v[56:59], a[72:75], v[144:147], v[56:59]
	v_mfma_f32_16x16x32_f16 v[60:63], a[76:79], v[144:147], v[60:63]
	s_waitcnt vmcnt(52)
	v_mfma_f32_16x16x32_f16 v[48:51], a[80:83], v[148:151], v[48:51]
	v_mfma_f32_16x16x32_f16 v[52:55], a[84:87], v[148:151], v[52:55]
	v_mfma_f32_16x16x32_f16 v[56:59], a[88:91], v[148:151], v[56:59]
	v_mfma_f32_16x16x32_f16 v[60:63], a[92:95], v[148:151], v[60:63]
	s_waitcnt vmcnt(48)
	v_mfma_f32_16x16x32_f16 v[48:51], a[96:99], v[152:155], v[48:51]
	v_mfma_f32_16x16x32_f16 v[52:55], a[100:103], v[152:155], v[52:55]
	v_mfma_f32_16x16x32_f16 v[56:59], a[104:107], v[152:155], v[56:59]
	v_mfma_f32_16x16x32_f16 v[60:63], a[108:111], v[152:155], v[60:63]
	s_waitcnt vmcnt(44)
	v_mfma_f32_16x16x32_f16 v[48:51], a[112:115], v[156:159], v[48:51]
	v_mfma_f32_16x16x32_f16 v[52:55], a[116:119], v[156:159], v[52:55]
	v_mfma_f32_16x16x32_f16 v[56:59], a[120:123], v[156:159], v[56:59]
	v_mfma_f32_16x16x32_f16 v[60:63], a[124:127], v[156:159], v[60:63]
	s_waitcnt vmcnt(40)
	v_mfma_f32_16x16x32_f16 v[48:51], a[128:131], v[160:163], v[48:51]
	v_mfma_f32_16x16x32_f16 v[52:55], a[132:135], v[160:163], v[52:55]
	v_mfma_f32_16x16x32_f16 v[56:59], a[136:139], v[160:163], v[56:59]
	v_mfma_f32_16x16x32_f16 v[60:63], a[140:143], v[160:163], v[60:63]
	s_waitcnt vmcnt(36)
	v_mfma_f32_16x16x32_f16 v[48:51], a[144:147], v[164:167], v[48:51]
	v_mfma_f32_16x16x32_f16 v[52:55], a[148:151], v[164:167], v[52:55]
	v_mfma_f32_16x16x32_f16 v[56:59], a[152:155], v[164:167], v[56:59]
	v_mfma_f32_16x16x32_f16 v[60:63], a[156:159], v[164:167], v[60:63]
	s_waitcnt vmcnt(32)
	v_mfma_f32_16x16x32_f16 v[48:51], a[160:163], v[168:171], v[48:51]
	v_mfma_f32_16x16x32_f16 v[52:55], a[164:167], v[168:171], v[52:55]
	v_mfma_f32_16x16x32_f16 v[56:59], a[168:171], v[168:171], v[56:59]
	v_mfma_f32_16x16x32_f16 v[60:63], a[172:175], v[168:171], v[60:63]
	s_waitcnt vmcnt(28)
	v_mfma_f32_16x16x32_f16 v[48:51], a[176:179], v[172:175], v[48:51]
	v_mfma_f32_16x16x32_f16 v[52:55], a[180:183], v[172:175], v[52:55]
	v_mfma_f32_16x16x32_f16 v[56:59], a[184:187], v[172:175], v[56:59]
	v_mfma_f32_16x16x32_f16 v[60:63], a[188:191], v[172:175], v[60:63]
	s_waitcnt vmcnt(24)
	v_mfma_f32_16x16x32_f16 v[48:51], a[192:195], v[176:179], v[48:51]
	v_mfma_f32_16x16x32_f16 v[52:55], a[196:199], v[176:179], v[52:55]
	v_mfma_f32_16x16x32_f16 v[56:59], a[200:203], v[176:179], v[56:59]
	v_mfma_f32_16x16x32_f16 v[60:63], a[204:207], v[176:179], v[60:63]
	s_waitcnt vmcnt(20)
	v_mfma_f32_16x16x32_f16 v[48:51], a[208:211], v[180:183], v[48:51]
	v_mfma_f32_16x16x32_f16 v[52:55], a[212:215], v[180:183], v[52:55]
	v_mfma_f32_16x16x32_f16 v[56:59], a[216:219], v[180:183], v[56:59]
	v_mfma_f32_16x16x32_f16 v[60:63], a[220:223], v[180:183], v[60:63]
	s_waitcnt vmcnt(16)
	v_mfma_f32_16x16x32_f16 v[48:51], a[224:227], v[184:187], v[48:51]
	v_mfma_f32_16x16x32_f16 v[52:55], a[228:231], v[184:187], v[52:55]
	v_mfma_f32_16x16x32_f16 v[56:59], a[232:235], v[184:187], v[56:59]
	v_mfma_f32_16x16x32_f16 v[60:63], a[236:239], v[184:187], v[60:63]
	s_waitcnt vmcnt(12)
	v_mfma_f32_16x16x32_f16 v[48:51], a[240:243], v[188:191], v[48:51]
	v_mfma_f32_16x16x32_f16 v[52:55], a[244:247], v[188:191], v[52:55]
	v_mfma_f32_16x16x32_f16 v[56:59], a[248:251], v[188:191], v[56:59]
	v_mfma_f32_16x16x32_f16 v[60:63], a[252:255], v[188:191], v[60:63]
Lg1_loop:
	s_waitcnt vmcnt(8) lgkmcnt(0)
	s_barrier
	v_mfma_f32_16x16x32_f16 v[64:67], a[0:3], v[192:195], v[32:35]
	v_mfma_f32_16x16x32_f16 v[68:71], a[4:7], v[192:195], v[36:39]
	v_add_u32_e32 v5, s29, v4
	v_xor_b32_e32 v6, 64, v5
	s_add_u32 s29, s29, 0x4000
	s_cmp_ge_u32 s29, 0x14000
	s_cselect_b32 s29, 0, s29
	v_mfma_f32_16x16x32_f16 v[72:75], a[8:11], v[192:195], v[40:43]
	ds_read_b128 v[128:131], v5 offset:0
	v_mfma_f32_16x16x32_f16 v[76:79], a[12:15], v[192:195], v[44:47]
	ds_read_b128 v[132:135], v6 offset:0
	v_and_b32_e32 v16, 0x7fffffff, v48
	v_fmaak_f32 v17, v113, v16, 0x384d0fec
	v_fmaak_f32 v17, v17, v16, 0x381f6607
	v_fmaak_f32 v17, v17, v16, 0x3b56cd72
	v_fmaak_f32 v17, v17, v16, 0x3cad2fe7
	v_mfma_f32_16x16x32_f16 v[64:67], a[16:19], v[196:199], v[64:67]
	ds_read_b128 v[136:139], v5 offset:2048
	v_fmaak_f32 v17, v17, v16, 0x3d4c41b4
	v_fmaak_f32 v17, v17, v16, 0x3f800000
	v_mul_f32_e32 v17, v17, v17
	v_mul_f32_e32 v17, v17, v17
	v_mfma_f32_16x16x32_f16 v[68:71], a[20:23], v[196:199], v[68:71]
	ds_read_b128 v[140:143], v6 offset:2048
	v_mul_f32_e32 v17, v17, v17
	v_mul_f32_e32 v17, v17, v17
	v_rcp_f32_e32 v17, v17
	v_max_f32_e32 v18, 0, v48
	v_mul_f32_e32 v16, v16, v17
	v_mfma_f32_16x16x32_f16 v[72:75], a[24:27], v[196:199], v[72:75]
	ds_read_b128 v[144:147], v5 offset:4096
	v_fmamk_f32 v96, v16, 0xbf000000, v18
	v_and_b32_e32 v19, 0x7fffffff, v49
	v_fmaak_f32 v20, v113, v19, 0x384d0fec
	v_fmaak_f32 v20, v20, v19, 0x381f6607
	v_mfma_f32_16x16x32_f16 v[76:79], a[28:31], v[196:199], v[76:79]
	ds_read_b128 v[148:151], v6 offset:4096
	v_fmaak_f32 v20, v20, v19, 0x3b56cd72
	v_fmaak_f32 v20, v20, v19, 0x3cad2fe7
	v_fmaak_f32 v20, v20, v19, 0x3d4c41b4
	v_fmaak_f32 v20, v20, v19, 0x3f800000
	v_mul_f32_e32 v20, v20, v20
	v_mfma_f32_16x16x32_f16 v[64:67], a[32:35], v[200:203], v[64:67]
	ds_read_b128 v[152:155], v5 offset:6144
	v_mul_f32_e32 v20, v20, v20
	v_mul_f32_e32 v20, v20, v20
	v_mul_f32_e32 v20, v20, v20
	v_rcp_f32_e32 v20, v20
	v_mfma_f32_16x16x32_f16 v[68:71], a[36:39], v[200:203], v[68:71]
	ds_read_b128 v[156:159], v6 offset:6144
	v_max_f32_e32 v21, 0, v49
	v_mul_f32_e32 v19, v19, v20
	v_fmamk_f32 v97, v19, 0xbf000000, v21
	v_and_b32_e32 v22, 0x7fffffff, v50
	v_fmaak_f32 v23, v113, v22, 0x384d0fec
	v_mfma_f32_16x16x32_f16 v[72:75], a[40:43], v[200:203], v[72:75]
	ds_read_b128 v[160:163], v5 offset:8192
	v_fmaak_f32 v23, v23, v22, 0x381f6607
	v_fmaak_f32 v23, v23, v22, 0x3b56cd72
	v_fmaak_f32 v23, v23, v22, 0x3cad2fe7
	v_fmaak_f32 v23, v23, v22, 0x3d4c41b4
	v_mfma_f32_16x16x32_f16 v[76:79], a[44:47], v[200:203], v[76:79]
	ds_read_b128 v[164:167], v6 offset:8192
	v_fmaak_f32 v23, v23, v22, 0x3f800000
	v_mul_f32_e32 v23, v23, v23
	v_mul_f32_e32 v23, v23, v23
	v_mul_f32_e32 v23, v23, v23
	v_mul_f32_e32 v23, v23, v23
	v_mfma_f32_16x16x32_f16 v[64:67], a[48:51], v[204:207], v[64:67]
	ds_read_b128 v[168:171], v5 offset:10240
	v_rcp_f32_e32 v23, v23
	v_max_f32_e32 v24, 0, v50
	v_mul_f32_e32 v22, v22, v23
	v_fmamk_f32 v98, v22, 0xbf000000, v24
	v_mfma_f32_16x16x32_f16 v[68:71], a[52:55], v[204:207], v[68:71]
	ds_read_b128 v[172:175], v6 offset:10240
	v_and_b32_e32 v25, 0x7fffffff, v51
	v_fmaak_f32 v26, v113, v25, 0x384d0fec
	v_fmaak_f32 v26, v26, v25, 0x381f6607
	v_fmaak_f32 v26, v26, v25, 0x3b56cd72
	v_fmaak_f32 v26, v26, v25, 0x3cad2fe7
	v_mfma_f32_16x16x32_f16 v[72:75], a[56:59], v[204:207], v[72:75]
	ds_read_b128 v[176:179], v5 offset:12288
	v_fmaak_f32 v26, v26, v25, 0x3d4c41b4
	v_fmaak_f32 v26, v26, v25, 0x3f800000
	v_mul_f32_e32 v26, v26, v26
	v_mul_f32_e32 v26, v26, v26
	v_mfma_f32_16x16x32_f16 v[76:79], a[60:63], v[204:207], v[76:79]
	ds_read_b128 v[180:183], v6 offset:12288
	v_mul_f32_e32 v26, v26, v26
	v_mul_f32_e32 v26, v26, v26
	v_rcp_f32_e32 v26, v26
	v_max_f32_e32 v27, 0, v51
	v_mul_f32_e32 v25, v25, v26
	v_mfma_f32_16x16x32_f16 v[64:67], a[64:67], v[208:211], v[64:67]
	ds_read_b128 v[184:187], v5 offset:14336
	v_fmamk_f32 v99, v25, 0xbf000000, v27
	v_and_b32_e32 v16, 0x7fffffff, v52
	v_fmaak_f32 v17, v113, v16, 0x384d0fec
	v_fmaak_f32 v17, v17, v16, 0x381f6607
	v_mfma_f32_16x16x32_f16 v[68:71], a[68:71], v[208:211], v[68:71]
	ds_read_b128 v[188:191], v6 offset:14336
	v_fmaak_f32 v17, v17, v16, 0x3b56cd72
	v_fmaak_f32 v17, v17, v16, 0x3cad2fe7
	v_fmaak_f32 v17, v17, v16, 0x3d4c41b4
	v_fmaak_f32 v17, v17, v16, 0x3f800000
	v_mfma_f32_16x16x32_f16 v[72:75], a[72:75], v[208:211], v[72:75]
	v_mul_f32_e32 v17, v17, v17
	v_mul_f32_e32 v17, v17, v17
	v_mul_f32_e32 v17, v17, v17
	v_mul_f32_e32 v17, v17, v17
	v_rcp_f32_e32 v17, v17
	v_mfma_f32_16x16x32_f16 v[76:79], a[76:79], v[208:211], v[76:79]
	v_max_f32_e32 v18, 0, v52
	v_mul_f32_e32 v16, v16, v17
	v_fmamk_f32 v100, v16, 0xbf000000, v18
	v_and_b32_e32 v19, 0x7fffffff, v53
	v_mfma_f32_16x16x32_f16 v[64:67], a[80:83], v[212:215], v[64:67]
	v_fmaak_f32 v20, v113, v19, 0x384d0fec
	v_fmaak_f32 v20, v20, v19, 0x381f6607
	v_fmaak_f32 v20, v20, v19, 0x3b56cd72
	v_fmaak_f32 v20, v20, v19, 0x3cad2fe7
	v_fmaak_f32 v20, v20, v19, 0x3d4c41b4
	v_mfma_f32_16x16x32_f16 v[68:71], a[84:87], v[212:215], v[68:71]
	v_fmaak_f32 v20, v20, v19, 0x3f800000
	v_mul_f32_e32 v20, v20, v20
	v_mul_f32_e32 v20, v20, v20
	v_mul_f32_e32 v20, v20, v20
	v_mfma_f32_16x16x32_f16 v[72:75], a[88:91], v[212:215], v[72:75]
	s_mov_b32 m0, s28
	s_add_u32 s28, s28, 0x4000
	s_cmp_ge_u32 s28, s46
	s_cselect_b32 s28, s47, s28
	global_load_lds_dwordx4 v9, s[26:27]
	v_mul_f32_e32 v20, v20, v20
	v_rcp_f32_e32 v20, v20
	v_max_f32_e32 v21, 0, v53
	v_mul_f32_e32 v19, v19, v20
	v_fmamk_f32 v101, v19, 0xbf000000, v21
	v_mfma_f32_16x16x32_f16 v[76:79], a[92:95], v[212:215], v[76:79]
	v_and_b32_e32 v22, 0x7fffffff, v54
	v_fmaak_f32 v23, v113, v22, 0x384d0fec
	v_fmaak_f32 v23, v23, v22, 0x381f6607
	v_fmaak_f32 v23, v23, v22, 0x3b56cd72
	v_mfma_f32_16x16x32_f16 v[64:67], a[96:99], v[216:219], v[64:67]
	v_fmaak_f32 v23, v23, v22, 0x3cad2fe7
	v_fmaak_f32 v23, v23, v22, 0x3d4c41b4
	v_fmaak_f32 v23, v23, v22, 0x3f800000
	v_mul_f32_e32 v23, v23, v23
	v_mul_f32_e32 v23, v23, v23
	v_mfma_f32_16x16x32_f16 v[68:71], a[100:103], v[216:219], v[68:71]
	v_mul_f32_e32 v23, v23, v23
	v_mul_f32_e32 v23, v23, v23
	v_rcp_f32_e32 v23, v23
	v_max_f32_e32 v24, 0, v54
	v_mfma_f32_16x16x32_f16 v[72:75], a[104:107], v[216:219], v[72:75]
	v_mul_f32_e32 v22, v22, v23
	v_fmamk_f32 v102, v22, 0xbf000000, v24
	v_and_b32_e32 v25, 0x7fffffff, v55
	v_fmaak_f32 v26, v113, v25, 0x384d0fec
	v_fmaak_f32 v26, v26, v25, 0x381f6607
	v_mfma_f32_16x16x32_f16 v[76:79], a[108:111], v[216:219], v[76:79]
	v_fmaak_f32 v26, v26, v25, 0x3b56cd72
	v_fmaak_f32 v26, v26, v25, 0x3cad2fe7
	v_fmaak_f32 v26, v26, v25, 0x3d4c41b4
	v_fmaak_f32 v26, v26, v25, 0x3f800000
	v_mfma_f32_16x16x32_f16 v[64:67], a[112:115], v[220:223], v[64:67]
	v_mul_f32_e32 v26, v26, v26
	v_mul_f32_e32 v26, v26, v26
	v_mul_f32_e32 v26, v26, v26
	v_mul_f32_e32 v26, v26, v26
	v_rcp_f32_e32 v26, v26
	v_mfma_f32_16x16x32_f16 v[68:71], a[116:119], v[220:223], v[68:71]
	v_max_f32_e32 v27, 0, v55
	v_mul_f32_e32 v25, v25, v26
	v_fmamk_f32 v103, v25, 0xbf000000, v27
	v_and_b32_e32 v16, 0x7fffffff, v56
	v_mfma_f32_16x16x32_f16 v[72:75], a[120:123], v[220:223], v[72:75]
	v_fmaak_f32 v17, v113, v16, 0x384d0fec
	v_fmaak_f32 v17, v17, v16, 0x381f6607
	v_fmaak_f32 v17, v17, v16, 0x3b56cd72
	v_fmaak_f32 v17, v17, v16, 0x3cad2fe7
	v_mfma_f32_16x16x32_f16 v[76:79], a[124:127], v[220:223], v[76:79]
	v_fmaak_f32 v17, v17, v16, 0x3d4c41b4
	v_fmaak_f32 v17, v17, v16, 0x3f800000
	v_mul_f32_e32 v17, v17, v17
	v_mul_f32_e32 v17, v17, v17
	v_mul_f32_e32 v17, v17, v17
	v_mfma_f32_16x16x32_f16 v[64:67], a[128:131], v[224:227], v[64:67]
	v_mul_f32_e32 v17, v17, v17
	v_rcp_f32_e32 v17, v17
	v_max_f32_e32 v18, 0, v56
	v_mul_f32_e32 v16, v16, v17
	v_mfma_f32_16x16x32_f16 v[68:71], a[132:135], v[224:227], v[68:71]
	global_load_lds_dwordx4 v9, s[26:27] offset:1024
	v_fmamk_f32 v104, v16, 0xbf000000, v18
	v_and_b32_e32 v19, 0x7fffffff, v57
	v_fmaak_f32 v20, v113, v19, 0x384d0fec
	v_fmaak_f32 v20, v20, v19, 0x381f6607
	v_fmaak_f32 v20, v20, v19, 0x3b56cd72
	v_mfma_f32_16x16x32_f16 v[72:75], a[136:139], v[224:227], v[72:75]
	v_fmaak_f32 v20, v20, v19, 0x3cad2fe7
	v_fmaak_f32 v20, v20, v19, 0x3d4c41b4
	v_fmaak_f32 v20, v20, v19, 0x3f800000
	v_mul_f32_e32 v20, v20, v20
	v_mfma_f32_16x16x32_f16 v[76:79], a[140:143], v[224:227], v[76:79]
	v_mul_f32_e32 v20, v20, v20
	v_mul_f32_e32 v20, v20, v20
	v_mul_f32_e32 v20, v20, v20
	v_rcp_f32_e32 v20, v20
	v_max_f32_e32 v21, 0, v57
	v_mfma_f32_16x16x32_f16 v[64:67], a[144:147], v[228:231], v[64:67]
	v_mul_f32_e32 v19, v19, v20
	v_fmamk_f32 v105, v19, 0xbf000000, v21
	v_and_b32_e32 v22, 0x7fffffff, v58
	v_fmaak_f32 v23, v113, v22, 0x384d0fec
	v_mfma_f32_16x16x32_f16 v[68:71], a[148:151], v[228:231], v[68:71]
	v_fmaak_f32 v23, v23, v22, 0x381f6607
	v_fmaak_f32 v23, v23, v22, 0x3b56cd72
	v_fmaak_f32 v23, v23, v22, 0x3cad2fe7
	v_fmaak_f32 v23, v23, v22, 0x3d4c41b4
	v_fmaak_f32 v23, v23, v22, 0x3f800000
	v_mfma_f32_16x16x32_f16 v[72:75], a[152:155], v[228:231], v[72:75]
	v_mul_f32_e32 v23, v23, v23
	v_mul_f32_e32 v23, v23, v23
	v_mul_f32_e32 v23, v23, v23
	v_mul_f32_e32 v23, v23, v23
	v_mfma_f32_16x16x32_f16 v[76:79], a[156:159], v[228:231], v[76:79]
	v_rcp_f32_e32 v23, v23
	v_max_f32_e32 v24, 0, v58
	v_mul_f32_e32 v22, v22, v23
	v_fmamk_f32 v106, v22, 0xbf000000, v24
	v_and_b32_e32 v25, 0x7fffffff, v59
	v_mfma_f32_16x16x32_f16 v[64:67], a[160:163], v[232:235], v[64:67]
	v_fmaak_f32 v26, v113, v25, 0x384d0fec
	v_fmaak_f32 v26, v26, v25, 0x381f6607
	v_fmaak_f32 v26, v26, v25, 0x3b56cd72
	v_fmaak_f32 v26, v26, v25, 0x3cad2fe7
	v_mfma_f32_16x16x32_f16 v[68:71], a[164:167], v[232:235], v[68:71]
	v_fmaak_f32 v26, v26, v25, 0x3d4c41b4
	v_fmaak_f32 v26, v26, v25, 0x3f800000
	v_mul_f32_e32 v26, v26, v26
	v_mul_f32_e32 v26, v26, v26
	v_mul_f32_e32 v26, v26, v26
	v_mfma_f32_16x16x32_f16 v[72:75], a[168:171], v[232:235], v[72:75]
	v_mul_f32_e32 v26, v26, v26
	v_rcp_f32_e32 v26, v26
	v_max_f32_e32 v27, 0, v59
	v_mul_f32_e32 v25, v25, v26
	v_mfma_f32_16x16x32_f16 v[76:79], a[172:175], v[232:235], v[76:79]
	v_fmamk_f32 v107, v25, 0xbf000000, v27
	v_and_b32_e32 v16, 0x7fffffff, v60
	v_fmaak_f32 v17, v113, v16, 0x384d0fec
	v_fmaak_f32 v17, v17, v16, 0x381f6607
	v_fmaak_f32 v17, v17, v16, 0x3b56cd72
	v_mfma_f32_16x16x32_f16 v[64:67], a[176:179], v[236:239], v[64:67]
	s_add_u32 m0, m0, 0x800
	s_nop 0
	global_load_lds_dwordx4 v10, s[26:27]
	v_fmaak_f32 v17, v17, v16, 0x3cad2fe7
	v_fmaak_f32 v17, v17, v16, 0x3d4c41b4
	v_fmaak_f32 v17, v17, v16, 0x3f800000
	v_mul_f32_e32 v17, v17, v17
	v_mfma_f32_16x16x32_f16 v[68:71], a[180:183], v[236:239], v[68:71]
	v_mul_f32_e32 v17, v17, v17
	v_mul_f32_e32 v17, v17, v17
	v_mul_f32_e32 v17, v17, v17
	v_rcp_f32_e32 v17, v17
	v_mfma_f32_16x16x32_f16 v[72:75], a[184:187], v[236:239], v[72:75]
	v_max_f32_e32 v18, 0, v60
	v_mul_f32_e32 v16, v16, v17
	v_fmamk_f32 v108, v16, 0xbf000000, v18
	v_and_b32_e32 v19, 0x7fffffff, v61
	v_fmaak_f32 v20, v113, v19, 0x384d0fec
	v_mfma_f32_16x16x32_f16 v[76:79], a[188:191], v[236:239], v[76:79]
	v_fmaak_f32 v20, v20, v19, 0x381f6607
	v_fmaak_f32 v20, v20, v19, 0x3b56cd72
	v_fmaak_f32 v20, v20, v19, 0x3cad2fe7
	v_fmaak_f32 v20, v20, v19, 0x3d4c41b4
	v_mfma_f32_16x16x32_f16 v[64:67], a[192:195], v[240:243], v[64:67]
	v_fmaak_f32 v20, v20, v19, 0x3f800000
	v_mul_f32_e32 v20, v20, v20
	v_mul_f32_e32 v20, v20, v20
	v_mul_f32_e32 v20, v20, v20
	v_mul_f32_e32 v20, v20, v20
	v_mfma_f32_16x16x32_f16 v[68:71], a[196:199], v[240:243], v[68:71]
	v_rcp_f32_e32 v20, v20
	v_max_f32_e32 v21, 0, v61
	v_mul_f32_e32 v19, v19, v20
	v_fmamk_f32 v109, v19, 0xbf000000, v21
	v_mfma_f32_16x16x32_f16 v[72:75], a[200:203], v[240:243], v[72:75]
	v_and_b32_e32 v22, 0x7fffffff, v62
	v_fmaak_f32 v23, v113, v22, 0x384d0fec
	v_fmaak_f32 v23, v23, v22, 0x381f6607
	v_fmaak_f32 v23, v23, v22, 0x3b56cd72
	v_fmaak_f32 v23, v23, v22, 0x3cad2fe7
	v_mfma_f32_16x16x32_f16 v[76:79], a[204:207], v[240:243], v[76:79]
	v_fmaak_f32 v23, v23, v22, 0x3d4c41b4
	v_fmaak_f32 v23, v23, v22, 0x3f800000
	v_mul_f32_e32 v23, v23, v23
	v_mul_f32_e32 v23, v23, v23
	v_mfma_f32_16x16x32_f16 v[64:67], a[208:211], v[244:247], v[64:67]
	v_mul_f32_e32 v23, v23, v23
	v_mul_f32_e32 v23, v23, v23
	v_rcp_f32_e32 v23, v23
	v_max_f32_e32 v24, 0, v62
	v_mul_f32_e32 v22, v22, v23
	v_mfma_f32_16x16x32_f16 v[68:71], a[212:215], v[244:247], v[68:71]
	v_fmamk_f32 v110, v22, 0xbf000000, v24
	v_and_b32_e32 v25, 0x7fffffff, v63
	v_fmaak_f32 v26, v113, v25, 0x384d0fec
	v_fmaak_f32 v26, v26, v25, 0x381f6607
	v_mfma_f32_16x16x32_f16 v[72:75], a[216:219], v[244:247], v[72:75]
	v_fmaak_f32 v26, v26, v25, 0x3b56cd72
	v_fmaak_f32 v26, v26, v25, 0x3cad2fe7
	v_fmaak_f32 v26, v26, v25, 0x3d4c41b4
	v_fmaak_f32 v26, v26, v25, 0x3f800000
	v_mul_f32_e32 v26, v26, v26
	v_mfma_f32_16x16x32_f16 v[76:79], a[220:223], v[244:247], v[76:79]
	v_mul_f32_e32 v26, v26, v26
	v_mul_f32_e32 v26, v26, v26
	v_mul_f32_e32 v26, v26, v26
	v_rcp_f32_e32 v26, v26
	v_mfma_f32_16x16x32_f16 v[64:67], a[224:227], v[248:251], v[64:67]
	global_load_lds_dwordx4 v10, s[26:27] offset:1024
	v_max_f32_e32 v27, 0, v63
	v_mul_f32_e32 v25, v25, v26
	v_fmamk_f32 v111, v25, 0xbf000000, v27
	v_cvt_pk_f16_f32 v96, v96, v97
	v_cvt_pk_f16_f32 v97, v98, v99
	v_mfma_f32_16x16x32_f16 v[68:71], a[228:231], v[248:251], v[68:71]
	s_add_u32 s26, s26, 0x800
	s_addc_u32 s27, s27, 0
	v_cvt_pk_f16_f32 v98, v100, v101
	v_cvt_pk_f16_f32 v99, v102, v103
	v_cvt_pk_f16_f32 v100, v104, v105
	v_cvt_pk_f16_f32 v101, v106, v107
	v_mfma_f32_16x16x32_f16 v[72:75], a[232:235], v[248:251], v[72:75]
	v_cvt_pk_f16_f32 v102, v108, v109
	v_cvt_pk_f16_f32 v103, v110, v111
	global_store_dwordx4 v14, v[96:99], s[30:31]
	global_store_dwordx4 v14, v[100:103], s[30:31] offset:16
	v_mfma_f32_16x16x32_f16 v[76:79], a[236:239], v[248:251], v[76:79]
	s_add_u32 s30, s30, 0x800
	s_addc_u32 s31, s31, 0
	v_mfma_f32_16x16x32_f16 v[64:67], a[240:243], v[252:255], v[64:67]
	v_mfma_f32_16x16x32_f16 v[68:71], a[244:247], v[252:255], v[68:71]
	v_mfma_f32_16x16x32_f16 v[72:75], a[248:251], v[252:255], v[72:75]
	v_mfma_f32_16x16x32_f16 v[76:79], a[252:255], v[252:255], v[76:79]
	s_sub_u32 s24, s24, 1
	s_cmp_le_u32 s24, 1
	s_cbranch_scc1 Lg1_exitA
	s_waitcnt vmcnt(8) lgkmcnt(0)
	s_barrier
	v_mfma_f32_16x16x32_f16 v[48:51], a[0:3], v[128:131], v[32:35]
	v_mfma_f32_16x16x32_f16 v[52:55], a[4:7], v[128:131], v[36:39]
	v_add_u32_e32 v7, s29, v4
	v_xor_b32_e32 v8, 64, v7
	s_add_u32 s29, s29, 0x4000
	s_cmp_ge_u32 s29, 0x14000
	s_cselect_b32 s29, 0, s29
	v_mfma_f32_16x16x32_f16 v[56:59], a[8:11], v[128:131], v[40:43]
	ds_read_b128 v[192:195], v7 offset:0
	v_mfma_f32_16x16x32_f16 v[60:63], a[12:15], v[128:131], v[44:47]
	ds_read_b128 v[196:199], v8 offset:0
	v_and_b32_e32 v16, 0x7fffffff, v64
	v_fmaak_f32 v17, v113, v16, 0x384d0fec
	v_fmaak_f32 v17, v17, v16, 0x381f6607
	v_fmaak_f32 v17, v17, v16, 0x3b56cd72
	v_fmaak_f32 v17, v17, v16, 0x3cad2fe7
	v_mfma_f32_16x16x32_f16 v[48:51], a[16:19], v[132:135], v[48:51]
	ds_read_b128 v[200:203], v7 offset:2048
	v_fmaak_f32 v17, v17, v16, 0x3d4c41b4
	v_fmaak_f32 v17, v17, v16, 0x3f800000
	v_mul_f32_e32 v17, v17, v17
	v_mul_f32_e32 v17, v17, v17
	v_mfma_f32_16x16x32_f16 v[52:55], a[20:23], v[132:135], v[52:55]
	ds_read_b128 v[204:207], v8 offset:2048
	v_mul_f32_e32 v17, v17, v17
	v_mul_f32_e32 v17, v17, v17
	v_rcp_f32_e32 v17, v17
	v_max_f32_e32 v18, 0, v64
	v_mul_f32_e32 v16, v16, v17
	v_mfma_f32_16x16x32_f16 v[56:59], a[24:27], v[132:135], v[56:59]
	ds_read_b128 v[208:211], v7 offset:4096
	v_fmamk_f32 v96, v16, 0xbf000000, v18
	v_and_b32_e32 v19, 0x7fffffff, v65
	v_fmaak_f32 v20, v113, v19, 0x384d0fec
	v_fmaak_f32 v20, v20, v19, 0x381f6607
	v_mfma_f32_16x16x32_f16 v[60:63], a[28:31], v[132:135], v[60:63]
	ds_read_b128 v[212:215], v8 offset:4096
	v_fmaak_f32 v20, v20, v19, 0x3b56cd72
	v_fmaak_f32 v20, v20, v19, 0x3cad2fe7
	v_fmaak_f32 v20, v20, v19, 0x3d4c41b4
	v_fmaak_f32 v20, v20, v19, 0x3f800000
	v_mul_f32_e32 v20, v20, v20
	v_mfma_f32_16x16x32_f16 v[48:51], a[32:35], v[136:139], v[48:51]
	ds_read_b128 v[216:219], v7 offset:6144
	v_mul_f32_e32 v20, v20, v20
	v_mul_f32_e32 v20, v20, v20
	v_mul_f32_e32 v20, v20, v20
	v_rcp_f32_e32 v20, v20
	v_mfma_f32_16x16x32_f16 v[52:55], a[36:39], v[136:139], v[52:55]
	ds_read_b128 v[220:223], v8 offset:6144
	v_max_f32_e32 v21, 0, v65
	v_mul_f32_e32 v19, v19, v20
	v_fmamk_f32 v97, v19, 0xbf000000, v21
	v_and_b32_e32 v22, 0x7fffffff, v66
	v_fmaak_f32 v23, v113, v22, 0x384d0fec
	v_mfma_f32_16x16x32_f16 v[56:59], a[40:43], v[136:139], v[56:59]
	ds_read_b128 v[224:227], v7 offset:8192
	v_fmaak_f32 v23, v23, v22, 0x381f6607
	v_fmaak_f32 v23, v23, v22, 0x3b56cd72
	v_fmaak_f32 v23, v23, v22, 0x3cad2fe7
	v_fmaak_f32 v23, v23, v22, 0x3d4c41b4
	v_mfma_f32_16x16x32_f16 v[60:63], a[44:47], v[136:139], v[60:63]
	ds_read_b128 v[228:231], v8 offset:8192
	v_fmaak_f32 v23, v23, v22, 0x3f800000
	v_mul_f32_e32 v23, v23, v23
	v_mul_f32_e32 v23, v23, v23
	v_mul_f32_e32 v23, v23, v23
	v_mul_f32_e32 v23, v23, v23
	v_mfma_f32_16x16x32_f16 v[48:51], a[48:51], v[140:143], v[48:51]
	ds_read_b128 v[232:235], v7 offset:10240
	v_rcp_f32_e32 v23, v23
	v_max_f32_e32 v24, 0, v66
	v_mul_f32_e32 v22, v22, v23
	v_fmamk_f32 v98, v22, 0xbf000000, v24
	v_mfma_f32_16x16x32_f16 v[52:55], a[52:55], v[140:143], v[52:55]
	ds_read_b128 v[236:239], v8 offset:10240
	v_and_b32_e32 v25, 0x7fffffff, v67
	v_fmaak_f32 v26, v113, v25, 0x384d0fec
	v_fmaak_f32 v26, v26, v25, 0x381f6607
	v_fmaak_f32 v26, v26, v25, 0x3b56cd72
	v_fmaak_f32 v26, v26, v25, 0x3cad2fe7
	v_mfma_f32_16x16x32_f16 v[56:59], a[56:59], v[140:143], v[56:59]
	ds_read_b128 v[240:243], v7 offset:12288
	v_fmaak_f32 v26, v26, v25, 0x3d4c41b4
	v_fmaak_f32 v26, v26, v25, 0x3f800000
	v_mul_f32_e32 v26, v26, v26
	v_mul_f32_e32 v26, v26, v26
	v_mfma_f32_16x16x32_f16 v[60:63], a[60:63], v[140:143], v[60:63]
	ds_read_b128 v[244:247], v8 offset:12288
	v_mul_f32_e32 v26, v26, v26
	v_mul_f32_e32 v26, v26, v26
	v_rcp_f32_e32 v26, v26
	v_max_f32_e32 v27, 0, v67
	v_mul_f32_e32 v25, v25, v26
	v_mfma_f32_16x16x32_f16 v[48:51], a[64:67], v[144:147], v[48:51]
	ds_read_b128 v[248:251], v7 offset:14336
	v_fmamk_f32 v99, v25, 0xbf000000, v27
	v_and_b32_e32 v16, 0x7fffffff, v68
	v_fmaak_f32 v17, v113, v16, 0x384d0fec
	v_fmaak_f32 v17, v17, v16, 0x381f6607
	v_mfma_f32_16x16x32_f16 v[52:55], a[68:71], v[144:147], v[52:55]
	ds_read_b128 v[252:255], v8 offset:14336
	v_fmaak_f32 v17, v17, v16, 0x3b56cd72
	v_fmaak_f32 v17, v17, v16, 0x3cad2fe7
	v_fmaak_f32 v17, v17, v16, 0x3d4c41b4
	v_fmaak_f32 v17, v17, v16, 0x3f800000
	v_mfma_f32_16x16x32_f16 v[56:59], a[72:75], v[144:147], v[56:59]
	v_mul_f32_e32 v17, v17, v17
	v_mul_f32_e32 v17, v17, v17
	v_mul_f32_e32 v17, v17, v17
	v_mul_f32_e32 v17, v17, v17
	v_rcp_f32_e32 v17, v17
	v_mfma_f32_16x16x32_f16 v[60:63], a[76:79], v[144:147], v[60:63]
	v_max_f32_e32 v18, 0, v68
	v_mul_f32_e32 v16, v16, v17
	v_fmamk_f32 v100, v16, 0xbf000000, v18
	v_and_b32_e32 v19, 0x7fffffff, v69
	v_mfma_f32_16x16x32_f16 v[48:51], a[80:83], v[148:151], v[48:51]
	v_fmaak_f32 v20, v113, v19, 0x384d0fec
	v_fmaak_f32 v20, v20, v19, 0x381f6607
	v_fmaak_f32 v20, v20, v19, 0x3b56cd72
	v_fmaak_f32 v20, v20, v19, 0x3cad2fe7
	v_fmaak_f32 v20, v20, v19, 0x3d4c41b4
	v_mfma_f32_16x16x32_f16 v[52:55], a[84:87], v[148:151], v[52:55]
	v_fmaak_f32 v20, v20, v19, 0x3f800000
	v_mul_f32_e32 v20, v20, v20
	v_mul_f32_e32 v20, v20, v20
	v_mul_f32_e32 v20, v20, v20
	v_mfma_f32_16x16x32_f16 v[56:59], a[88:91], v[148:151], v[56:59]
	s_mov_b32 m0, s28
	s_add_u32 s28, s28, 0x4000
	s_cmp_ge_u32 s28, s46
	s_cselect_b32 s28, s47, s28
	global_load_lds_dwordx4 v9, s[26:27]
	v_mul_f32_e32 v20, v20, v20
	v_rcp_f32_e32 v20, v20
	v_max_f32_e32 v21, 0, v69
	v_mul_f32_e32 v19, v19, v20
	v_fmamk_f32 v101, v19, 0xbf000000, v21
	v_mfma_f32_16x16x32_f16 v[60:63], a[92:95], v[148:151], v[60:63]
	v_and_b32_e32 v22, 0x7fffffff, v70
	v_fmaak_f32 v23, v113, v22, 0x384d0fec
	v_fmaak_f32 v23, v23, v22, 0x381f6607
	v_fmaak_f32 v23, v23, v22, 0x3b56cd72
	v_mfma_f32_16x16x32_f16 v[48:51], a[96:99], v[152:155], v[48:51]
	v_fmaak_f32 v23, v23, v22, 0x3cad2fe7
	v_fmaak_f32 v23, v23, v22, 0x3d4c41b4
	v_fmaak_f32 v23, v23, v22, 0x3f800000
	v_mul_f32_e32 v23, v23, v23
	v_mul_f32_e32 v23, v23, v23
	v_mfma_f32_16x16x32_f16 v[52:55], a[100:103], v[152:155], v[52:55]
	v_mul_f32_e32 v23, v23, v23
	v_mul_f32_e32 v23, v23, v23
	v_rcp_f32_e32 v23, v23
	v_max_f32_e32 v24, 0, v70
	v_mfma_f32_16x16x32_f16 v[56:59], a[104:107], v[152:155], v[56:59]
	v_mul_f32_e32 v22, v22, v23
	v_fmamk_f32 v102, v22, 0xbf000000, v24
	v_and_b32_e32 v25, 0x7fffffff, v71
	v_fmaak_f32 v26, v113, v25, 0x384d0fec
	v_fmaak_f32 v26, v26, v25, 0x381f6607
	v_mfma_f32_16x16x32_f16 v[60:63], a[108:111], v[152:155], v[60:63]
	v_fmaak_f32 v26, v26, v25, 0x3b56cd72
	v_fmaak_f32 v26, v26, v25, 0x3cad2fe7
	v_fmaak_f32 v26, v26, v25, 0x3d4c41b4
	v_fmaak_f32 v26, v26, v25, 0x3f800000
	v_mfma_f32_16x16x32_f16 v[48:51], a[112:115], v[156:159], v[48:51]
	v_mul_f32_e32 v26, v26, v26
	v_mul_f32_e32 v26, v26, v26
	v_mul_f32_e32 v26, v26, v26
	v_mul_f32_e32 v26, v26, v26
	v_rcp_f32_e32 v26, v26
	v_mfma_f32_16x16x32_f16 v[52:55], a[116:119], v[156:159], v[52:55]
	v_max_f32_e32 v27, 0, v71
	v_mul_f32_e32 v25, v25, v26
	v_fmamk_f32 v103, v25, 0xbf000000, v27
	v_and_b32_e32 v16, 0x7fffffff, v72
	v_mfma_f32_16x16x32_f16 v[56:59], a[120:123], v[156:159], v[56:59]
	v_fmaak_f32 v17, v113, v16, 0x384d0fec
	v_fmaak_f32 v17, v17, v16, 0x381f6607
	v_fmaak_f32 v17, v17, v16, 0x3b56cd72
	v_fmaak_f32 v17, v17, v16, 0x3cad2fe7
	v_mfma_f32_16x16x32_f16 v[60:63], a[124:127], v[156:159], v[60:63]
	v_fmaak_f32 v17, v17, v16, 0x3d4c41b4
	v_fmaak_f32 v17, v17, v16, 0x3f800000
	v_mul_f32_e32 v17, v17, v17
	v_mul_f32_e32 v17, v17, v17
	v_mul_f32_e32 v17, v17, v17
	v_mfma_f32_16x16x32_f16 v[48:51], a[128:131], v[160:163], v[48:51]
	v_mul_f32_e32 v17, v17, v17
	v_rcp_f32_e32 v17, v17
	v_max_f32_e32 v18, 0, v72
	v_mul_f32_e32 v16, v16, v17
	v_mfma_f32_16x16x32_f16 v[52:55], a[132:135], v[160:163], v[52:55]
	global_load_lds_dwordx4 v9, s[26:27] offset:1024
	v_fmamk_f32 v104, v16, 0xbf000000, v18
	v_and_b32_e32 v19, 0x7fffffff, v73
	v_fmaak_f32 v20, v113, v19, 0x384d0fec
	v_fmaak_f32 v20, v20, v19, 0x381f6607
	v_fmaak_f32 v20, v20, v19, 0x3b56cd72
	v_mfma_f32_16x16x32_f16 v[56:59], a[136:139], v[160:163], v[56:59]
	v_fmaak_f32 v20, v20, v19, 0x3cad2fe7
	v_fmaak_f32 v20, v20, v19, 0x3d4c41b4
	v_fmaak_f32 v20, v20, v19, 0x3f800000
	v_mul_f32_e32 v20, v20, v20
	v_mfma_f32_16x16x32_f16 v[60:63], a[140:143], v[160:163], v[60:63]
	v_mul_f32_e32 v20, v20, v20
	v_mul_f32_e32 v20, v20, v20
	v_mul_f32_e32 v20, v20, v20
	v_rcp_f32_e32 v20, v20
	v_max_f32_e32 v21, 0, v73
	v_mfma_f32_16x16x32_f16 v[48:51], a[144:147], v[164:167], v[48:51]
	v_mul_f32_e32 v19, v19, v20
	v_fmamk_f32 v105, v19, 0xbf000000, v21
	v_and_b32_e32 v22, 0x7fffffff, v74
	v_fmaak_f32 v23, v113, v22, 0x384d0fec
	v_mfma_f32_16x16x32_f16 v[52:55], a[148:151], v[164:167], v[52:55]
	v_fmaak_f32 v23, v23, v22, 0x381f6607
	v_fmaak_f32 v23, v23, v22, 0x3b56cd72
	v_fmaak_f32 v23, v23, v22, 0x3cad2fe7
	v_fmaak_f32 v23, v23, v22, 0x3d4c41b4
	v_fmaak_f32 v23, v23, v22, 0x3f800000
	v_mfma_f32_16x16x32_f16 v[56:59], a[152:155], v[164:167], v[56:59]
	v_mul_f32_e32 v23, v23, v23
	v_mul_f32_e32 v23, v23, v23
	v_mul_f32_e32 v23, v23, v23
	v_mul_f32_e32 v23, v23, v23
	v_mfma_f32_16x16x32_f16 v[60:63], a[156:159], v[164:167], v[60:63]
	v_rcp_f32_e32 v23, v23
	v_max_f32_e32 v24, 0, v74
	v_mul_f32_e32 v22, v22, v23
	v_fmamk_f32 v106, v22, 0xbf000000, v24
	v_and_b32_e32 v25, 0x7fffffff, v75
	v_mfma_f32_16x16x32_f16 v[48:51], a[160:163], v[168:171], v[48:51]
	v_fmaak_f32 v26, v113, v25, 0x384d0fec
	v_fmaak_f32 v26, v26, v25, 0x381f6607
	v_fmaak_f32 v26, v26, v25, 0x3b56cd72
	v_fmaak_f32 v26, v26, v25, 0x3cad2fe7
	v_mfma_f32_16x16x32_f16 v[52:55], a[164:167], v[168:171], v[52:55]
	v_fmaak_f32 v26, v26, v25, 0x3d4c41b4
	v_fmaak_f32 v26, v26, v25, 0x3f800000
	v_mul_f32_e32 v26, v26, v26
	v_mul_f32_e32 v26, v26, v26
	v_mul_f32_e32 v26, v26, v26
	v_mfma_f32_16x16x32_f16 v[56:59], a[168:171], v[168:171], v[56:59]
	v_mul_f32_e32 v26, v26, v26
	v_rcp_f32_e32 v26, v26
	v_max_f32_e32 v27, 0, v75
	v_mul_f32_e32 v25, v25, v26
	v_mfma_f32_16x16x32_f16 v[60:63], a[172:175], v[168:171], v[60:63]
	v_fmamk_f32 v107, v25, 0xbf000000, v27
	v_and_b32_e32 v16, 0x7fffffff, v76
	v_fmaak_f32 v17, v113, v16, 0x384d0fec
	v_fmaak_f32 v17, v17, v16, 0x381f6607
	v_fmaak_f32 v17, v17, v16, 0x3b56cd72
	v_mfma_f32_16x16x32_f16 v[48:51], a[176:179], v[172:175], v[48:51]
	s_add_u32 m0, m0, 0x800
	s_nop 0
	global_load_lds_dwordx4 v10, s[26:27]
	v_fmaak_f32 v17, v17, v16, 0x3cad2fe7
	v_fmaak_f32 v17, v17, v16, 0x3d4c41b4
	v_fmaak_f32 v17, v17, v16, 0x3f800000
	v_mul_f32_e32 v17, v17, v17
	v_mfma_f32_16x16x32_f16 v[52:55], a[180:183], v[172:175], v[52:55]
	v_mul_f32_e32 v17, v17, v17
	v_mul_f32_e32 v17, v17, v17
	v_mul_f32_e32 v17, v17, v17
	v_rcp_f32_e32 v17, v17
	v_mfma_f32_16x16x32_f16 v[56:59], a[184:187], v[172:175], v[56:59]
	v_max_f32_e32 v18, 0, v76
	v_mul_f32_e32 v16, v16, v17
	v_fmamk_f32 v108, v16, 0xbf000000, v18
	v_and_b32_e32 v19, 0x7fffffff, v77
	v_fmaak_f32 v20, v113, v19, 0x384d0fec
	v_mfma_f32_16x16x32_f16 v[60:63], a[188:191], v[172:175], v[60:63]
	v_fmaak_f32 v20, v20, v19, 0x381f6607
	v_fmaak_f32 v20, v20, v19, 0x3b56cd72
	v_fmaak_f32 v20, v20, v19, 0x3cad2fe7
	v_fmaak_f32 v20, v20, v19, 0x3d4c41b4
	v_mfma_f32_16x16x32_f16 v[48:51], a[192:195], v[176:179], v[48:51]
	v_fmaak_f32 v20, v20, v19, 0x3f800000
	v_mul_f32_e32 v20, v20, v20
	v_mul_f32_e32 v20, v20, v20
	v_mul_f32_e32 v20, v20, v20
	v_mul_f32_e32 v20, v20, v20
	v_mfma_f32_16x16x32_f16 v[52:55], a[196:199], v[176:179], v[52:55]
	v_rcp_f32_e32 v20, v20
	v_max_f32_e32 v21, 0, v77
	v_mul_f32_e32 v19, v19, v20
	v_fmamk_f32 v109, v19, 0xbf000000, v21
	v_mfma_f32_16x16x32_f16 v[56:59], a[200:203], v[176:179], v[56:59]
	v_and_b32_e32 v22, 0x7fffffff, v78
	v_fmaak_f32 v23, v113, v22, 0x384d0fec
	v_fmaak_f32 v23, v23, v22, 0x381f6607
	v_fmaak_f32 v23, v23, v22, 0x3b56cd72
	v_fmaak_f32 v23, v23, v22, 0x3cad2fe7
	v_mfma_f32_16x16x32_f16 v[60:63], a[204:207], v[176:179], v[60:63]
	v_fmaak_f32 v23, v23, v22, 0x3d4c41b4
	v_fmaak_f32 v23, v23, v22, 0x3f800000
	v_mul_f32_e32 v23, v23, v23
	v_mul_f32_e32 v23, v23, v23
	v_mfma_f32_16x16x32_f16 v[48:51], a[208:211], v[180:183], v[48:51]
	v_mul_f32_e32 v23, v23, v23
	v_mul_f32_e32 v23, v23, v23
	v_rcp_f32_e32 v23, v23
	v_max_f32_e32 v24, 0, v78
	v_mul_f32_e32 v22, v22, v23
	v_mfma_f32_16x16x32_f16 v[52:55], a[212:215], v[180:183], v[52:55]
	v_fmamk_f32 v110, v22, 0xbf000000, v24
	v_and_b32_e32 v25, 0x7fffffff, v79
	v_fmaak_f32 v26, v113, v25, 0x384d0fec
	v_fmaak_f32 v26, v26, v25, 0x381f6607
	v_mfma_f32_16x16x32_f16 v[56:59], a[216:219], v[180:183], v[56:59]
	v_fmaak_f32 v26, v26, v25, 0x3b56cd72
	v_fmaak_f32 v26, v26, v25, 0x3cad2fe7
	v_fmaak_f32 v26, v26, v25, 0x3d4c41b4
	v_fmaak_f32 v26, v26, v25, 0x3f800000
	v_mul_f32_e32 v26, v26, v26
	v_mfma_f32_16x16x32_f16 v[60:63], a[220:223], v[180:183], v[60:63]
	v_mul_f32_e32 v26, v26, v26
	v_mul_f32_e32 v26, v26, v26
	v_mul_f32_e32 v26, v26, v26
	v_rcp_f32_e32 v26, v26
	v_mfma_f32_16x16x32_f16 v[48:51], a[224:227], v[184:187], v[48:51]
	global_load_lds_dwordx4 v10, s[26:27] offset:1024
	v_max_f32_e32 v27, 0, v79
	v_mul_f32_e32 v25, v25, v26
	v_fmamk_f32 v111, v25, 0xbf000000, v27
	v_cvt_pk_f16_f32 v96, v96, v97
	v_cvt_pk_f16_f32 v97, v98, v99
	v_mfma_f32_16x16x32_f16 v[52:55], a[228:231], v[184:187], v[52:55]
	s_add_u32 s26, s26, 0x800
	s_addc_u32 s27, s27, 0
	v_cvt_pk_f16_f32 v98, v100, v101
	v_cvt_pk_f16_f32 v99, v102, v103
	v_cvt_pk_f16_f32 v100, v104, v105
	v_cvt_pk_f16_f32 v101, v106, v107
	v_mfma_f32_16x16x32_f16 v[56:59], a[232:235], v[184:187], v[56:59]
	v_cvt_pk_f16_f32 v102, v108, v109
	v_cvt_pk_f16_f32 v103, v110, v111
	global_store_dwordx4 v14, v[96:99], s[30:31]
	global_store_dwordx4 v14, v[100:103], s[30:31] offset:16
	v_mfma_f32_16x16x32_f16 v[60:63], a[236:239], v[184:187], v[60:63]
	s_add_u32 s30, s30, 0x800
	s_addc_u32 s31, s31, 0
	v_mfma_f32_16x16x32_f16 v[48:51], a[240:243], v[188:191], v[48:51]
	v_mfma_f32_16x16x32_f16 v[52:55], a[244:247], v[188:191], v[52:55]
	v_mfma_f32_16x16x32_f16 v[56:59], a[248:251], v[188:191], v[56:59]
	v_mfma_f32_16x16x32_f16 v[60:63], a[252:255], v[188:191], v[60:63]
	s_sub_u32 s24, s24, 1
	s_cmp_le_u32 s24, 1
	s_cbranch_scc0 Lg1_loop
	s_nop 7
	s_nop 7
	v_and_b32_e32 v16, 0x7fffffff, v48
	v_fmaak_f32 v17, v113, v16, 0x384d0fec
	v_fmaak_f32 v17, v17, v16, 0x381f6607
	v_fmaak_f32 v17, v17, v16, 0x3b56cd72
	v_fmaak_f32 v17, v17, v16, 0x3cad2fe7
	v_fmaak_f32 v17, v17, v16, 0x3d4c41b4
	v_fmaak_f32 v17, v17, v16, 0x3f800000
	v_mul_f32_e32 v17, v17, v17
	v_mul_f32_e32 v17, v17, v17
	v_mul_f32_e32 v17, v17, v17
	v_mul_f32_e32 v17, v17, v17
	v_rcp_f32_e32 v17, v17
	v_max_f32_e32 v18, 0, v48
	v_mul_f32_e32 v16, v16, v17
	v_fmamk_f32 v96, v16, 0xbf000000, v18
	v_and_b32_e32 v19, 0x7fffffff, v49
	v_fmaak_f32 v20, v113, v19, 0x384d0fec
	v_fmaak_f32 v20, v20, v19, 0x381f6607
	v_fmaak_f32 v20, v20, v19, 0x3b56cd72
	v_fmaak_f32 v20, v20, v19, 0x3cad2fe7
	v_fmaak_f32 v20, v20, v19, 0x3d4c41b4
	v_fmaak_f32 v20, v20, v19, 0x3f800000
	v_mul_f32_e32 v20, v20, v20
	v_mul_f32_e32 v20, v20, v20
	v_mul_f32_e32 v20, v20, v20
	v_mul_f32_e32 v20, v20, v20
	v_rcp_f32_e32 v20, v20
	v_max_f32_e32 v21, 0, v49
	v_mul_f32_e32 v19, v19, v20
	v_fmamk_f32 v97, v19, 0xbf000000, v21
	v_and_b32_e32 v22, 0x7fffffff, v50
	v_fmaak_f32 v23, v113, v22, 0x384d0fec
	v_fmaak_f32 v23, v23, v22, 0x381f6607
	v_fmaak_f32 v23, v23, v22, 0x3b56cd72
	v_fmaak_f32 v23, v23, v22, 0x3cad2fe7
	v_fmaak_f32 v23, v23, v22, 0x3d4c41b4
	v_fmaak_f32 v23, v23, v22, 0x3f800000
	v_mul_f32_e32 v23, v23, v23
	v_mul_f32_e32 v23, v23, v23
	v_mul_f32_e32 v23, v23, v23
	v_mul_f32_e32 v23, v23, v23
	v_rcp_f32_e32 v23, v23
	v_max_f32_e32 v24, 0, v50
	v_mul_f32_e32 v22, v22, v23
	v_fmamk_f32 v98, v22, 0xbf000000, v24
	v_and_b32_e32 v25, 0x7fffffff, v51
	v_fmaak_f32 v26, v113, v25, 0x384d0fec
	v_fmaak_f32 v26, v26, v25, 0x381f6607
	v_fmaak_f32 v26, v26, v25, 0x3b56cd72
	v_fmaak_f32 v26, v26, v25, 0x3cad2fe7
	v_fmaak_f32 v26, v26, v25, 0x3d4c41b4
	v_fmaak_f32 v26, v26, v25, 0x3f800000
	v_mul_f32_e32 v26, v26, v26
	v_mul_f32_e32 v26, v26, v26
	v_mul_f32_e32 v26, v26, v26
	v_mul_f32_e32 v26, v26, v26
	v_rcp_f32_e32 v26, v26
	v_max_f32_e32 v27, 0, v51
	v_mul_f32_e32 v25, v25, v26
	v_fmamk_f32 v99, v25, 0xbf000000, v27
	v_and_b32_e32 v16, 0x7fffffff, v52
	v_fmaak_f32 v17, v113, v16, 0x384d0fec
	v_fmaak_f32 v17, v17, v16, 0x381f6607
	v_fmaak_f32 v17, v17, v16, 0x3b56cd72
	v_fmaak_f32 v17, v17, v16, 0x3cad2fe7
	v_fmaak_f32 v17, v17, v16, 0x3d4c41b4
	v_fmaak_f32 v17, v17, v16, 0x3f800000
	v_mul_f32_e32 v17, v17, v17
	v_mul_f32_e32 v17, v17, v17
	v_mul_f32_e32 v17, v17, v17
	v_mul_f32_e32 v17, v17, v17
	v_rcp_f32_e32 v17, v17
	v_max_f32_e32 v18, 0, v52
	v_mul_f32_e32 v16, v16, v17
	v_fmamk_f32 v100, v16, 0xbf000000, v18
	v_and_b32_e32 v19, 0x7fffffff, v53
	v_fmaak_f32 v20, v113, v19, 0x384d0fec
	v_fmaak_f32 v20, v20, v19, 0x381f6607
	v_fmaak_f32 v20, v20, v19, 0x3b56cd72
	v_fmaak_f32 v20, v20, v19, 0x3cad2fe7
	v_fmaak_f32 v20, v20, v19, 0x3d4c41b4
	v_fmaak_f32 v20, v20, v19, 0x3f800000
	v_mul_f32_e32 v20, v20, v20
	v_mul_f32_e32 v20, v20, v20
	v_mul_f32_e32 v20, v20, v20
	v_mul_f32_e32 v20, v20, v20
	v_rcp_f32_e32 v20, v20
	v_max_f32_e32 v21, 0, v53
	v_mul_f32_e32 v19, v19, v20
	v_fmamk_f32 v101, v19, 0xbf000000, v21
	v_and_b32_e32 v22, 0x7fffffff, v54
	v_fmaak_f32 v23, v113, v22, 0x384d0fec
	v_fmaak_f32 v23, v23, v22, 0x381f6607
	v_fmaak_f32 v23, v23, v22, 0x3b56cd72
	v_fmaak_f32 v23, v23, v22, 0x3cad2fe7
	v_fmaak_f32 v23, v23, v22, 0x3d4c41b4
	v_fmaak_f32 v23, v23, v22, 0x3f800000
	v_mul_f32_e32 v23, v23, v23
	v_mul_f32_e32 v23, v23, v23
	v_mul_f32_e32 v23, v23, v23
	v_mul_f32_e32 v23, v23, v23
	v_rcp_f32_e32 v23, v23
	v_max_f32_e32 v24, 0, v54
	v_mul_f32_e32 v22, v22, v23
	v_fmamk_f32 v102, v22, 0xbf000000, v24
	v_and_b32_e32 v25, 0x7fffffff, v55
	v_fmaak_f32 v26, v113, v25, 0x384d0fec
	v_fmaak_f32 v26, v26, v25, 0x381f6607
	v_fmaak_f32 v26, v26, v25, 0x3b56cd72
	v_fmaak_f32 v26, v26, v25, 0x3cad2fe7
	v_fmaak_f32 v26, v26, v25, 0x3d4c41b4
	v_fmaak_f32 v26, v26, v25, 0x3f800000
	v_mul_f32_e32 v26, v26, v26
	v_mul_f32_e32 v26, v26, v26
	v_mul_f32_e32 v26, v26, v26
	v_mul_f32_e32 v26, v26, v26
	v_rcp_f32_e32 v26, v26
	v_max_f32_e32 v27, 0, v55
	v_mul_f32_e32 v25, v25, v26
	v_fmamk_f32 v103, v25, 0xbf000000, v27
	v_and_b32_e32 v16, 0x7fffffff, v56
	v_fmaak_f32 v17, v113, v16, 0x384d0fec
	v_fmaak_f32 v17, v17, v16, 0x381f6607
	v_fmaak_f32 v17, v17, v16, 0x3b56cd72
	v_fmaak_f32 v17, v17, v16, 0x3cad2fe7
	v_fmaak_f32 v17, v17, v16, 0x3d4c41b4
	v_fmaak_f32 v17, v17, v16, 0x3f800000
	v_mul_f32_e32 v17, v17, v17
	v_mul_f32_e32 v17, v17, v17
	v_mul_f32_e32 v17, v17, v17
	v_mul_f32_e32 v17, v17, v17
	v_rcp_f32_e32 v17, v17
	v_max_f32_e32 v18, 0, v56
	v_mul_f32_e32 v16, v16, v17
	v_fmamk_f32 v104, v16, 0xbf000000, v18
	v_and_b32_e32 v19, 0x7fffffff, v57
	v_fmaak_f32 v20, v113, v19, 0x384d0fec
	v_fmaak_f32 v20, v20, v19, 0x381f6607
	v_fmaak_f32 v20, v20, v19, 0x3b56cd72
	v_fmaak_f32 v20, v20, v19, 0x3cad2fe7
	v_fmaak_f32 v20, v20, v19, 0x3d4c41b4
	v_fmaak_f32 v20, v20, v19, 0x3f800000
	v_mul_f32_e32 v20, v20, v20
	v_mul_f32_e32 v20, v20, v20
	v_mul_f32_e32 v20, v20, v20
	v_mul_f32_e32 v20, v20, v20
	v_rcp_f32_e32 v20, v20
	v_max_f32_e32 v21, 0, v57
	v_mul_f32_e32 v19, v19, v20
	v_fmamk_f32 v105, v19, 0xbf000000, v21
	v_and_b32_e32 v22, 0x7fffffff, v58
	v_fmaak_f32 v23, v113, v22, 0x384d0fec
	v_fmaak_f32 v23, v23, v22, 0x381f6607
	v_fmaak_f32 v23, v23, v22, 0x3b56cd72
	v_fmaak_f32 v23, v23, v22, 0x3cad2fe7
	v_fmaak_f32 v23, v23, v22, 0x3d4c41b4
	v_fmaak_f32 v23, v23, v22, 0x3f800000
	v_mul_f32_e32 v23, v23, v23
	v_mul_f32_e32 v23, v23, v23
	v_mul_f32_e32 v23, v23, v23
	v_mul_f32_e32 v23, v23, v23
	v_rcp_f32_e32 v23, v23
	v_max_f32_e32 v24, 0, v58
	v_mul_f32_e32 v22, v22, v23
	v_fmamk_f32 v106, v22, 0xbf000000, v24
	v_and_b32_e32 v25, 0x7fffffff, v59
	v_fmaak_f32 v26, v113, v25, 0x384d0fec
	v_fmaak_f32 v26, v26, v25, 0x381f6607
	v_fmaak_f32 v26, v26, v25, 0x3b56cd72
	v_fmaak_f32 v26, v26, v25, 0x3cad2fe7
	v_fmaak_f32 v26, v26, v25, 0x3d4c41b4
	v_fmaak_f32 v26, v26, v25, 0x3f800000
	v_mul_f32_e32 v26, v26, v26
	v_mul_f32_e32 v26, v26, v26
	v_mul_f32_e32 v26, v26, v26
	v_mul_f32_e32 v26, v26, v26
	v_rcp_f32_e32 v26, v26
	v_max_f32_e32 v27, 0, v59
	v_mul_f32_e32 v25, v25, v26
	v_fmamk_f32 v107, v25, 0xbf000000, v27
	v_and_b32_e32 v16, 0x7fffffff, v60
	v_fmaak_f32 v17, v113, v16, 0x384d0fec
	v_fmaak_f32 v17, v17, v16, 0x381f6607
	v_fmaak_f32 v17, v17, v16, 0x3b56cd72
	v_fmaak_f32 v17, v17, v16, 0x3cad2fe7
	v_fmaak_f32 v17, v17, v16, 0x3d4c41b4
	v_fmaak_f32 v17, v17, v16, 0x3f800000
	v_mul_f32_e32 v17, v17, v17
	v_mul_f32_e32 v17, v17, v17
	v_mul_f32_e32 v17, v17, v17
	v_mul_f32_e32 v17, v17, v17
	v_rcp_f32_e32 v17, v17
	v_max_f32_e32 v18, 0, v60
	v_mul_f32_e32 v16, v16, v17
	v_fmamk_f32 v108, v16, 0xbf000000, v18
	v_and_b32_e32 v19, 0x7fffffff, v61
	v_fmaak_f32 v20, v113, v19, 0x384d0fec
	v_fmaak_f32 v20, v20, v19, 0x381f6607
	v_fmaak_f32 v20, v20, v19, 0x3b56cd72
	v_fmaak_f32 v20, v20, v19, 0x3cad2fe7
	v_fmaak_f32 v20, v20, v19, 0x3d4c41b4
	v_fmaak_f32 v20, v20, v19, 0x3f800000
	v_mul_f32_e32 v20, v20, v20
	v_mul_f32_e32 v20, v20, v20
	v_mul_f32_e32 v20, v20, v20
	v_mul_f32_e32 v20, v20, v20
	v_rcp_f32_e32 v20, v20
	v_max_f32_e32 v21, 0, v61
	v_mul_f32_e32 v19, v19, v20
	v_fmamk_f32 v109, v19, 0xbf000000, v21
	v_and_b32_e32 v22, 0x7fffffff, v62
	v_fmaak_f32 v23, v113, v22, 0x384d0fec
	v_fmaak_f32 v23, v23, v22, 0x381f6607
	v_fmaak_f32 v23, v23, v22, 0x3b56cd72
	v_fmaak_f32 v23, v23, v22, 0x3cad2fe7
	v_fmaak_f32 v23, v23, v22, 0x3d4c41b4
	v_fmaak_f32 v23, v23, v22, 0x3f800000
	v_mul_f32_e32 v23, v23, v23
	v_mul_f32_e32 v23, v23, v23
	v_mul_f32_e32 v23, v23, v23
	v_mul_f32_e32 v23, v23, v23
	v_rcp_f32_e32 v23, v23
	v_max_f32_e32 v24, 0, v62
	v_mul_f32_e32 v22, v22, v23
	v_fmamk_f32 v110, v22, 0xbf000000, v24
	v_and_b32_e32 v25, 0x7fffffff, v63
	v_fmaak_f32 v26, v113, v25, 0x384d0fec
	v_fmaak_f32 v26, v26, v25, 0x381f6607
	v_fmaak_f32 v26, v26, v25, 0x3b56cd72
	v_fmaak_f32 v26, v26, v25, 0x3cad2fe7
	v_fmaak_f32 v26, v26, v25, 0x3d4c41b4
	v_fmaak_f32 v26, v26, v25, 0x3f800000
	v_mul_f32_e32 v26, v26, v26
	v_mul_f32_e32 v26, v26, v26
	v_mul_f32_e32 v26, v26, v26
	v_mul_f32_e32 v26, v26, v26
	v_rcp_f32_e32 v26, v26
	v_max_f32_e32 v27, 0, v63
	v_mul_f32_e32 v25, v25, v26
	v_fmamk_f32 v111, v25, 0xbf000000, v27
	v_cvt_pk_f16_f32 v96, v96, v97
	v_cvt_pk_f16_f32 v97, v98, v99
	v_cvt_pk_f16_f32 v98, v100, v101
	v_cvt_pk_f16_f32 v99, v102, v103
	v_cvt_pk_f16_f32 v100, v104, v105
	v_cvt_pk_f16_f32 v101, v106, v107
	v_cvt_pk_f16_f32 v102, v108, v109
	v_cvt_pk_f16_f32 v103, v110, v111
	global_store_dwordx4 v14, v[96:99], s[30:31]
	global_store_dwordx4 v14, v[100:103], s[30:31] offset:16
	s_add_u32 s30, s30, 0x800
	s_addc_u32 s31, s31, 0
	s_endpgm
Lg1_exitA:
	s_nop 7
	s_nop 7
	v_and_b32_e32 v16, 0x7fffffff, v64
	v_fmaak_f32 v17, v113, v16, 0x384d0fec
	v_fmaak_f32 v17, v17, v16, 0x381f6607
	v_fmaak_f32 v17, v17, v16, 0x3b56cd72
	v_fmaak_f32 v17, v17, v16, 0x3cad2fe7
	v_fmaak_f32 v17, v17, v16, 0x3d4c41b4
	v_fmaak_f32 v17, v17, v16, 0x3f800000
	v_mul_f32_e32 v17, v17, v17
	v_mul_f32_e32 v17, v17, v17
	v_mul_f32_e32 v17, v17, v17
	v_mul_f32_e32 v17, v17, v17
	v_rcp_f32_e32 v17, v17
	v_max_f32_e32 v18, 0, v64
	v_mul_f32_e32 v16, v16, v17
	v_fmamk_f32 v96, v16, 0xbf000000, v18
	v_and_b32_e32 v19, 0x7fffffff, v65
	v_fmaak_f32 v20, v113, v19, 0x384d0fec
	v_fmaak_f32 v20, v20, v19, 0x381f6607
	v_fmaak_f32 v20, v20, v19, 0x3b56cd72
	v_fmaak_f32 v20, v20, v19, 0x3cad2fe7
	v_fmaak_f32 v20, v20, v19, 0x3d4c41b4
	v_fmaak_f32 v20, v20, v19, 0x3f800000
	v_mul_f32_e32 v20, v20, v20
	v_mul_f32_e32 v20, v20, v20
	v_mul_f32_e32 v20, v20, v20
	v_mul_f32_e32 v20, v20, v20
	v_rcp_f32_e32 v20, v20
	v_max_f32_e32 v21, 0, v65
	v_mul_f32_e32 v19, v19, v20
	v_fmamk_f32 v97, v19, 0xbf000000, v21
	v_and_b32_e32 v22, 0x7fffffff, v66
	v_fmaak_f32 v23, v113, v22, 0x384d0fec
	v_fmaak_f32 v23, v23, v22, 0x381f6607
	v_fmaak_f32 v23, v23, v22, 0x3b56cd72
	v_fmaak_f32 v23, v23, v22, 0x3cad2fe7
	v_fmaak_f32 v23, v23, v22, 0x3d4c41b4
	v_fmaak_f32 v23, v23, v22, 0x3f800000
	v_mul_f32_e32 v23, v23, v23
	v_mul_f32_e32 v23, v23, v23
	v_mul_f32_e32 v23, v23, v23
	v_mul_f32_e32 v23, v23, v23
	v_rcp_f32_e32 v23, v23
	v_max_f32_e32 v24, 0, v66
	v_mul_f32_e32 v22, v22, v23
	v_fmamk_f32 v98, v22, 0xbf000000, v24
	v_and_b32_e32 v25, 0x7fffffff, v67
	v_fmaak_f32 v26, v113, v25, 0x384d0fec
	v_fmaak_f32 v26, v26, v25, 0x381f6607
	v_fmaak_f32 v26, v26, v25, 0x3b56cd72
	v_fmaak_f32 v26, v26, v25, 0x3cad2fe7
	v_fmaak_f32 v26, v26, v25, 0x3d4c41b4
	v_fmaak_f32 v26, v26, v25, 0x3f800000
	v_mul_f32_e32 v26, v26, v26
	v_mul_f32_e32 v26, v26, v26
	v_mul_f32_e32 v26, v26, v26
	v_mul_f32_e32 v26, v26, v26
	v_rcp_f32_e32 v26, v26
	v_max_f32_e32 v27, 0, v67
	v_mul_f32_e32 v25, v25, v26
	v_fmamk_f32 v99, v25, 0xbf000000, v27
	v_and_b32_e32 v16, 0x7fffffff, v68
	v_fmaak_f32 v17, v113, v16, 0x384d0fec
	v_fmaak_f32 v17, v17, v16, 0x381f6607
	v_fmaak_f32 v17, v17, v16, 0x3b56cd72
	v_fmaak_f32 v17, v17, v16, 0x3cad2fe7
	v_fmaak_f32 v17, v17, v16, 0x3d4c41b4
	v_fmaak_f32 v17, v17, v16, 0x3f800000
	v_mul_f32_e32 v17, v17, v17
	v_mul_f32_e32 v17, v17, v17
	v_mul_f32_e32 v17, v17, v17
	v_mul_f32_e32 v17, v17, v17
	v_rcp_f32_e32 v17, v17
	v_max_f32_e32 v18, 0, v68
	v_mul_f32_e32 v16, v16, v17
	v_fmamk_f32 v100, v16, 0xbf000000, v18
	v_and_b32_e32 v19, 0x7fffffff, v69
	v_fmaak_f32 v20, v113, v19, 0x384d0fec
	v_fmaak_f32 v20, v20, v19, 0x381f6607
	v_fmaak_f32 v20, v20, v19, 0x3b56cd72
	v_fmaak_f32 v20, v20, v19, 0x3cad2fe7
	v_fmaak_f32 v20, v20, v19, 0x3d4c41b4
	v_fmaak_f32 v20, v20, v19, 0x3f800000
	v_mul_f32_e32 v20, v20, v20
	v_mul_f32_e32 v20, v20, v20
	v_mul_f32_e32 v20, v20, v20
	v_mul_f32_e32 v20, v20, v20
	v_rcp_f32_e32 v20, v20
	v_max_f32_e32 v21, 0, v69
	v_mul_f32_e32 v19, v19, v20
	v_fmamk_f32 v101, v19, 0xbf000000, v21
	v_and_b32_e32 v22, 0x7fffffff, v70
	v_fmaak_f32 v23, v113, v22, 0x384d0fec
	v_fmaak_f32 v23, v23, v22, 0x381f6607
	v_fmaak_f32 v23, v23, v22, 0x3b56cd72
	v_fmaak_f32 v23, v23, v22, 0x3cad2fe7
	v_fmaak_f32 v23, v23, v22, 0x3d4c41b4
	v_fmaak_f32 v23, v23, v22, 0x3f800000
	v_mul_f32_e32 v23, v23, v23
	v_mul_f32_e32 v23, v23, v23
	v_mul_f32_e32 v23, v23, v23
	v_mul_f32_e32 v23, v23, v23
	v_rcp_f32_e32 v23, v23
	v_max_f32_e32 v24, 0, v70
	v_mul_f32_e32 v22, v22, v23
	v_fmamk_f32 v102, v22, 0xbf000000, v24
	v_and_b32_e32 v25, 0x7fffffff, v71
	v_fmaak_f32 v26, v113, v25, 0x384d0fec
	v_fmaak_f32 v26, v26, v25, 0x381f6607
	v_fmaak_f32 v26, v26, v25, 0x3b56cd72
	v_fmaak_f32 v26, v26, v25, 0x3cad2fe7
	v_fmaak_f32 v26, v26, v25, 0x3d4c41b4
	v_fmaak_f32 v26, v26, v25, 0x3f800000
	v_mul_f32_e32 v26, v26, v26
	v_mul_f32_e32 v26, v26, v26
	v_mul_f32_e32 v26, v26, v26
	v_mul_f32_e32 v26, v26, v26
	v_rcp_f32_e32 v26, v26
	v_max_f32_e32 v27, 0, v71
	v_mul_f32_e32 v25, v25, v26
	v_fmamk_f32 v103, v25, 0xbf000000, v27
	v_and_b32_e32 v16, 0x7fffffff, v72
	v_fmaak_f32 v17, v113, v16, 0x384d0fec
	v_fmaak_f32 v17, v17, v16, 0x381f6607
	v_fmaak_f32 v17, v17, v16, 0x3b56cd72
	v_fmaak_f32 v17, v17, v16, 0x3cad2fe7
	v_fmaak_f32 v17, v17, v16, 0x3d4c41b4
	v_fmaak_f32 v17, v17, v16, 0x3f800000
	v_mul_f32_e32 v17, v17, v17
	v_mul_f32_e32 v17, v17, v17
	v_mul_f32_e32 v17, v17, v17
	v_mul_f32_e32 v17, v17, v17
	v_rcp_f32_e32 v17, v17
	v_max_f32_e32 v18, 0, v72
	v_mul_f32_e32 v16, v16, v17
	v_fmamk_f32 v104, v16, 0xbf000000, v18
	v_and_b32_e32 v19, 0x7fffffff, v73
	v_fmaak_f32 v20, v113, v19, 0x384d0fec
	v_fmaak_f32 v20, v20, v19, 0x381f6607
	v_fmaak_f32 v20, v20, v19, 0x3b56cd72
	v_fmaak_f32 v20, v20, v19, 0x3cad2fe7
	v_fmaak_f32 v20, v20, v19, 0x3d4c41b4
	v_fmaak_f32 v20, v20, v19, 0x3f800000
	v_mul_f32_e32 v20, v20, v20
	v_mul_f32_e32 v20, v20, v20
	v_mul_f32_e32 v20, v20, v20
	v_mul_f32_e32 v20, v20, v20
	v_rcp_f32_e32 v20, v20
	v_max_f32_e32 v21, 0, v73
	v_mul_f32_e32 v19, v19, v20
	v_fmamk_f32 v105, v19, 0xbf000000, v21
	v_and_b32_e32 v22, 0x7fffffff, v74
	v_fmaak_f32 v23, v113, v22, 0x384d0fec
	v_fmaak_f32 v23, v23, v22, 0x381f6607
	v_fmaak_f32 v23, v23, v22, 0x3b56cd72
	v_fmaak_f32 v23, v23, v22, 0x3cad2fe7
	v_fmaak_f32 v23, v23, v22, 0x3d4c41b4
	v_fmaak_f32 v23, v23, v22, 0x3f800000
	v_mul_f32_e32 v23, v23, v23
	v_mul_f32_e32 v23, v23, v23
	v_mul_f32_e32 v23, v23, v23
	v_mul_f32_e32 v23, v23, v23
	v_rcp_f32_e32 v23, v23
	v_max_f32_e32 v24, 0, v74
	v_mul_f32_e32 v22, v22, v23
	v_fmamk_f32 v106, v22, 0xbf000000, v24
	v_and_b32_e32 v25, 0x7fffffff, v75
	v_fmaak_f32 v26, v113, v25, 0x384d0fec
	v_fmaak_f32 v26, v26, v25, 0x381f6607
	v_fmaak_f32 v26, v26, v25, 0x3b56cd72
	v_fmaak_f32 v26, v26, v25, 0x3cad2fe7
	v_fmaak_f32 v26, v26, v25, 0x3d4c41b4
	v_fmaak_f32 v26, v26, v25, 0x3f800000
	v_mul_f32_e32 v26, v26, v26
	v_mul_f32_e32 v26, v26, v26
	v_mul_f32_e32 v26, v26, v26
	v_mul_f32_e32 v26, v26, v26
	v_rcp_f32_e32 v26, v26
	v_max_f32_e32 v27, 0, v75
	v_mul_f32_e32 v25, v25, v26
	v_fmamk_f32 v107, v25, 0xbf000000, v27
	v_and_b32_e32 v16, 0x7fffffff, v76
	v_fmaak_f32 v17, v113, v16, 0x384d0fec
	v_fmaak_f32 v17, v17, v16, 0x381f6607
	v_fmaak_f32 v17, v17, v16, 0x3b56cd72
	v_fmaak_f32 v17, v17, v16, 0x3cad2fe7
	v_fmaak_f32 v17, v17, v16, 0x3d4c41b4
	v_fmaak_f32 v17, v17, v16, 0x3f800000
	v_mul_f32_e32 v17, v17, v17
	v_mul_f32_e32 v17, v17, v17
	v_mul_f32_e32 v17, v17, v17
	v_mul_f32_e32 v17, v17, v17
	v_rcp_f32_e32 v17, v17
	v_max_f32_e32 v18, 0, v76
	v_mul_f32_e32 v16, v16, v17
	v_fmamk_f32 v108, v16, 0xbf000000, v18
	v_and_b32_e32 v19, 0x7fffffff, v77
	v_fmaak_f32 v20, v113, v19, 0x384d0fec
	v_fmaak_f32 v20, v20, v19, 0x381f6607
	v_fmaak_f32 v20, v20, v19, 0x3b56cd72
	v_fmaak_f32 v20, v20, v19, 0x3cad2fe7
	v_fmaak_f32 v20, v20, v19, 0x3d4c41b4
	v_fmaak_f32 v20, v20, v19, 0x3f800000
	v_mul_f32_e32 v20, v20, v20
	v_mul_f32_e32 v20, v20, v20
	v_mul_f32_e32 v20, v20, v20
	v_mul_f32_e32 v20, v20, v20
	v_rcp_f32_e32 v20, v20
	v_max_f32_e32 v21, 0, v77
	v_mul_f32_e32 v19, v19, v20
	v_fmamk_f32 v109, v19, 0xbf000000, v21
	v_and_b32_e32 v22, 0x7fffffff, v78
	v_fmaak_f32 v23, v113, v22, 0x384d0fec
	v_fmaak_f32 v23, v23, v22, 0x381f6607
	v_fmaak_f32 v23, v23, v22, 0x3b56cd72
	v_fmaak_f32 v23, v23, v22, 0x3cad2fe7
	v_fmaak_f32 v23, v23, v22, 0x3d4c41b4
	v_fmaak_f32 v23, v23, v22, 0x3f800000
	v_mul_f32_e32 v23, v23, v23
	v_mul_f32_e32 v23, v23, v23
	v_mul_f32_e32 v23, v23, v23
	v_mul_f32_e32 v23, v23, v23
	v_rcp_f32_e32 v23, v23
	v_max_f32_e32 v24, 0, v78
	v_mul_f32_e32 v22, v22, v23
	v_fmamk_f32 v110, v22, 0xbf000000, v24
	v_and_b32_e32 v25, 0x7fffffff, v79
	v_fmaak_f32 v26, v113, v25, 0x384d0fec
	v_fmaak_f32 v26, v26, v25, 0x381f6607
	v_fmaak_f32 v26, v26, v25, 0x3b56cd72
	v_fmaak_f32 v26, v26, v25, 0x3cad2fe7
	v_fmaak_f32 v26, v26, v25, 0x3d4c41b4
	v_fmaak_f32 v26, v26, v25, 0x3f800000
	v_mul_f32_e32 v26, v26, v26
	v_mul_f32_e32 v26, v26, v26
	v_mul_f32_e32 v26, v26, v26
	v_mul_f32_e32 v26, v26, v26
	v_rcp_f32_e32 v26, v26
	v_max_f32_e32 v27, 0, v79
	v_mul_f32_e32 v25, v25, v26
	v_fmamk_f32 v111, v25, 0xbf000000, v27
	v_cvt_pk_f16_f32 v96, v96, v97
	v_cvt_pk_f16_f32 v97, v98, v99
	v_cvt_pk_f16_f32 v98, v100, v101
	v_cvt_pk_f16_f32 v99, v102, v103
	v_cvt_pk_f16_f32 v100, v104, v105
	v_cvt_pk_f16_f32 v101, v106, v107
	v_cvt_pk_f16_f32 v102, v108, v109
	v_cvt_pk_f16_f32 v103, v110, v111
	global_store_dwordx4 v14, v[96:99], s[30:31]
	global_store_dwordx4 v14, v[100:103], s[30:31] offset:16
	s_add_u32 s30, s30, 0x800
	s_addc_u32 s31, s31, 0
	s_endpgm
Lg1_exit:
	s_endpgm
	.p2align	8

	.amdhsa_kernel _Z6gemm_kILi1ELi2ELi2EEvPKDF16_S1_iiiPKfS1_PDF16_PfS4_
		.amdhsa_group_segment_fixed_size 81920
		.amdhsa_private_segment_fixed_size 0
		.amdhsa_kernarg_size 72
		.amdhsa_user_sgpr_count 2
		.amdhsa_user_sgpr_dispatch_ptr 0
		.amdhsa_user_sgpr_queue_ptr 0
		.amdhsa_user_sgpr_kernarg_segment_ptr 1
		.amdhsa_user_sgpr_dispatch_id 0
		.amdhsa_user_sgpr_kernarg_preload_length 0
		.amdhsa_user_sgpr_kernarg_preload_offset 0
		.amdhsa_user_sgpr_private_segment_size 0
		.amdhsa_uses_dynamic_stack 0
		.amdhsa_enable_private_segment 0
		.amdhsa_system_sgpr_workgroup_id_x 1
		.amdhsa_system_sgpr_workgroup_id_y 0
		.amdhsa_system_sgpr_workgroup_id_z 0
		.amdhsa_system_sgpr_workgroup_info 0
		.amdhsa_system_vgpr_workitem_id 0
		.amdhsa_next_free_vgpr 512
		.amdhsa_next_free_sgpr 48
		.amdhsa_accum_offset 256
		.amdhsa_reserve_vcc 1
		.amdhsa_float_round_mode_32 0
		.amdhsa_float_round_mode_16_64 0
		.amdhsa_float_denorm_mode_32 3
		.amdhsa_float_denorm_mode_16_64 3
		.amdhsa_dx10_clamp 1
		.amdhsa_ieee_mode 1
		.amdhsa_fp16_overflow 0
		.amdhsa_tg_split 0
		.amdhsa_exception_fp_ieee_invalid_op 0
		.amdhsa_exception_fp_denorm_src 0
		.amdhsa_exception_fp_ieee_div_zero 0
		.amdhsa_exception_fp_ieee_overflow 0
		.amdhsa_exception_fp_ieee_underflow 0
		.amdhsa_exception_fp_ieee_inexact 0
		.amdhsa_exception_int_div_zero 0
	.end_amdhsa_kernel

_Z6gemm_kILi2ELi3ELi2EEvPKDF16_S1_iiiPKfS1_PDF16_PfS4_:
	s_and_b32 s36, s2, 7
	s_lshr_b32 s37, s2, 3
	s_lshr_b32 s38, s37, 2
	s_lshl_b32 s36, s36, 3
	s_add_u32 s22, s36, s38
	s_and_b32 s21, s37, 3
	s_cmp_ge_u32 s22, 63
	s_cbranch_scc1 Lg2_exit
	s_load_dwordx4 s[4:7], s[0:1], 0x0
	s_load_dwordx4 s[8:11], s[0:1], 0x20
	s_load_dwordx4 s[12:15], s[0:1], 0x30
	s_load_dwordx2 s[16:17], s[0:1], 0x40
	v_lshrrev_b32_e32 v20, 6, v0
	v_and_b32_e32 v1, 63, v0
	v_readfirstlane_b32 s20, v20
	v_and_b32_e32 v2, 15, v0
	v_bfe_u32 v3, v0, 4, 2
	v_and_b32_e32 v16, 7, v2
	v_xor_b32_e32 v16, v16, v3
	v_lshlrev_b32_e32 v16, 4, v16
	v_lshl_or_b32 v4, v2, 7, v16
	v_lshrrev_b32_e32 v16, 3, v1
	v_and_b32_e32 v17, 7, v1
	v_xor_b32_e32 v17, v17, v16
	v_lshlrev_b32_e32 v17, 4, v17
	v_lshl_or_b32 v9, v16, 7, v17
	v_add_u32_e32 v10, 0x140000, v9
	v_add_u32_e32 v11, 0x280000, v9
	v_add_u32_e32 v12, 0x3c0000, v9
	s_mul_i32 s23, s22, 10
	s_sub_u32 s24, 625, s23
	s_min_u32 s24, s24, 10
	s_waitcnt lgkmcnt(0)
	s_mul_i32 s36, s20, 0x500000
	s_lshl_b32 s37, s23, 11
	s_add_u32 s36, s36, s37
	s_add_u32 s26, s4, s36
	s_addc_u32 s27, s5, 0
	s_mul_i32 s28, s20, 0x2000
	s_add_u32 s46, s28, 0x20000
	s_mov_b32 s47, s28
	s_mov_b32 s29, 0
	s_lshl_b32 s36, s21, 7
	s_lshl_b32 s37, s20, 5
	s_add_u32 s36, s36, s37
	v_lshlrev_b32_e32 v16, 3, v3
	v_add_u32_e32 v16, s36, v16
	v_lshlrev_b32_e32 v17, 2, v16
	global_load_dwordx4 v[32:35], v17, s[8:9]
	global_load_dwordx4 v[36:39], v17, s[8:9] offset:16
	v_lshlrev_b32_e32 v18, 1, v16
	v_lshl_or_b32 v14, v2, 10, v18
	s_lshl_b32 s38, s23, 14
	s_add_u32 s30, s12, s38
	s_addc_u32 s31, s13, 0
	v_lshrrev_b32_e32 v18, 6, v16
	v_mul_u32_u24_e32 v18, 0x140000, v18
	v_and_b32_e32 v19, 63, v16
	v_lshlrev_b32_e32 v19, 1, v19
	v_add_u32_e32 v18, v18, v19
	v_lshl_add_u32 v15, v2, 7, v18
	s_lshl_b32 s38, s23, 11
	s_add_u32 s32, s10, s38
	s_addc_u32 s33, s11, 0
	s_mov_b32 m0, s28
	s_add_u32 s28, s28, 0x8000
	s_cmp_ge_u32 s28, s46
	s_cselect_b32 s28, s47, s28
	global_load_lds_dwordx4 v9, s[26:27]
	global_load_lds_dwordx4 v9, s[26:27] offset:1024
	s_add_u32 m0, m0, 0x800
	s_nop 0
	global_load_lds_dwordx4 v10, s[26:27]
	global_load_lds_dwordx4 v10, s[26:27] offset:1024
	s_add_u32 m0, m0, 0x800
	s_nop 0
	global_load_lds_dwordx4 v11, s[26:27]
	global_load_lds_dwordx4 v11, s[26:27] offset:1024
	s_add_u32 m0, m0, 0x800
	s_nop 0
	global_load_lds_dwordx4 v12, s[26:27]
	global_load_lds_dwordx4 v12, s[26:27] offset:1024
	s_add_u32 s26, s26, 0x800
	s_addc_u32 s27, s27, 0
	s_mov_b32 m0, s28
	s_add_u32 s28, s28, 0x8000
	s_cmp_ge_u32 s28, s46
	s_cselect_b32 s28, s47, s28
	global_load_lds_dwordx4 v9, s[26:27]
	global_load_lds_dwordx4 v9, s[26:27] offset:1024
	s_add_u32 m0, m0, 0x800
	s_nop 0
	global_load_lds_dwordx4 v10, s[26:27]
	global_load_lds_dwordx4 v10, s[26:27] offset:1024
	s_add_u32 m0, m0, 0x800
	s_nop 0
	global_load_lds_dwordx4 v11, s[26:27]
	global_load_lds_dwordx4 v11, s[26:27] offset:1024
	s_add_u32 m0, m0, 0x800
	s_nop 0
	global_load_lds_dwordx4 v12, s[26:27]
	global_load_lds_dwordx4 v12, s[26:27] offset:1024
	s_add_u32 s26, s26, 0x800
	s_addc_u32 s27, s27, 0
	s_lshl_b32 s36, s21, 2
	s_add_u32 s36, s36, s20
	s_mul_i32 s36, s36, 0x10000
	v_lshlrev_b32_e32 v16, 4, v1
	v_add_u32_e32 v13, s36, v16
	global_load_dwordx4 a[0:3], v13, s[6:7] offset:0
	global_load_dwordx4 a[4:7], v13, s[6:7] offset:1024
	global_load_dwordx4 a[8:11], v13, s[6:7] offset:2048
	global_load_dwordx4 a[12:15], v13, s[6:7] offset:3072
	v_add_u32_e32 v13, 0x1000, v13
	global_load_dwordx4 a[16:19], v13, s[6:7] offset:0
	global_load_dwordx4 a[20:23], v13, s[6:7] offset:1024
	global_load_dwordx4 a[24:27], v13, s[6:7] offset:2048
	global_load_dwordx4 a[28:31], v13, s[6:7] offset:3072
	v_add_u32_e32 v13, 0x1000, v13
	global_load_dwordx4 a[32:35], v13, s[6:7] offset:0
	global_load_dwordx4 a[36:39], v13, s[6:7] offset:1024
	global_load_dwordx4 a[40:43], v13, s[6:7] offset:2048
	global_load_dwordx4 a[44:47], v13, s[6:7] offset:3072
	v_add_u32_e32 v13, 0x1000, v13
	global_load_dwordx4 a[48:51], v13, s[6:7] offset:0
	global_load_dwordx4 a[52:55], v13, s[6:7] offset:1024
	global_load_dwordx4 a[56:59], v13, s[6:7] offset:2048
	global_load_dwordx4 a[60:63], v13, s[6:7] offset:3072
	v_add_u32_e32 v13, 0x1000, v13
	global_load_dwordx4 a[64:67], v13, s[6:7] offset:0
	global_load_dwordx4 a[68:71], v13, s[6:7] offset:1024
	global_load_dwordx4 a[72:75], v13, s[6:7] offset:2048
	global_load_dwordx4 a[76:79], v13, s[6:7] offset:3072
	v_add_u32_e32 v13, 0x1000, v13
	global_load_dwordx4 a[80:83], v13, s[6:7] offset:0
	global_load_dwordx4 a[84:87], v13, s[6:7] offset:1024
	global_load_dwordx4 a[88:91], v13, s[6:7] offset:2048
	global_load_dwordx4 a[92:95], v13, s[6:7] offset:3072
	v_add_u32_e32 v13, 0x1000, v13
	global_load_dwordx4 a[96:99], v13, s[6:7] offset:0
	global_load_dwordx4 a[100:103], v13, s[6:7] offset:1024
	global_load_dwordx4 a[104:107], v13, s[6:7] offset:2048
	global_load_dwordx4 a[108:111], v13, s[6:7] offset:3072
	v_add_u32_e32 v13, 0x1000, v13
	global_load_dwordx4 a[112:115], v13, s[6:7] offset:0
	global_load_dwordx4 a[116:119], v13, s[6:7] offset:1024
	global_load_dwordx4 a[120:123], v13, s[6:7] offset:2048
	global_load_dwordx4 a[124:127], v13, s[6:7] offset:3072
	v_add_u32_e32 v13, 0x1000, v13
	global_load_dwordx4 a[128:131], v13, s[6:7] offset:0
	global_load_dwordx4 a[132:135], v13, s[6:7] offset:1024
	global_load_dwordx4 a[136:139], v13, s[6:7] offset:2048
	global_load_dwordx4 a[140:143], v13, s[6:7] offset:3072
	v_add_u32_e32 v13, 0x1000, v13
	global_load_dwordx4 a[144:147], v13, s[6:7] offset:0
	global_load_dwordx4 a[148:151], v13, s[6:7] offset:1024
	global_load_dwordx4 a[152:155], v13, s[6:7] offset:2048
	global_load_dwordx4 a[156:159], v13, s[6:7] offset:3072
	v_add_u32_e32 v13, 0x1000, v13
	global_load_dwordx4 a[160:163], v13, s[6:7] offset:0
	global_load_dwordx4 a[164:167], v13, s[6:7] offset:1024
	global_load_dwordx4 a[168:171], v13, s[6:7] offset:2048
	global_load_dwordx4 a[172:175], v13, s[6:7] offset:3072
	v_add_u32_e32 v13, 0x1000, v13
	global_load_dwordx4 a[176:179], v13, s[6:7] offset:0
	global_load_dwordx4 a[180:183], v13, s[6:7] offset:1024
	global_load_dwordx4 a[184:187], v13, s[6:7] offset:2048
	global_load_dwordx4 a[188:191], v13, s[6:7] offset:3072
	v_add_u32_e32 v13, 0x1000, v13
	global_load_dwordx4 a[192:195], v13, s[6:7] offset:0
	global_load_dwordx4 a[196:199], v13, s[6:7] offset:1024
	global_load_dwordx4 a[200:203], v13, s[6:7] offset:2048
	global_load_dwordx4 a[204:207], v13, s[6:7] offset:3072
	v_add_u32_e32 v13, 0x1000, v13
	global_load_dwordx4 a[208:211], v13, s[6:7] offset:0
	global_load_dwordx4 a[212:215], v13, s[6:7] offset:1024
	global_load_dwordx4 a[216:219], v13, s[6:7] offset:2048
	global_load_dwordx4 a[220:223], v13, s[6:7] offset:3072
	v_add_u32_e32 v13, 0x1000, v13
	global_load_dwordx4 a[224:227], v13, s[6:7] offset:0
	global_load_dwordx4 a[228:231], v13, s[6:7] offset:1024
	global_load_dwordx4 a[232:235], v13, s[6:7] offset:2048
	global_load_dwordx4 a[236:239], v13, s[6:7] offset:3072
	v_add_u32_e32 v13, 0x1000, v13
	global_load_dwordx4 a[240:243], v13, s[6:7] offset:0
	global_load_dwordx4 a[244:247], v13, s[6:7] offset:1024
	global_load_dwordx4 a[248:251], v13, s[6:7] offset:2048
	global_load_dwordx4 a[252:255], v13, s[6:7] offset:3072
	s_mov_b32 m0, s28
	s_add_u32 s28, s28, 0x8000
	s_cmp_ge_u32 s28, s46
	s_cselect_b32 s28, s47, s28
	global_load_lds_dwordx4 v9, s[26:27]
	global_load_lds_dwordx4 v9, s[26:27] offset:1024
	s_add_u32 m0, m0, 0x800
	s_nop 0
	global_load_lds_dwordx4 v10, s[26:27]
	global_load_lds_dwordx4 v10, s[26:27] offset:1024
	s_add_u32 m0, m0, 0x800
	s_nop 0
	global_load_lds_dwordx4 v11, s[26:27]
	global_load_lds_dwordx4 v11, s[26:27] offset:1024
	s_add_u32 m0, m0, 0x800
	s_nop 0
	global_load_lds_dwordx4 v12, s[26:27]
	global_load_lds_dwordx4 v12, s[26:27] offset:1024
	s_add_u32 s26, s26, 0x800
	s_addc_u32 s27, s27, 0
	s_waitcnt vmcnt(63)
	s_barrier
	v_add_u32_e32 v5, s29, v4
	v_xor_b32_e32 v6, 64, v5
	s_add_u32 s29, s29, 0x8000
	s_cmp_ge_u32 s29, 0x20000
	s_cselect_b32 s29, 0, s29
	ds_read_b128 v[128:131], v5 offset:0
	ds_read_b128 v[132:135], v6 offset:0
	ds_read_b128 v[136:139], v5 offset:2048
	ds_read_b128 v[140:143], v6 offset:2048
	ds_read_b128 v[144:147], v5 offset:4096
	ds_read_b128 v[148:151], v6 offset:4096
	ds_read_b128 v[152:155], v5 offset:6144
	ds_read_b128 v[156:159], v6 offset:6144
	ds_read_b128 v[160:163], v5 offset:8192
	ds_read_b128 v[164:167], v6 offset:8192
	ds_read_b128 v[168:171], v5 offset:10240
	ds_read_b128 v[172:175], v6 offset:10240
	ds_read_b128 v[176:179], v5 offset:12288
	ds_read_b128 v[180:183], v6 offset:12288
	ds_read_b128 v[184:187], v5 offset:14336
	ds_read_b128 v[188:191], v6 offset:14336
	s_waitcnt lgkmcnt(0)
	global_load_dwordx4 v[80:83], v15, s[32:33]
	s_add_u32 s32, s32, 0x800
	s_addc_u32 s33, s33, 0
	s_mov_b32 m0, s28
	s_add_u32 s28, s28, 0x8000
	s_cmp_ge_u32 s28, s46
	s_cselect_b32 s28, s47, s28
	global_load_lds_dwordx4 v9, s[26:27]
	global_load_lds_dwordx4 v9, s[26:27] offset:1024
	s_add_u32 m0, m0, 0x800
	s_nop 0
	global_load_lds_dwordx4 v10, s[26:27]
	global_load_lds_dwordx4 v10, s[26:27] offset:1024
	s_add_u32 m0, m0, 0x800
	s_nop 0
	global_load_lds_dwordx4 v11, s[26:27]
	global_load_lds_dwordx4 v11, s[26:27] offset:1024
	s_add_u32 m0, m0, 0x800
	s_nop 0
	global_load_lds_dwordx4 v12, s[26:27]
	global_load_lds_dwordx4 v12, s[26:27] offset:1024
	s_add_u32 s26, s26, 0x800
	s_addc_u32 s27, s27, 0
	v_add_u32_e32 v7, s29, v4
	v_xor_b32_e32 v8, 64, v7
	s_add_u32 s29, s29, 0x8000
	s_cmp_ge_u32 s29, 0x20000
	s_cselect_b32 s29, 0, s29
	s_waitcnt vmcnt(63)
	v_mfma_f32_16x16x32_f16 v[48:51], a[0:3], v[128:131], v[32:35]
	v_mfma_f32_16x16x32_f16 v[52:55], a[4:7], v[128:131], v[36:39]
	s_waitcnt vmcnt(63)
	v_mfma_f32_16x16x32_f16 v[48:51], a[8:11], v[132:135], v[48:51]
	ds_read_b128 v[192:195], v5 offset:16384
	v_mfma_f32_16x16x32_f16 v[52:55], a[12:15], v[132:135], v[52:55]
	ds_read_b128 v[196:199], v6 offset:16384
	s_waitcnt vmcnt(63)
	v_mfma_f32_16x16x32_f16 v[48:51], a[16:19], v[136:139], v[48:51]
	ds_read_b128 v[200:203], v5 offset:18432
	v_mfma_f32_16x16x32_f16 v[52:55], a[20:23], v[136:139], v[52:55]
	ds_read_b128 v[204:207], v6 offset:18432
	s_waitcnt vmcnt(63)
	v_mfma_f32_16x16x32_f16 v[48:51], a[24:27], v[140:143], v[48:51]
	ds_read_b128 v[208:211], v5 offset:20480
	v_mfma_f32_16x16x32_f16 v[52:55], a[28:31], v[140:143], v[52:55]
	ds_read_b128 v[212:215], v6 offset:20480
	s_waitcnt vmcnt(63)
	v_mfma_f32_16x16x32_f16 v[48:51], a[32:35], v[144:147], v[48:51]
	ds_read_b128 v[216:219], v5 offset:22528
	v_mfma_f32_16x16x32_f16 v[52:55], a[36:39], v[144:147], v[52:55]
	ds_read_b128 v[220:223], v6 offset:22528
	s_waitcnt vmcnt(63)
	v_mfma_f32_16x16x32_f16 v[48:51], a[40:43], v[148:151], v[48:51]
	ds_read_b128 v[224:227], v5 offset:24576
	v_mfma_f32_16x16x32_f16 v[52:55], a[44:47], v[148:151], v[52:55]
	ds_read_b128 v[228:231], v6 offset:24576
	s_waitcnt vmcnt(63)
	v_mfma_f32_16x16x32_f16 v[48:51], a[48:51], v[152:155], v[48:51]
	ds_read_b128 v[232:235], v5 offset:26624
	v_mfma_f32_16x16x32_f16 v[52:55], a[52:55], v[152:155], v[52:55]
	ds_read_b128 v[236:239], v6 offset:26624
	s_waitcnt vmcnt(63)
	v_mfma_f32_16x16x32_f16 v[48:51], a[56:59], v[156:159], v[48:51]
	ds_read_b128 v[240:243], v5 offset:28672
	v_mfma_f32_16x16x32_f16 v[52:55], a[60:63], v[156:159], v[52:55]
	ds_read_b128 v[244:247], v6 offset:28672
	s_waitcnt vmcnt(63)
	v_mfma_f32_16x16x32_f16 v[48:51], a[64:67], v[160:163], v[48:51]
	ds_read_b128 v[248:251], v5 offset:30720
	v_mfma_f32_16x16x32_f16 v[52:55], a[68:71], v[160:163], v[52:55]
	ds_read_b128 v[252:255], v6 offset:30720
	s_waitcnt vmcnt(61)
	v_mfma_f32_16x16x32_f16 v[48:51], a[72:75], v[164:167], v[48:51]
	v_mfma_f32_16x16x32_f16 v[52:55], a[76:79], v[164:167], v[52:55]
	s_waitcnt vmcnt(59)
	v_mfma_f32_16x16x32_f16 v[48:51], a[80:83], v[168:171], v[48:51]
	v_mfma_f32_16x16x32_f16 v[52:55], a[84:87], v[168:171], v[52:55]
	s_waitcnt vmcnt(57)
	v_mfma_f32_16x16x32_f16 v[48:51], a[88:91], v[172:175], v[48:51]
	v_mfma_f32_16x16x32_f16 v[52:55], a[92:95], v[172:175], v[52:55]
	s_waitcnt vmcnt(55)
	v_mfma_f32_16x16x32_f16 v[48:51], a[96:99], v[176:179], v[48:51]
	v_mfma_f32_16x16x32_f16 v[52:55], a[100:103], v[176:179], v[52:55]
	s_waitcnt vmcnt(53)
	v_mfma_f32_16x16x32_f16 v[48:51], a[104:107], v[180:183], v[48:51]
	v_mfma_f32_16x16x32_f16 v[52:55], a[108:111], v[180:183], v[52:55]
	s_waitcnt vmcnt(51)
	v_mfma_f32_16x16x32_f16 v[48:51], a[112:115], v[184:187], v[48:51]
	v_mfma_f32_16x16x32_f16 v[52:55], a[116:119], v[184:187], v[52:55]
	s_waitcnt vmcnt(49)
	v_mfma_f32_16x16x32_f16 v[48:51], a[120:123], v[188:191], v[48:51]
	v_mfma_f32_16x16x32_f16 v[52:55], a[124:127], v[188:191], v[52:55]
	s_waitcnt lgkmcnt(0)
	s_waitcnt vmcnt(47)
	v_mfma_f32_16x16x32_f16 v[48:51], a[128:131], v[192:195], v[48:51]
	v_mfma_f32_16x16x32_f16 v[52:55], a[132:135], v[192:195], v[52:55]
	s_waitcnt vmcnt(45)
	v_mfma_f32_16x16x32_f16 v[48:51], a[136:139], v[196:199], v[48:51]
	ds_read_b128 v[128:131], v7 offset:0
	v_mfma_f32_16x16x32_f16 v[52:55], a[140:143], v[196:199], v[52:55]
	ds_read_b128 v[132:135], v8 offset:0
	s_waitcnt vmcnt(43)
	v_mfma_f32_16x16x32_f16 v[48:51], a[144:147], v[200:203], v[48:51]
	ds_read_b128 v[136:139], v7 offset:2048
	v_mfma_f32_16x16x32_f16 v[52:55], a[148:151], v[200:203], v[52:55]
	ds_read_b128 v[140:143], v8 offset:2048
	s_waitcnt vmcnt(41)
	v_mfma_f32_16x16x32_f16 v[48:51], a[152:155], v[204:207], v[48:51]
	ds_read_b128 v[144:147], v7 offset:4096
	v_mfma_f32_16x16x32_f16 v[52:55], a[156:159], v[204:207], v[52:55]
	ds_read_b128 v[148:151], v8 offset:4096
	s_waitcnt vmcnt(39)
	v_mfma_f32_16x16x32_f16 v[48:51], a[160:163], v[208:211], v[48:51]
	ds_read_b128 v[152:155], v7 offset:6144
	v_mfma_f32_16x16x32_f16 v[52:55], a[164:167], v[208:211], v[52:55]
	ds_read_b128 v[156:159], v8 offset:6144
	s_waitcnt vmcnt(37)
	v_mfma_f32_16x16x32_f16 v[48:51], a[168:171], v[212:215], v[48:51]
	ds_read_b128 v[160:163], v7 offset:8192
	v_mfma_f32_16x16x32_f16 v[52:55], a[172:175], v[212:215], v[52:55]
	ds_read_b128 v[164:167], v8 offset:8192
	s_waitcnt vmcnt(35)
	v_mfma_f32_16x16x32_f16 v[48:51], a[176:179], v[216:219], v[48:51]
	ds_read_b128 v[168:171], v7 offset:10240
	v_mfma_f32_16x16x32_f16 v[52:55], a[180:183], v[216:219], v[52:55]
	ds_read_b128 v[172:175], v8 offset:10240
	s_waitcnt vmcnt(33)
	v_mfma_f32_16x16x32_f16 v[48:51], a[184:187], v[220:223], v[48:51]
	ds_read_b128 v[176:179], v7 offset:12288
	v_mfma_f32_16x16x32_f16 v[52:55], a[188:191], v[220:223], v[52:55]
	ds_read_b128 v[180:183], v8 offset:12288
	s_waitcnt vmcnt(31)
	v_mfma_f32_16x16x32_f16 v[48:51], a[192:195], v[224:227], v[48:51]
	ds_read_b128 v[184:187], v7 offset:14336
	v_mfma_f32_16x16x32_f16 v[52:55], a[196:199], v[224:227], v[52:55]
	ds_read_b128 v[188:191], v8 offset:14336
	s_waitcnt vmcnt(29)
	v_mfma_f32_16x16x32_f16 v[48:51], a[200:203], v[228:231], v[48:51]
	v_mfma_f32_16x16x32_f16 v[52:55], a[204:207], v[228:231], v[52:55]
	s_waitcnt vmcnt(27)
	v_mfma_f32_16x16x32_f16 v[48:51], a[208:211], v[232:235], v[48:51]
	v_mfma_f32_16x16x32_f16 v[52:55], a[212:215], v[232:235], v[52:55]
	s_waitcnt vmcnt(25)
	v_mfma_f32_16x16x32_f16 v[48:51], a[216:219], v[236:239], v[48:51]
	v_mfma_f32_16x16x32_f16 v[52:55], a[220:223], v[236:239], v[52:55]
	s_waitcnt vmcnt(23)
	v_mfma_f32_16x16x32_f16 v[48:51], a[224:227], v[240:243], v[48:51]
	v_mfma_f32_16x16x32_f16 v[52:55], a[228:231], v[240:243], v[52:55]
	s_waitcnt vmcnt(21)
	v_mfma_f32_16x16x32_f16 v[48:51], a[232:235], v[244:247], v[48:51]
	v_mfma_f32_16x16x32_f16 v[52:55], a[236:239], v[244:247], v[52:55]
	s_waitcnt vmcnt(19)
	v_mfma_f32_16x16x32_f16 v[48:51], a[240:243], v[248:251], v[48:51]
	v_mfma_f32_16x16x32_f16 v[52:55], a[244:247], v[248:251], v[52:55]
	s_waitcnt vmcnt(17)
	v_mfma_f32_16x16x32_f16 v[48:51], a[248:251], v[252:255], v[48:51]
	v_mfma_f32_16x16x32_f16 v[52:55], a[252:255], v[252:255], v[52:55]

amdhsa.kernels:
  - .agpr_count:     0
    .args:
      - .actual_access:  read_only
        .address_space:  global
        .offset:         0
        .size:           8
        .value_kind:     global_buffer
      - .actual_access:  write_only
        .address_space:  global
        .offset:         8
        .size:           8
        .value_kind:     global_buffer
      - .actual_access:  read_only
        .address_space:  global
        .offset:         16
        .size:           8
        .value_kind:     global_buffer
      - .actual_access:  read_only
        .address_space:  global
        .offset:         24
        .size:           8
        .value_kind:     global_buffer
      - .actual_access:  read_only
        .address_space:  global
        .offset:         32
        .size:           8
        .value_kind:     global_buffer
      - .actual_access:  read_only
        .address_space:  global
        .offset:         40
        .size:           8
        .value_kind:     global_buffer
      - .actual_access:  write_only
        .address_space:  global
        .offset:         48
        .size:           8
        .value_kind:     global_buffer
      - .actual_access:  read_only
        .address_space:  global
        .offset:         56
        .size:           8
        .value_kind:     global_buffer
      - .actual_access:  read_only
        .address_space:  global
        .offset:         64
        .size:           8
        .value_kind:     global_buffer
      - .actual_access:  read_only
        .address_space:  global
        .offset:         72
        .size:           8
        .value_kind:     global_buffer
      - .actual_access:  read_only
        .address_space:  global
        .offset:         80
        .size:           8
        .value_kind:     global_buffer
      - .actual_access:  read_only
        .address_space:  global
        .offset:         88
        .size:           8
        .value_kind:     global_buffer
      - .actual_access:  write_only
        .address_space:  global
        .offset:         96
        .size:           8
        .value_kind:     global_buffer
      - .actual_access:  write_only
        .address_space:  global
        .offset:         104
        .size:           8
        .value_kind:     global_buffer
      - .actual_access:  write_only
        .address_space:  global
        .offset:         112
        .size:           8
        .value_kind:     global_buffer
    .group_segment_fixed_size: 51552
    .kernarg_segment_align: 8
    .kernarg_segment_size: 120
    .language:       OpenCL C
    .language_version:
      - 2
      - 0
    .max_flat_workgroup_size: 1024
    .name:           _Z6prep_kPKfPDF16_S0_S0_S0_S0_S1_S1_S1_PKiS3_S3_PiS4_S4_
    .private_segment_fixed_size: 0
    .sgpr_count:     106
    .sgpr_spill_count: 15
    .symbol:         _Z6prep_kPKfPDF16_S0_S0_S0_S0_S1_S1_S1_PKiS3_S3_PiS4_S4_.kd
    .uniform_work_group_size: 1
    .uses_dynamic_stack: false
    .vgpr_count:     48
    .vgpr_spill_count: 0
    .wavefront_size: 64
  - .agpr_count:     0
    .args:
      - .actual_access:  read_only
        .address_space:  global
        .offset:         0
        .size:           8
        .value_kind:     global_buffer
      - .actual_access:  read_only
        .address_space:  global
        .offset:         8
        .size:           8
        .value_kind:     global_buffer
      - .actual_access:  read_only
        .address_space:  global
        .offset:         16
        .size:           8
        .value_kind:     global_buffer
      - .actual_access:  read_only
        .address_space:  global
        .offset:         24
        .size:           8
        .value_kind:     global_buffer
      - .actual_access:  read_only
        .address_space:  global
        .offset:         32
        .size:           8
        .value_kind:     global_buffer
      - .actual_access:  read_only
        .address_space:  global
        .offset:         40
        .size:           8
        .value_kind:     global_buffer
      - .actual_access:  read_only
        .address_space:  global
        .offset:         48
        .size:           8
        .value_kind:     global_buffer
      - .actual_access:  read_only
        .address_space:  global
        .offset:         56
        .size:           8
        .value_kind:     global_buffer
      - .actual_access:  read_only
        .address_space:  global
        .offset:         64
        .size:           8
        .value_kind:     global_buffer
      - .actual_access:  write_only
        .address_space:  global
        .offset:         72
        .size:           8
        .value_kind:     global_buffer
      - .actual_access:  read_only
        .address_space:  global
        .offset:         80
        .size:           8
        .value_kind:     global_buffer
      - .actual_access:  read_only
        .address_space:  global
        .offset:         88
        .size:           8
        .value_kind:     global_buffer
      - .actual_access:  write_only
        .address_space:  global
        .offset:         96
        .size:           8
        .value_kind:     global_buffer
      - .actual_access:  write_only
        .address_space:  global
        .offset:         104
        .size:           8
        .value_kind:     global_buffer
    .group_segment_fixed_size: 16640
    .kernarg_segment_align: 8
    .kernarg_segment_size: 112
    .language:       OpenCL C
    .language_version:
      - 2
      - 0
    .max_flat_workgroup_size: 256
    .name:           _Z7agg_ln1PKDF16_S0_S0_PKiS2_S2_PKfS4_S4_PDF16_S4_S4_S5_S5_
    .private_segment_fixed_size: 0
    .sgpr_count:     45
    .sgpr_spill_count: 0
    .symbol:         _Z7agg_ln1PKDF16_S0_S0_PKiS2_S2_PKfS4_S4_PDF16_S4_S4_S5_S5_.kd
    .uniform_work_group_size: 1
    .uses_dynamic_stack: false
    .vgpr_count:     64
    .vgpr_spill_count: 0
    .wavefront_size: 64
  - .agpr_count:     0
    .args:
      - .actual_access:  read_only
        .address_space:  global
        .offset:         0
        .size:           8
        .value_kind:     global_buffer
      - .actual_access:  read_only
        .address_space:  global
        .offset:         8
        .size:           8
        .value_kind:     global_buffer
      - .actual_access:  read_only
        .address_space:  global
        .offset:         16
        .size:           8
        .value_kind:     global_buffer
      - .actual_access:  write_only
        .address_space:  global
        .offset:         24
        .size:           8
        .value_kind:     global_buffer
    .group_segment_fixed_size: 0
    .kernarg_segment_align: 8
    .kernarg_segment_size: 32
    .language:       OpenCL C
    .language_version:
      - 2
      - 0
    .max_flat_workgroup_size: 256
    .name:           _Z5ln2_kPKDF16_PKfS2_Pf
    .private_segment_fixed_size: 0
    .sgpr_count:     18
    .sgpr_spill_count: 0
    .symbol:         _Z5ln2_kPKDF16_PKfS2_Pf.kd
    .uniform_work_group_size: 1
    .uses_dynamic_stack: false
    .vgpr_count:     37
    .vgpr_spill_count: 0
    .wavefront_size: 64
  - .agpr_count:     256
    .args:
      - .address_space:  global
        .offset:         0
        .size:           8
        .value_kind:     global_buffer
      - .address_space:  global
        .offset:         8
        .size:           8
        .value_kind:     global_buffer
      - .offset:         16
        .size:           4
        .value_kind:     by_value
      - .offset:         20
        .size:           4
        .value_kind:     by_value
      - .offset:         24
        .size:           4
        .value_kind:     by_value
      - .actual_access:  read_only
        .address_space:  global
        .offset:         32
        .size:           8
        .value_kind:     global_buffer
      - .actual_access:  read_only
        .address_space:  global
        .offset:         40
        .size:           8
        .value_kind:     global_buffer
      - .actual_access:  write_only
        .address_space:  global
        .offset:         48
        .size:           8
        .value_kind:     global_buffer
      - .actual_access:  read_only
        .address_space:  global
        .offset:         56
        .size:           8
        .value_kind:     global_buffer
      - .actual_access:  write_only
        .address_space:  global
        .offset:         64
        .size:           8
        .value_kind:     global_buffer
    .group_segment_fixed_size: 81920
    .kernarg_segment_align: 8
    .kernarg_segment_size: 72
    .language:       OpenCL C
    .language_version:
      - 2
      - 0
    .max_flat_workgroup_size: 256
    .name:           _Z6gemm_kILi0ELi1ELi2EEvPKDF16_S1_iiiPKfS1_PDF16_PfS4_
    .private_segment_fixed_size: 0
    .sgpr_count:     54
    .sgpr_spill_count: 0
    .symbol:         _Z6gemm_kILi0ELi1ELi2EEvPKDF16_S1_iiiPKfS1_PDF16_PfS4_.kd
    .uniform_work_group_size: 1
    .uses_dynamic_stack: false
    .vgpr_count:     512
    .vgpr_spill_count: 0
    .wavefront_size: 64
  - .agpr_count:     256
    .args:
      - .address_space:  global
        .offset:         0
        .size:           8
        .value_kind:     global_buffer
      - .address_space:  global
        .offset:         8
        .size:           8
        .value_kind:     global_buffer
      - .offset:         16
        .size:           4
        .value_kind:     by_value
      - .offset:         20
        .size:           4
        .value_kind:     by_value
      - .offset:         24
        .size:           4
        .value_kind:     by_value
      - .actual_access:  read_only
        .address_space:  global
        .offset:         32
        .size:           8
        .value_kind:     global_buffer
      - .actual_access:  read_only
        .address_space:  global
        .offset:         40
        .size:           8
        .value_kind:     global_buffer
      - .actual_access:  write_only
        .address_space:  global
        .offset:         48
        .size:           8
        .value_kind:     global_buffer
      - .actual_access:  read_only
        .address_space:  global
        .offset:         56
        .size:           8
        .value_kind:     global_buffer
      - .actual_access:  read_only
        .address_space:  global
        .offset:         64
        .size:           8
        .value_kind:     global_buffer
    .group_segment_fixed_size: 81920
    .kernarg_segment_align: 8
    .kernarg_segment_size: 72
    .language:       OpenCL C
    .language_version:
      - 2
      - 0
    .max_flat_workgroup_size: 256
    .name:           _Z6gemm_kILi1ELi2ELi2EEvPKDF16_S1_iiiPKfS1_PDF16_PfS4_
    .private_segment_fixed_size: 0
    .sgpr_count:     54
    .sgpr_spill_count: 0
    .symbol:         _Z6gemm_kILi1ELi2ELi2EEvPKDF16_S1_iiiPKfS1_PDF16_PfS4_.kd
    .uniform_work_group_size: 1
    .uses_dynamic_stack: false
    .vgpr_count:     512
    .vgpr_spill_count: 0
    .wavefront_size: 64
  - .agpr_count:     256
    .args:
      - .address_space:  global
        .offset:         0
        .size:           8
        .value_kind:     global_buffer
      - .address_space:  global
        .offset:         8
        .size:           8
        .value_kind:     global_buffer
      - .offset:         16
        .size:           4
        .value_kind:     by_value
      - .offset:         20
        .size:           4
        .value_kind:     by_value
      - .offset:         24
        .size:           4
        .value_kind:     by_value
      - .actual_access:  read_only
        .address_space:  global
        .offset:         32
        .size:           8
        .value_kind:     global_buffer
      - .actual_access:  read_only
        .address_space:  global
        .offset:         40
        .size:           8
        .value_kind:     global_buffer
      - .actual_access:  write_only
        .address_space:  global
        .offset:         48
        .size:           8
        .value_kind:     global_buffer
      - .actual_access:  read_only
        .address_space:  global
        .offset:         56
        .size:           8
        .value_kind:     global_buffer
      - .actual_access:  read_only
        .address_space:  global
        .offset:         64
        .size:           8
        .value_kind:     global_buffer
    .group_segment_fixed_size: 131072
    .kernarg_segment_align: 8
    .kernarg_segment_size: 72
    .language:       OpenCL C
    .language_version:
      - 2
      - 0
    .max_flat_workgroup_size: 256
    .name:           _Z6gemm_kILi2ELi3ELi2EEvPKDF16_S1_iiiPKfS1_PDF16_PfS4_
    .private_segment_fixed_size: 0
    .sgpr_count:     54
    .sgpr_spill_count: 0
    .symbol:         _Z6gemm_kILi2ELi3ELi2EEvPKDF16_S1_iiiPKfS1_PDF16_PfS4_.kd
    .uniform_work_group_size: 1
    .uses_dynamic_stack: false
    .vgpr_count:     512
    .vgpr_spill_count: 0
    .wavefront_size: 64
